# GEMM K-loops: priority raise issued before the pre-MFMA barrier and dropped after the post-MFMA barrier (one SALU fewer on each side of the MFMA block)
# speedup vs baseline: 1.0055x; 1.0051x over previous
.LBB0_276:
	s_or_b64 exec, exec, s[60:61]
	s_add_u32 s62, s56, 0x10000
	s_addc_u32 s63, s57, 0
	s_and_b64 s[60:61], s[34:35], exec
	s_cselect_b32 s67, s51, s63
	s_cselect_b32 s66, s50, s62
	s_add_u32 s62, s58, 0x10000
	s_addc_u32 s63, s59, 0
	s_and_b64 s[60:61], s[34:35], exec
	s_cselect_b32 s63, s53, s63
	s_cselect_b32 s62, s52, s62
	s_add_u32 s60, s66, 0x8000
	s_addc_u32 s61, s67, 0
	s_add_u32 s64, s62, 0x8000
	s_addc_u32 s65, s63, 0
	s_add_i32 s84, 0, 0x10000
	s_add_i32 s85, 0, 0x14000
	v_add_u32_e32 v132, s84, v141
	v_add_u32_e32 v133, s85, v141
	ds_read_b128 v[2:5], v132
	ds_read_b128 v[6:9], v132 offset:1024
	ds_read_b128 v[10:13], v132 offset:2048
	ds_read_b128 v[14:17], v132 offset:3072
	ds_read_b128 v[18:21], v133
	ds_read_b128 v[22:25], v133 offset:1024
	ds_read_b128 v[26:29], v133 offset:2048
	ds_read_b128 v[30:33], v133 offset:3072
	s_add_u32 s82, s56, 0xc000
	s_addc_u32 s83, s57, 0
	s_add_i32 s80, s15, 0xc000
	s_mov_b32 m0, s80
	s_add_i32 s81, s15, 0xe000
	ds_read_b128 v[34:37], v143
	ds_read_b128 v[38:41], v143 offset:1024
	ds_read_b128 v[42:45], v143 offset:2048
	ds_read_b128 v[46:49], v143 offset:3072
	ds_read_b128 v[50:53], v143 offset:4096
	ds_read_b128 v[54:57], v143 offset:5120
	ds_read_b128 v[58:61], v143 offset:6144
	ds_read_b128 v[62:65], v143 offset:7168
	s_nop 0
	global_load_lds_dwordx4 v137, s[82:83]
	s_mov_b32 m0, s81
	s_nop 0
	global_load_lds_dwordx4 v139, s[82:83]
	s_waitcnt vmcnt(8)
	s_waitcnt lgkmcnt(0)
	s_setprio 1
	s_barrier
	s_waitcnt lgkmcnt(0)
	v_mfma_f32_16x16x32_bf16 v[86:89], v[10:13], v[50:53], 0
	v_mfma_f32_16x16x32_bf16 v[90:93], v[14:17], v[54:57], v[86:89]
	v_mfma_f32_16x16x32_bf16 v[86:89], v[2:5], v[58:61], 0
	v_mfma_f32_16x16x32_bf16 v[66:69], v[2:5], v[34:37], 0
	v_mfma_f32_16x16x32_bf16 v[70:73], v[10:13], v[34:37], 0
	v_mfma_f32_16x16x32_bf16 v[74:77], v[2:5], v[42:45], 0
	v_mfma_f32_16x16x32_bf16 v[78:81], v[10:13], v[42:45], 0
	v_mfma_f32_16x16x32_bf16 v[82:85], v[2:5], v[50:53], 0
	v_mfma_f32_16x16x32_bf16 v[94:97], v[6:9], v[62:65], v[86:89]
	v_mfma_f32_16x16x32_bf16 v[86:89], v[10:13], v[58:61], 0
	v_mfma_f32_16x16x32_bf16 v[66:69], v[6:9], v[38:41], v[66:69]
	v_mfma_f32_16x16x32_bf16 v[70:73], v[14:17], v[38:41], v[70:73]
	v_mfma_f32_16x16x32_bf16 v[74:77], v[6:9], v[46:49], v[74:77]
	v_mfma_f32_16x16x32_bf16 v[78:81], v[14:17], v[46:49], v[78:81]
	v_mfma_f32_16x16x32_bf16 v[82:85], v[6:9], v[54:57], v[82:85]
	v_mfma_f32_16x16x32_bf16 v[106:109], v[14:17], v[62:65], v[86:89]
	s_setprio 0
	s_setprio 1
	v_mfma_f32_16x16x32_bf16 v[86:89], v[18:21], v[34:37], 0
	v_mfma_f32_16x16x32_bf16 v[34:37], v[26:29], v[34:37], 0
	v_mfma_f32_16x16x32_bf16 v[110:113], v[22:25], v[38:41], v[86:89]
	v_mfma_f32_16x16x32_bf16 v[34:37], v[30:33], v[38:41], v[34:37]
	v_mfma_f32_16x16x32_bf16 v[38:41], v[18:21], v[42:45], 0
	v_mfma_f32_16x16x32_bf16 v[42:45], v[26:29], v[42:45], 0
	v_mfma_f32_16x16x32_bf16 v[38:41], v[22:25], v[46:49], v[38:41]
	v_mfma_f32_16x16x32_bf16 v[42:45], v[30:33], v[46:49], v[42:45]
	v_mfma_f32_16x16x32_bf16 v[46:49], v[18:21], v[50:53], 0
	v_mfma_f32_16x16x32_bf16 v[50:53], v[26:29], v[50:53], 0
	v_mfma_f32_16x16x32_bf16 v[46:49], v[22:25], v[54:57], v[46:49]
	v_mfma_f32_16x16x32_bf16 v[50:53], v[30:33], v[54:57], v[50:53]
	v_mfma_f32_16x16x32_bf16 v[54:57], v[18:21], v[58:61], 0
	v_mfma_f32_16x16x32_bf16 v[144:147], v[22:25], v[62:65], v[54:57]
	v_mfma_f32_16x16x32_bf16 v[54:57], v[26:29], v[58:61], 0
	v_mfma_f32_16x16x32_bf16 v[58:61], v[30:33], v[62:65], v[54:57]
	s_barrier
	s_setprio 0
	s_add_i32 s82, s84, s14
	s_add_i32 s83, s82, 0x2000
	s_mov_b32 m0, s82
	s_add_u32 s86, s62, 0x4000
	s_nop 0
	ds_read_b128 v[54:57], v143 offset:16384
	ds_read_b128 v[62:65], v143 offset:17408
	ds_read_b128 v[86:89], v143 offset:18432
	ds_read_b128 v[98:101], v143 offset:19456
	ds_read_b128 v[102:105], v143 offset:20480
	ds_read_b128 v[114:117], v143 offset:21504
	ds_read_b128 v[118:121], v143 offset:22528
	ds_read_b128 v[122:125], v143 offset:23552
	s_addc_u32 s87, s63, 0
	global_load_lds_dwordx4 v138, s[62:63]
	s_mov_b32 m0, s83
	s_add_i32 s84, s85, s14
	s_add_i32 s85, s84, 0x2000
	global_load_lds_dwordx4 v140, s[62:63]
	s_mov_b32 m0, s84
	s_nop 0
	global_load_lds_dwordx4 v138, s[86:87]
	s_mov_b32 m0, s85
	s_nop 0
	global_load_lds_dwordx4 v140, s[86:87]
	s_mov_b32 m0, s15
	s_nop 0
	global_load_lds_dwordx4 v137, s[66:67]
	s_mov_b32 m0, s18
	s_nop 0
	global_load_lds_dwordx4 v139, s[66:67]
	s_waitcnt vmcnt(8)
	s_waitcnt lgkmcnt(0)
	s_setprio 1
	s_barrier
	s_waitcnt lgkmcnt(0)
	v_mfma_f32_16x16x32_bf16 v[126:129], v[2:5], v[54:57], 0
	v_mfma_f32_16x16x32_bf16 v[148:151], v[6:9], v[62:65], v[126:129]
	v_mfma_f32_16x16x32_bf16 v[126:129], v[10:13], v[54:57], 0
	v_mfma_f32_16x16x32_bf16 v[152:155], v[14:17], v[62:65], v[126:129]
	v_mfma_f32_16x16x32_bf16 v[126:129], v[2:5], v[86:89], 0
	v_mfma_f32_16x16x32_bf16 v[156:159], v[6:9], v[98:101], v[126:129]
	v_mfma_f32_16x16x32_bf16 v[126:129], v[10:13], v[86:89], 0
	v_mfma_f32_16x16x32_bf16 v[160:163], v[14:17], v[98:101], v[126:129]
	v_mfma_f32_16x16x32_bf16 v[126:129], v[2:5], v[102:105], 0
	v_mfma_f32_16x16x32_bf16 v[2:5], v[2:5], v[118:121], 0
	v_mfma_f32_16x16x32_bf16 v[164:167], v[6:9], v[114:117], v[126:129]
	v_mfma_f32_16x16x32_bf16 v[2:5], v[6:9], v[122:125], v[2:5]
	v_mfma_f32_16x16x32_bf16 v[6:9], v[10:13], v[118:121], 0
	v_mfma_f32_16x16x32_bf16 v[126:129], v[10:13], v[102:105], 0
	v_mfma_f32_16x16x32_bf16 v[10:13], v[14:17], v[122:125], v[6:9]
	v_mfma_f32_16x16x32_bf16 v[168:171], v[14:17], v[114:117], v[126:129]
	s_setprio 0
	s_setprio 1
	v_mfma_f32_16x16x32_bf16 v[6:9], v[18:21], v[54:57], 0
	v_mfma_f32_16x16x32_bf16 v[14:17], v[22:25], v[62:65], v[6:9]
	v_mfma_f32_16x16x32_bf16 v[6:9], v[26:29], v[54:57], 0
	v_mfma_f32_16x16x32_bf16 v[172:175], v[30:33], v[62:65], v[6:9]
	v_mfma_f32_16x16x32_bf16 v[6:9], v[18:21], v[86:89], 0
	v_mfma_f32_16x16x32_bf16 v[176:179], v[22:25], v[98:101], v[6:9]
	v_mfma_f32_16x16x32_bf16 v[6:9], v[26:29], v[86:89], 0
	v_mfma_f32_16x16x32_bf16 v[180:183], v[30:33], v[98:101], v[6:9]
	v_mfma_f32_16x16x32_bf16 v[6:9], v[18:21], v[102:105], 0
	v_mfma_f32_16x16x32_bf16 v[184:187], v[22:25], v[114:117], v[6:9]
	v_mfma_f32_16x16x32_bf16 v[6:9], v[26:29], v[102:105], 0
	v_mfma_f32_16x16x32_bf16 v[210:213], v[30:33], v[114:117], v[6:9]
	v_mfma_f32_16x16x32_bf16 v[6:9], v[18:21], v[118:121], 0
	v_mfma_f32_16x16x32_bf16 v[214:217], v[22:25], v[122:125], v[6:9]
	v_mfma_f32_16x16x32_bf16 v[6:9], v[26:29], v[118:121], 0
	v_mfma_f32_16x16x32_bf16 v[218:221], v[30:33], v[122:125], v[6:9]
	s_barrier
	s_setprio 0
	s_add_i32 s86, 0, 0x18000
	s_add_i32 s87, 0, 0x1c000
	v_add_u32_e32 v134, s86, v141
	v_add_u32_e32 v135, s87, v141
	s_nop 0
	ds_read_b128 v[6:9], v134
	ds_read_b128 v[26:29], v134 offset:1024
	ds_read_b128 v[30:33], v134 offset:2048
	ds_read_b128 v[222:225], v134 offset:3072
	ds_read_b128 v[236:239], v135
	ds_read_b128 v[240:243], v135 offset:1024
	ds_read_b128 v[244:247], v135 offset:2048
	ds_read_b128 v[232:235], v135 offset:3072
	s_add_u32 s66, s66, 0x4000
	s_addc_u32 s67, s67, 0
	s_mov_b32 m0, s20
	ds_read_b128 v[18:21], v143 offset:32768
	ds_read_b128 v[22:25], v143 offset:33792
	ds_read_b128 v[194:197], v143 offset:34816
	ds_read_b128 v[202:205], v143 offset:35840
	ds_read_b128 v[188:191], v143 offset:36864
	ds_read_b128 v[206:209], v143 offset:37888
	ds_read_b128 v[198:201], v143 offset:38912
	ds_read_b128 v[226:229], v143 offset:39936
	s_nop 0
	global_load_lds_dwordx4 v137, s[66:67]
	s_mov_b32 m0, s21
	s_nop 0
	global_load_lds_dwordx4 v139, s[66:67]
	s_waitcnt vmcnt(8)
	s_waitcnt lgkmcnt(0)
	s_setprio 1
	s_barrier
	s_waitcnt lgkmcnt(0)
	v_mfma_f32_16x16x32_bf16 v[54:57], v[6:9], v[18:21], v[66:69]
	v_mfma_f32_16x16x32_bf16 v[118:121], v[26:29], v[22:25], v[54:57]
	v_mfma_f32_16x16x32_bf16 v[54:57], v[30:33], v[18:21], v[70:73]
	v_mfma_f32_16x16x32_bf16 v[114:117], v[222:225], v[22:25], v[54:57]
	v_mfma_f32_16x16x32_bf16 v[54:57], v[6:9], v[194:197], v[74:77]
	v_mfma_f32_16x16x32_bf16 v[102:105], v[26:29], v[202:205], v[54:57]
	v_mfma_f32_16x16x32_bf16 v[54:57], v[30:33], v[194:197], v[78:81]
	v_mfma_f32_16x16x32_bf16 v[98:101], v[222:225], v[202:205], v[54:57]
	v_mfma_f32_16x16x32_bf16 v[54:57], v[6:9], v[188:191], v[82:85]
	v_mfma_f32_16x16x32_bf16 v[86:89], v[26:29], v[206:209], v[54:57]
	v_mfma_f32_16x16x32_bf16 v[54:57], v[30:33], v[188:191], v[90:93]
	v_mfma_f32_16x16x32_bf16 v[82:85], v[222:225], v[206:209], v[54:57]
	v_mfma_f32_16x16x32_bf16 v[54:57], v[6:9], v[198:201], v[94:97]
	v_mfma_f32_16x16x32_bf16 v[62:65], v[26:29], v[226:229], v[54:57]
	v_mfma_f32_16x16x32_bf16 v[54:57], v[30:33], v[198:201], v[106:109]
	v_mfma_f32_16x16x32_bf16 v[54:57], v[222:225], v[226:229], v[54:57]
	s_setprio 0
	s_setprio 1
	v_mfma_f32_16x16x32_bf16 v[66:69], v[236:239], v[18:21], v[110:113]
	v_mfma_f32_16x16x32_bf16 v[18:21], v[244:247], v[18:21], v[34:37]
	v_mfma_f32_16x16x32_bf16 v[122:125], v[232:235], v[22:25], v[18:21]
	v_mfma_f32_16x16x32_bf16 v[18:21], v[236:239], v[194:197], v[38:41]
	v_mfma_f32_16x16x32_bf16 v[110:113], v[240:243], v[202:205], v[18:21]
	v_mfma_f32_16x16x32_bf16 v[18:21], v[244:247], v[194:197], v[42:45]
	v_mfma_f32_16x16x32_bf16 v[106:109], v[232:235], v[202:205], v[18:21]
	v_mfma_f32_16x16x32_bf16 v[18:21], v[236:239], v[188:191], v[46:49]
	v_mfma_f32_16x16x32_bf16 v[94:97], v[240:243], v[206:209], v[18:21]
	v_mfma_f32_16x16x32_bf16 v[18:21], v[244:247], v[188:191], v[50:53]
	v_mfma_f32_16x16x32_bf16 v[90:93], v[232:235], v[206:209], v[18:21]
	v_mfma_f32_16x16x32_bf16 v[18:21], v[236:239], v[198:201], v[144:147]
	v_mfma_f32_16x16x32_bf16 v[78:81], v[240:243], v[226:229], v[18:21]
	v_mfma_f32_16x16x32_bf16 v[18:21], v[244:247], v[198:201], v[58:61]
	v_mfma_f32_16x16x32_bf16 v[126:129], v[240:243], v[22:25], v[66:69]
	v_mfma_f32_16x16x32_bf16 v[70:73], v[232:235], v[226:229], v[18:21]
	s_barrier
	s_setprio 0
	s_add_i32 s66, s86, s14
	s_add_i32 s67, s66, 0x2000
	s_mov_b32 m0, s66
	s_add_u32 s62, s62, 0xc000
	ds_read_b128 v[42:45], v143 offset:49152
	ds_read_b128 v[46:49], v143 offset:50176
	ds_read_b128 v[144:147], v143 offset:51200
	ds_read_b128 v[188:191], v143 offset:52224
	ds_read_b128 v[194:197], v143 offset:53248
	ds_read_b128 v[198:201], v143 offset:54272
	ds_read_b128 v[202:205], v143 offset:55296
	ds_read_b128 v[206:209], v143 offset:56320
	s_addc_u32 s63, s63, 0
	global_load_lds_dwordx4 v138, s[64:65]
	s_mov_b32 m0, s67
	s_add_i32 s86, s87, s14
	s_add_i32 s87, s86, 0x2000
	global_load_lds_dwordx4 v140, s[64:65]
	s_mov_b32 m0, s86
	s_nop 0
	global_load_lds_dwordx4 v138, s[62:63]
	s_mov_b32 m0, s87
	s_nop 0
	global_load_lds_dwordx4 v140, s[62:63]
	s_mov_b32 m0, s69
	s_nop 0
	global_load_lds_dwordx4 v137, s[60:61]
	s_mov_b32 m0, s70
	s_nop 0
	global_load_lds_dwordx4 v139, s[60:61]
	s_waitcnt vmcnt(8)
	s_waitcnt lgkmcnt(0)
	s_setprio 1
	s_barrier
	s_waitcnt lgkmcnt(0)
	v_mfma_f32_16x16x32_bf16 v[18:21], v[6:9], v[42:45], v[148:151]
	v_mfma_f32_16x16x32_bf16 v[58:61], v[26:29], v[46:49], v[18:21]
	v_mfma_f32_16x16x32_bf16 v[18:21], v[30:33], v[42:45], v[152:155]
	v_mfma_f32_16x16x32_bf16 v[50:53], v[222:225], v[46:49], v[18:21]
	v_mfma_f32_16x16x32_bf16 v[18:21], v[6:9], v[144:147], v[156:159]
	v_mfma_f32_16x16x32_bf16 v[38:41], v[26:29], v[188:191], v[18:21]
	v_mfma_f32_16x16x32_bf16 v[18:21], v[30:33], v[144:147], v[160:163]
	v_mfma_f32_16x16x32_bf16 v[34:37], v[222:225], v[188:191], v[18:21]
	v_mfma_f32_16x16x32_bf16 v[18:21], v[6:9], v[194:197], v[164:167]
	v_mfma_f32_16x16x32_bf16 v[2:5], v[6:9], v[202:205], v[2:5]
	v_mfma_f32_16x16x32_bf16 v[22:25], v[26:29], v[198:201], v[18:21]
	v_mfma_f32_16x16x32_bf16 v[18:21], v[30:33], v[194:197], v[168:171]
	v_mfma_f32_16x16x32_bf16 v[6:9], v[26:29], v[206:209], v[2:5]
	v_mfma_f32_16x16x32_bf16 v[2:5], v[30:33], v[202:205], v[10:13]
	v_mfma_f32_16x16x32_bf16 v[18:21], v[222:225], v[198:201], v[18:21]
	v_mfma_f32_16x16x32_bf16 v[2:5], v[222:225], v[206:209], v[2:5]
	s_setprio 0
	s_setprio 1
	v_mfma_f32_16x16x32_bf16 v[10:13], v[236:239], v[42:45], v[14:17]
	v_mfma_f32_16x16x32_bf16 v[74:77], v[240:243], v[46:49], v[10:13]
	v_mfma_f32_16x16x32_bf16 v[10:13], v[244:247], v[42:45], v[172:175]
	v_mfma_f32_16x16x32_bf16 v[66:69], v[232:235], v[46:49], v[10:13]
	v_mfma_f32_16x16x32_bf16 v[10:13], v[236:239], v[144:147], v[176:179]
	v_mfma_f32_16x16x32_bf16 v[46:49], v[240:243], v[188:191], v[10:13]
	v_mfma_f32_16x16x32_bf16 v[10:13], v[244:247], v[144:147], v[180:183]
	v_mfma_f32_16x16x32_bf16 v[42:45], v[232:235], v[188:191], v[10:13]
	v_mfma_f32_16x16x32_bf16 v[10:13], v[236:239], v[194:197], v[184:187]
	v_mfma_f32_16x16x32_bf16 v[30:33], v[240:243], v[198:201], v[10:13]
	v_mfma_f32_16x16x32_bf16 v[10:13], v[244:247], v[194:197], v[210:213]
	v_mfma_f32_16x16x32_bf16 v[26:29], v[232:235], v[198:201], v[10:13]
	v_mfma_f32_16x16x32_bf16 v[10:13], v[236:239], v[202:205], v[214:217]
	v_mfma_f32_16x16x32_bf16 v[14:17], v[240:243], v[206:209], v[10:13]
	v_mfma_f32_16x16x32_bf16 v[10:13], v[244:247], v[202:205], v[218:221]
	v_mfma_f32_16x16x32_bf16 v[10:13], v[232:235], v[206:209], v[10:13]
	s_barrier
	s_setprio 0
	s_andn2_b64 vcc, exec, s[44:45]
	s_cbranch_vccnz .LBB0_282
	s_lshl_b32 s60, s74, 10
	s_xor_b32 s88, s60, 0x400
	s_add_u32 s89, s58, 0x20000
	s_addc_u32 s90, s59, 0
	v_ashrrev_i32_e32 v131, 31, v130
	s_add_u32 s56, s56, 0x1c000
	v_lshl_add_u64 v[130:131], v[130:131], 3, s[26:27]
	s_addc_u32 s57, s57, 0
	s_mov_b32 s91, 4

.LBB0_280:
	s_or_b64 exec, exec, s[60:61]
	ds_read_b128 v[144:147], v132
	ds_read_b128 v[148:151], v132 offset:1024
	ds_read_b128 v[152:155], v132 offset:2048
	ds_read_b128 v[156:159], v132 offset:3072
	ds_read_b128 v[160:163], v133
	ds_read_b128 v[164:167], v133 offset:1024
	ds_read_b128 v[168:171], v133 offset:2048
	ds_read_b128 v[172:175], v133 offset:3072
	s_add_u32 s60, s56, 0x4000
	s_addc_u32 s61, s57, 0
	s_and_b64 s[58:59], s[58:59], exec
	s_cselect_b32 s64, s50, s60
	s_cselect_b32 s65, s51, s61
	s_cselect_b32 s61, s53, s90
	s_cselect_b32 s60, s52, s89
	s_add_u32 s58, s64, 0x8000
	s_addc_u32 s59, s65, 0
	s_add_u32 s62, s60, 0x8000
	s_addc_u32 s63, s61, 0
	s_mov_b32 m0, s80
	ds_read_b128 v[176:179], v143
	ds_read_b128 v[180:183], v143 offset:1024
	ds_read_b128 v[184:187], v143 offset:2048
	ds_read_b128 v[188:191], v143 offset:3072
	ds_read_b128 v[194:197], v143 offset:4096
	ds_read_b128 v[198:201], v143 offset:5120
	ds_read_b128 v[202:205], v143 offset:6144
	ds_read_b128 v[206:209], v143 offset:7168
	s_nop 0
	global_load_lds_dwordx4 v137, s[56:57]
	s_mov_b32 m0, s81
	s_nop 0
	global_load_lds_dwordx4 v139, s[56:57]
	s_waitcnt vmcnt(8)
	s_waitcnt lgkmcnt(0)
	s_setprio 1
	s_barrier
	s_waitcnt lgkmcnt(0)
	v_mfma_f32_16x16x32_bf16 v[118:121], v[144:147], v[176:179], v[118:121]
	v_mfma_f32_16x16x32_bf16 v[114:117], v[152:155], v[176:179], v[114:117]
	v_mfma_f32_16x16x32_bf16 v[102:105], v[144:147], v[184:187], v[102:105]
	v_mfma_f32_16x16x32_bf16 v[98:101], v[152:155], v[184:187], v[98:101]
	v_mfma_f32_16x16x32_bf16 v[86:89], v[144:147], v[194:197], v[86:89]
	v_mfma_f32_16x16x32_bf16 v[82:85], v[152:155], v[194:197], v[82:85]
	v_mfma_f32_16x16x32_bf16 v[62:65], v[144:147], v[202:205], v[62:65]
	v_mfma_f32_16x16x32_bf16 v[54:57], v[152:155], v[202:205], v[54:57]
	v_mfma_f32_16x16x32_bf16 v[118:121], v[148:151], v[180:183], v[118:121]
	v_mfma_f32_16x16x32_bf16 v[114:117], v[156:159], v[180:183], v[114:117]
	v_mfma_f32_16x16x32_bf16 v[102:105], v[148:151], v[188:191], v[102:105]
	v_mfma_f32_16x16x32_bf16 v[98:101], v[156:159], v[188:191], v[98:101]
	v_mfma_f32_16x16x32_bf16 v[86:89], v[148:151], v[198:201], v[86:89]
	v_mfma_f32_16x16x32_bf16 v[82:85], v[156:159], v[198:201], v[82:85]
	v_mfma_f32_16x16x32_bf16 v[62:65], v[148:151], v[206:209], v[62:65]
	v_mfma_f32_16x16x32_bf16 v[54:57], v[156:159], v[206:209], v[54:57]
	s_setprio 0
	s_setprio 1
	v_mfma_f32_16x16x32_bf16 v[126:129], v[160:163], v[176:179], v[126:129]
	v_mfma_f32_16x16x32_bf16 v[122:125], v[168:171], v[176:179], v[122:125]
	v_mfma_f32_16x16x32_bf16 v[110:113], v[160:163], v[184:187], v[110:113]
	v_mfma_f32_16x16x32_bf16 v[106:109], v[168:171], v[184:187], v[106:109]
	v_mfma_f32_16x16x32_bf16 v[94:97], v[160:163], v[194:197], v[94:97]
	v_mfma_f32_16x16x32_bf16 v[90:93], v[168:171], v[194:197], v[90:93]
	v_mfma_f32_16x16x32_bf16 v[78:81], v[160:163], v[202:205], v[78:81]
	v_mfma_f32_16x16x32_bf16 v[70:73], v[168:171], v[202:205], v[70:73]
	v_mfma_f32_16x16x32_bf16 v[126:129], v[164:167], v[180:183], v[126:129]
	v_mfma_f32_16x16x32_bf16 v[122:125], v[172:175], v[180:183], v[122:125]
	v_mfma_f32_16x16x32_bf16 v[110:113], v[164:167], v[188:191], v[110:113]
	v_mfma_f32_16x16x32_bf16 v[106:109], v[172:175], v[188:191], v[106:109]
	v_mfma_f32_16x16x32_bf16 v[94:97], v[164:167], v[198:201], v[94:97]
	v_mfma_f32_16x16x32_bf16 v[90:93], v[172:175], v[198:201], v[90:93]
	v_mfma_f32_16x16x32_bf16 v[78:81], v[164:167], v[206:209], v[78:81]
	v_mfma_f32_16x16x32_bf16 v[70:73], v[172:175], v[206:209], v[70:73]
	s_barrier
	s_setprio 0
	s_mov_b32 m0, s82
	ds_read_b128 v[176:179], v143 offset:16384
	ds_read_b128 v[180:183], v143 offset:17408
	ds_read_b128 v[184:187], v143 offset:18432
	ds_read_b128 v[188:191], v143 offset:19456
	ds_read_b128 v[194:197], v143 offset:20480
	ds_read_b128 v[198:201], v143 offset:21504
	ds_read_b128 v[202:205], v143 offset:22528
	ds_read_b128 v[206:209], v143 offset:23552
	s_add_u32 s92, s60, 0x4000
	global_load_lds_dwordx4 v138, s[60:61]
	s_mov_b32 m0, s83
	s_addc_u32 s93, s61, 0
	global_load_lds_dwordx4 v140, s[60:61]
	s_mov_b32 m0, s84
	s_nop 0
	global_load_lds_dwordx4 v138, s[92:93]
	s_mov_b32 m0, s85
	s_nop 0
	global_load_lds_dwordx4 v140, s[92:93]
	s_mov_b32 m0, s15
	s_nop 0
	global_load_lds_dwordx4 v137, s[64:65]
	s_mov_b32 m0, s18
	s_nop 0
	global_load_lds_dwordx4 v139, s[64:65]
	s_waitcnt vmcnt(8)
	s_waitcnt lgkmcnt(0)
	s_setprio 1
	s_barrier
	s_waitcnt lgkmcnt(0)
	v_mfma_f32_16x16x32_bf16 v[58:61], v[144:147], v[176:179], v[58:61]
	v_mfma_f32_16x16x32_bf16 v[50:53], v[152:155], v[176:179], v[50:53]
	v_mfma_f32_16x16x32_bf16 v[38:41], v[144:147], v[184:187], v[38:41]
	v_mfma_f32_16x16x32_bf16 v[34:37], v[152:155], v[184:187], v[34:37]
	v_mfma_f32_16x16x32_bf16 v[22:25], v[144:147], v[194:197], v[22:25]
	v_mfma_f32_16x16x32_bf16 v[18:21], v[152:155], v[194:197], v[18:21]
	v_mfma_f32_16x16x32_bf16 v[6:9], v[144:147], v[202:205], v[6:9]
	v_mfma_f32_16x16x32_bf16 v[2:5], v[152:155], v[202:205], v[2:5]
	v_mfma_f32_16x16x32_bf16 v[58:61], v[148:151], v[180:183], v[58:61]
	v_mfma_f32_16x16x32_bf16 v[50:53], v[156:159], v[180:183], v[50:53]
	v_mfma_f32_16x16x32_bf16 v[38:41], v[148:151], v[188:191], v[38:41]
	v_mfma_f32_16x16x32_bf16 v[34:37], v[156:159], v[188:191], v[34:37]
	v_mfma_f32_16x16x32_bf16 v[22:25], v[148:151], v[198:201], v[22:25]
	v_mfma_f32_16x16x32_bf16 v[18:21], v[156:159], v[198:201], v[18:21]
	v_mfma_f32_16x16x32_bf16 v[6:9], v[148:151], v[206:209], v[6:9]
	v_mfma_f32_16x16x32_bf16 v[2:5], v[156:159], v[206:209], v[2:5]
	s_setprio 0
	s_setprio 1
	v_mfma_f32_16x16x32_bf16 v[74:77], v[160:163], v[176:179], v[74:77]
	v_mfma_f32_16x16x32_bf16 v[66:69], v[168:171], v[176:179], v[66:69]
	v_mfma_f32_16x16x32_bf16 v[46:49], v[160:163], v[184:187], v[46:49]
	v_mfma_f32_16x16x32_bf16 v[42:45], v[168:171], v[184:187], v[42:45]
	v_mfma_f32_16x16x32_bf16 v[30:33], v[160:163], v[194:197], v[30:33]
	v_mfma_f32_16x16x32_bf16 v[26:29], v[168:171], v[194:197], v[26:29]
	v_mfma_f32_16x16x32_bf16 v[14:17], v[160:163], v[202:205], v[14:17]
	v_mfma_f32_16x16x32_bf16 v[10:13], v[168:171], v[202:205], v[10:13]
	v_mfma_f32_16x16x32_bf16 v[74:77], v[164:167], v[180:183], v[74:77]
	v_mfma_f32_16x16x32_bf16 v[66:69], v[172:175], v[180:183], v[66:69]
	v_mfma_f32_16x16x32_bf16 v[46:49], v[164:167], v[188:191], v[46:49]
	v_mfma_f32_16x16x32_bf16 v[42:45], v[172:175], v[188:191], v[42:45]
	v_mfma_f32_16x16x32_bf16 v[30:33], v[164:167], v[198:201], v[30:33]
	v_mfma_f32_16x16x32_bf16 v[26:29], v[172:175], v[198:201], v[26:29]
	v_mfma_f32_16x16x32_bf16 v[14:17], v[164:167], v[206:209], v[14:17]
	v_mfma_f32_16x16x32_bf16 v[10:13], v[172:175], v[206:209], v[10:13]
	s_barrier
	s_setprio 0
	ds_read_b128 v[144:147], v134
	ds_read_b128 v[148:151], v134 offset:1024
	ds_read_b128 v[152:155], v134 offset:2048
	ds_read_b128 v[156:159], v134 offset:3072
	ds_read_b128 v[160:163], v135
	ds_read_b128 v[164:167], v135 offset:1024
	ds_read_b128 v[168:171], v135 offset:2048
	ds_read_b128 v[172:175], v135 offset:3072
	s_add_u32 s64, s64, 0x4000
	s_addc_u32 s65, s65, 0
	s_mov_b32 m0, s20
	ds_read_b128 v[176:179], v143 offset:32768
	ds_read_b128 v[180:183], v143 offset:33792
	ds_read_b128 v[184:187], v143 offset:34816
	ds_read_b128 v[188:191], v143 offset:35840
	ds_read_b128 v[194:197], v143 offset:36864
	ds_read_b128 v[198:201], v143 offset:37888
	ds_read_b128 v[202:205], v143 offset:38912
	ds_read_b128 v[206:209], v143 offset:39936
	s_nop 0
	global_load_lds_dwordx4 v137, s[64:65]
	s_mov_b32 m0, s21
	s_nop 0
	global_load_lds_dwordx4 v139, s[64:65]
	s_waitcnt vmcnt(8)
	s_waitcnt lgkmcnt(0)
	s_setprio 1
	s_barrier
	s_waitcnt lgkmcnt(0)
	v_mfma_f32_16x16x32_bf16 v[118:121], v[144:147], v[176:179], v[118:121]
	v_mfma_f32_16x16x32_bf16 v[114:117], v[152:155], v[176:179], v[114:117]
	v_mfma_f32_16x16x32_bf16 v[102:105], v[144:147], v[184:187], v[102:105]
	v_mfma_f32_16x16x32_bf16 v[98:101], v[152:155], v[184:187], v[98:101]
	v_mfma_f32_16x16x32_bf16 v[86:89], v[144:147], v[194:197], v[86:89]
	v_mfma_f32_16x16x32_bf16 v[82:85], v[152:155], v[194:197], v[82:85]
	v_mfma_f32_16x16x32_bf16 v[62:65], v[144:147], v[202:205], v[62:65]
	v_mfma_f32_16x16x32_bf16 v[54:57], v[152:155], v[202:205], v[54:57]
	v_mfma_f32_16x16x32_bf16 v[118:121], v[148:151], v[180:183], v[118:121]
	v_mfma_f32_16x16x32_bf16 v[114:117], v[156:159], v[180:183], v[114:117]
	v_mfma_f32_16x16x32_bf16 v[102:105], v[148:151], v[188:191], v[102:105]
	v_mfma_f32_16x16x32_bf16 v[98:101], v[156:159], v[188:191], v[98:101]
	v_mfma_f32_16x16x32_bf16 v[86:89], v[148:151], v[198:201], v[86:89]
	v_mfma_f32_16x16x32_bf16 v[82:85], v[156:159], v[198:201], v[82:85]
	v_mfma_f32_16x16x32_bf16 v[62:65], v[148:151], v[206:209], v[62:65]
	v_mfma_f32_16x16x32_bf16 v[54:57], v[156:159], v[206:209], v[54:57]
	s_setprio 0
	s_setprio 1
	v_mfma_f32_16x16x32_bf16 v[126:129], v[160:163], v[176:179], v[126:129]
	v_mfma_f32_16x16x32_bf16 v[122:125], v[168:171], v[176:179], v[122:125]
	v_mfma_f32_16x16x32_bf16 v[110:113], v[160:163], v[184:187], v[110:113]
	v_mfma_f32_16x16x32_bf16 v[106:109], v[168:171], v[184:187], v[106:109]
	v_mfma_f32_16x16x32_bf16 v[94:97], v[160:163], v[194:197], v[94:97]
	v_mfma_f32_16x16x32_bf16 v[90:93], v[168:171], v[194:197], v[90:93]
	v_mfma_f32_16x16x32_bf16 v[78:81], v[160:163], v[202:205], v[78:81]
	v_mfma_f32_16x16x32_bf16 v[70:73], v[168:171], v[202:205], v[70:73]
	v_mfma_f32_16x16x32_bf16 v[126:129], v[164:167], v[180:183], v[126:129]
	v_mfma_f32_16x16x32_bf16 v[122:125], v[172:175], v[180:183], v[122:125]
	v_mfma_f32_16x16x32_bf16 v[110:113], v[164:167], v[188:191], v[110:113]
	v_mfma_f32_16x16x32_bf16 v[106:109], v[172:175], v[188:191], v[106:109]
	v_mfma_f32_16x16x32_bf16 v[94:97], v[164:167], v[198:201], v[94:97]
	v_mfma_f32_16x16x32_bf16 v[90:93], v[172:175], v[198:201], v[90:93]
	v_mfma_f32_16x16x32_bf16 v[78:81], v[164:167], v[206:209], v[78:81]
	v_mfma_f32_16x16x32_bf16 v[70:73], v[172:175], v[206:209], v[70:73]
	s_barrier
	s_setprio 0
	s_mov_b32 m0, s66
	ds_read_b128 v[176:179], v143 offset:49152
	ds_read_b128 v[180:183], v143 offset:50176
	ds_read_b128 v[184:187], v143 offset:51200
	ds_read_b128 v[188:191], v143 offset:52224
	ds_read_b128 v[194:197], v143 offset:53248
	ds_read_b128 v[198:201], v143 offset:54272
	ds_read_b128 v[202:205], v143 offset:55296
	ds_read_b128 v[206:209], v143 offset:56320
	s_add_u32 s60, s60, 0xc000
	global_load_lds_dwordx4 v138, s[62:63]
	s_mov_b32 m0, s67
	s_addc_u32 s61, s61, 0
	global_load_lds_dwordx4 v140, s[62:63]
	s_mov_b32 m0, s86
	s_nop 0
	global_load_lds_dwordx4 v138, s[60:61]
	s_mov_b32 m0, s87
	s_nop 0
	global_load_lds_dwordx4 v140, s[60:61]
	s_mov_b32 m0, s69
	s_nop 0
	global_load_lds_dwordx4 v137, s[58:59]
	s_mov_b32 m0, s70
	s_nop 0
	global_load_lds_dwordx4 v139, s[58:59]
	s_waitcnt vmcnt(8)
	s_waitcnt lgkmcnt(0)
	s_setprio 1
	s_barrier
	s_waitcnt lgkmcnt(0)
	v_mfma_f32_16x16x32_bf16 v[58:61], v[144:147], v[176:179], v[58:61]
	v_mfma_f32_16x16x32_bf16 v[50:53], v[152:155], v[176:179], v[50:53]
	v_mfma_f32_16x16x32_bf16 v[38:41], v[144:147], v[184:187], v[38:41]
	v_mfma_f32_16x16x32_bf16 v[34:37], v[152:155], v[184:187], v[34:37]
	v_mfma_f32_16x16x32_bf16 v[22:25], v[144:147], v[194:197], v[22:25]
	v_mfma_f32_16x16x32_bf16 v[18:21], v[152:155], v[194:197], v[18:21]
	v_mfma_f32_16x16x32_bf16 v[6:9], v[144:147], v[202:205], v[6:9]
	v_mfma_f32_16x16x32_bf16 v[2:5], v[152:155], v[202:205], v[2:5]
	v_mfma_f32_16x16x32_bf16 v[58:61], v[148:151], v[180:183], v[58:61]
	v_mfma_f32_16x16x32_bf16 v[50:53], v[156:159], v[180:183], v[50:53]
	v_mfma_f32_16x16x32_bf16 v[38:41], v[148:151], v[188:191], v[38:41]
	v_mfma_f32_16x16x32_bf16 v[34:37], v[156:159], v[188:191], v[34:37]
	v_mfma_f32_16x16x32_bf16 v[22:25], v[148:151], v[198:201], v[22:25]
	v_mfma_f32_16x16x32_bf16 v[18:21], v[156:159], v[198:201], v[18:21]
	v_mfma_f32_16x16x32_bf16 v[6:9], v[148:151], v[206:209], v[6:9]
	v_mfma_f32_16x16x32_bf16 v[2:5], v[156:159], v[206:209], v[2:5]
	s_setprio 0
	s_setprio 1
	v_mfma_f32_16x16x32_bf16 v[74:77], v[160:163], v[176:179], v[74:77]
	v_mfma_f32_16x16x32_bf16 v[66:69], v[168:171], v[176:179], v[66:69]
	v_mfma_f32_16x16x32_bf16 v[46:49], v[160:163], v[184:187], v[46:49]
	v_mfma_f32_16x16x32_bf16 v[42:45], v[168:171], v[184:187], v[42:45]
	v_mfma_f32_16x16x32_bf16 v[30:33], v[160:163], v[194:197], v[30:33]
	v_mfma_f32_16x16x32_bf16 v[26:29], v[168:171], v[194:197], v[26:29]
	v_mfma_f32_16x16x32_bf16 v[14:17], v[160:163], v[202:205], v[14:17]
	v_mfma_f32_16x16x32_bf16 v[10:13], v[168:171], v[202:205], v[10:13]
	v_mfma_f32_16x16x32_bf16 v[74:77], v[164:167], v[180:183], v[74:77]
	v_mfma_f32_16x16x32_bf16 v[66:69], v[172:175], v[180:183], v[66:69]
	v_mfma_f32_16x16x32_bf16 v[46:49], v[164:167], v[188:191], v[46:49]
	v_mfma_f32_16x16x32_bf16 v[42:45], v[172:175], v[188:191], v[42:45]
	v_mfma_f32_16x16x32_bf16 v[30:33], v[164:167], v[198:201], v[30:33]
	v_mfma_f32_16x16x32_bf16 v[26:29], v[172:175], v[198:201], v[26:29]
	v_mfma_f32_16x16x32_bf16 v[14:17], v[164:167], v[206:209], v[14:17]
	v_mfma_f32_16x16x32_bf16 v[10:13], v[172:175], v[206:209], v[10:13]
	s_barrier
	s_setprio 0
	s_add_i32 s58, s91, 2
	s_add_u32 s89, s89, 0x10000
	s_addc_u32 s90, s90, 0
	s_add_u32 s56, s56, 0x10000
	s_addc_u32 s57, s57, 0
	s_cmp_lt_i32 s91, s25
	s_cbranch_scc0 .LBB0_282
	s_mov_b32 s91, s58
	s_branch .LBB0_278

.LBB0_306:
	s_add_i32 s68, s50, 2
	s_add_u32 s48, s46, 0x100
	s_addc_u32 s49, s47, 0
	s_add_i32 s69, 0, 0x10000
	s_cmp_eq_u32 s60, s50
	s_cselect_b32 s51, s41, s49
	s_cselect_b32 s50, s40, s48
	v_add_u32_e32 v131, s69, v133
	s_cselect_b32 s53, s43, s67
	s_cselect_b32 s52, s42, s45
	s_add_i32 s70, 0, 0x14000
	ds_read_b128 v[138:141], v131
	ds_read_b128 v[142:145], v131 offset:1024
	ds_read_b128 v[146:149], v131 offset:2048
	ds_read_b128 v[150:153], v131 offset:3072
	v_add_u32_e32 v131, s70, v133
	ds_read_b128 v[154:157], v131
	ds_read_b128 v[158:161], v131 offset:1024
	ds_read_b128 v[162:165], v131 offset:2048
	ds_read_b128 v[166:169], v131 offset:3072
	s_add_u32 s46, s46, s61
	s_addc_u32 s47, s47, s62
	s_add_i32 m0, s15, 0xc000
	ds_read_b128 v[170:173], v136
	ds_read_b128 v[174:177], v136 offset:1024
	ds_read_b128 v[178:181], v136 offset:2048
	ds_read_b128 v[182:185], v136 offset:3072
	ds_read_b128 v[186:189], v136 offset:4096
	ds_read_b128 v[194:197], v136 offset:5120
	ds_read_b128 v[198:201], v136 offset:6144
	ds_read_b128 v[202:205], v136 offset:7168
	s_nop 0
	global_load_lds_dwordx4 v0, s[46:47]
	s_add_i32 m0, s15, 0xe000
	s_nop 0
	global_load_lds_dwordx4 v130, s[46:47]
	s_waitcnt vmcnt(8)
	s_waitcnt lgkmcnt(0)
	s_setprio 1
	s_barrier
	s_waitcnt lgkmcnt(0)
	v_mfma_f32_16x16x32_bf16 v[126:129], v[138:141], v[170:173], v[126:129]
	v_mfma_f32_16x16x32_bf16 v[118:121], v[146:149], v[170:173], v[118:121]
	v_mfma_f32_16x16x32_bf16 v[110:113], v[138:141], v[178:181], v[110:113]
	v_mfma_f32_16x16x32_bf16 v[102:105], v[146:149], v[178:181], v[102:105]
	v_mfma_f32_16x16x32_bf16 v[94:97], v[138:141], v[186:189], v[94:97]
	v_mfma_f32_16x16x32_bf16 v[86:89], v[146:149], v[186:189], v[86:89]
	v_mfma_f32_16x16x32_bf16 v[78:81], v[138:141], v[198:201], v[78:81]
	v_mfma_f32_16x16x32_bf16 v[70:73], v[146:149], v[198:201], v[70:73]
	v_mfma_f32_16x16x32_bf16 v[126:129], v[142:145], v[174:177], v[126:129]
	v_mfma_f32_16x16x32_bf16 v[118:121], v[150:153], v[174:177], v[118:121]
	v_mfma_f32_16x16x32_bf16 v[110:113], v[142:145], v[182:185], v[110:113]
	v_mfma_f32_16x16x32_bf16 v[102:105], v[150:153], v[182:185], v[102:105]
	v_mfma_f32_16x16x32_bf16 v[94:97], v[142:145], v[194:197], v[94:97]
	v_mfma_f32_16x16x32_bf16 v[86:89], v[150:153], v[194:197], v[86:89]
	v_mfma_f32_16x16x32_bf16 v[78:81], v[142:145], v[202:205], v[78:81]
	v_mfma_f32_16x16x32_bf16 v[70:73], v[150:153], v[202:205], v[70:73]
	s_setprio 0
	s_setprio 1
	v_mfma_f32_16x16x32_bf16 v[54:57], v[154:157], v[170:173], v[54:57]
	v_mfma_f32_16x16x32_bf16 v[46:49], v[162:165], v[170:173], v[46:49]
	v_mfma_f32_16x16x32_bf16 v[38:41], v[154:157], v[178:181], v[38:41]
	v_mfma_f32_16x16x32_bf16 v[30:33], v[162:165], v[178:181], v[30:33]
	v_mfma_f32_16x16x32_bf16 v[22:25], v[154:157], v[186:189], v[22:25]
	v_mfma_f32_16x16x32_bf16 v[14:17], v[162:165], v[186:189], v[14:17]
	v_mfma_f32_16x16x32_bf16 v[6:9], v[154:157], v[198:201], v[6:9]
	v_mfma_f32_16x16x32_bf16 v[2:5], v[162:165], v[198:201], v[2:5]
	v_mfma_f32_16x16x32_bf16 v[54:57], v[158:161], v[174:177], v[54:57]
	v_mfma_f32_16x16x32_bf16 v[46:49], v[166:169], v[174:177], v[46:49]
	v_mfma_f32_16x16x32_bf16 v[38:41], v[158:161], v[182:185], v[38:41]
	v_mfma_f32_16x16x32_bf16 v[30:33], v[166:169], v[182:185], v[30:33]
	v_mfma_f32_16x16x32_bf16 v[22:25], v[158:161], v[194:197], v[22:25]
	v_mfma_f32_16x16x32_bf16 v[14:17], v[166:169], v[194:197], v[14:17]
	v_mfma_f32_16x16x32_bf16 v[6:9], v[158:161], v[202:205], v[6:9]
	v_mfma_f32_16x16x32_bf16 v[2:5], v[166:169], v[202:205], v[2:5]
	s_barrier
	s_setprio 0
	s_add_i32 s46, s69, s14
	s_mov_b32 m0, s46
	ds_read_b128 v[170:173], v136 offset:16384
	ds_read_b128 v[174:177], v136 offset:17408
	ds_read_b128 v[178:181], v136 offset:18432
	ds_read_b128 v[182:185], v136 offset:19456
	ds_read_b128 v[186:189], v136 offset:20480
	ds_read_b128 v[194:197], v136 offset:21504
	ds_read_b128 v[198:201], v136 offset:22528
	ds_read_b128 v[202:205], v136 offset:23552
	s_nop 0
	global_load_lds_dwordx4 v135, s[52:53]
	s_add_i32 m0, s46, 0x2000
	s_add_u32 s46, s52, 0x4000
	s_addc_u32 s47, s53, 0
	s_add_i32 s69, s70, s14
	s_nop 0
	global_load_lds_dwordx4 v134, s[52:53]
	s_mov_b32 m0, s69
	s_nop 0
	global_load_lds_dwordx4 v135, s[46:47]
	s_add_i32 m0, s69, 0x2000
	s_nop 0
	global_load_lds_dwordx4 v134, s[46:47]
	s_mov_b32 m0, s15
	s_nop 0
	global_load_lds_dwordx4 v0, s[50:51]
	s_mov_b32 m0, s18
	s_nop 0
	global_load_lds_dwordx4 v130, s[50:51]
	s_waitcnt vmcnt(8)
	s_waitcnt lgkmcnt(0)
	s_setprio 1
	s_barrier
	s_waitcnt lgkmcnt(0)
	v_mfma_f32_16x16x32_bf16 v[122:125], v[138:141], v[170:173], v[122:125]
	v_mfma_f32_16x16x32_bf16 v[114:117], v[146:149], v[170:173], v[114:117]
	v_mfma_f32_16x16x32_bf16 v[106:109], v[138:141], v[178:181], v[106:109]
	v_mfma_f32_16x16x32_bf16 v[98:101], v[146:149], v[178:181], v[98:101]
	v_mfma_f32_16x16x32_bf16 v[90:93], v[138:141], v[186:189], v[90:93]
	v_mfma_f32_16x16x32_bf16 v[82:85], v[146:149], v[186:189], v[82:85]
	v_mfma_f32_16x16x32_bf16 v[74:77], v[138:141], v[198:201], v[74:77]
	v_mfma_f32_16x16x32_bf16 v[66:69], v[146:149], v[198:201], v[66:69]
	v_mfma_f32_16x16x32_bf16 v[122:125], v[142:145], v[174:177], v[122:125]
	v_mfma_f32_16x16x32_bf16 v[114:117], v[150:153], v[174:177], v[114:117]
	v_mfma_f32_16x16x32_bf16 v[106:109], v[142:145], v[182:185], v[106:109]
	v_mfma_f32_16x16x32_bf16 v[98:101], v[150:153], v[182:185], v[98:101]
	v_mfma_f32_16x16x32_bf16 v[90:93], v[142:145], v[194:197], v[90:93]
	v_mfma_f32_16x16x32_bf16 v[82:85], v[150:153], v[194:197], v[82:85]
	v_mfma_f32_16x16x32_bf16 v[74:77], v[142:145], v[202:205], v[74:77]
	v_mfma_f32_16x16x32_bf16 v[66:69], v[150:153], v[202:205], v[66:69]
	s_setprio 0
	s_setprio 1
	v_mfma_f32_16x16x32_bf16 v[50:53], v[154:157], v[170:173], v[50:53]
	v_mfma_f32_16x16x32_bf16 v[42:45], v[162:165], v[170:173], v[42:45]
	v_mfma_f32_16x16x32_bf16 v[34:37], v[154:157], v[178:181], v[34:37]
	v_mfma_f32_16x16x32_bf16 v[26:29], v[162:165], v[178:181], v[26:29]
	v_mfma_f32_16x16x32_bf16 v[18:21], v[154:157], v[186:189], v[18:21]
	v_mfma_f32_16x16x32_bf16 v[10:13], v[162:165], v[186:189], v[10:13]
	v_mfma_f32_16x16x32_bf16 v[58:61], v[154:157], v[198:201], v[58:61]
	v_mfma_f32_16x16x32_bf16 v[62:65], v[162:165], v[198:201], v[62:65]
	v_mfma_f32_16x16x32_bf16 v[50:53], v[158:161], v[174:177], v[50:53]
	v_mfma_f32_16x16x32_bf16 v[42:45], v[166:169], v[174:177], v[42:45]
	v_mfma_f32_16x16x32_bf16 v[34:37], v[158:161], v[182:185], v[34:37]
	v_mfma_f32_16x16x32_bf16 v[26:29], v[166:169], v[182:185], v[26:29]
	v_mfma_f32_16x16x32_bf16 v[18:21], v[158:161], v[194:197], v[18:21]
	v_mfma_f32_16x16x32_bf16 v[10:13], v[166:169], v[194:197], v[10:13]
	v_mfma_f32_16x16x32_bf16 v[58:61], v[158:161], v[202:205], v[58:61]
	v_mfma_f32_16x16x32_bf16 v[62:65], v[166:169], v[202:205], v[62:65]
	s_barrier
	s_setprio 0
	s_add_i32 s69, 0, 0x18000
	v_add_u32_e32 v131, s69, v133
	s_add_i32 s70, 0, 0x1c000
	ds_read_b128 v[138:141], v131
	ds_read_b128 v[142:145], v131 offset:1024
	ds_read_b128 v[146:149], v131 offset:2048
	ds_read_b128 v[150:153], v131 offset:3072
	v_add_u32_e32 v131, s70, v133
	ds_read_b128 v[154:157], v131
	ds_read_b128 v[158:161], v131 offset:1024
	ds_read_b128 v[162:165], v131 offset:2048
	ds_read_b128 v[166:169], v131 offset:3072
	s_add_u32 s46, s50, s26
	s_addc_u32 s47, s51, s27
	s_mov_b32 m0, s20
	ds_read_b128 v[170:173], v136 offset:32768
	ds_read_b128 v[174:177], v136 offset:33792
	ds_read_b128 v[178:181], v136 offset:34816
	ds_read_b128 v[182:185], v136 offset:35840
	ds_read_b128 v[186:189], v136 offset:36864
	ds_read_b128 v[194:197], v136 offset:37888
	ds_read_b128 v[198:201], v136 offset:38912
	ds_read_b128 v[202:205], v136 offset:39936
	s_nop 0
	global_load_lds_dwordx4 v0, s[46:47]
	s_mov_b32 m0, s21
	s_nop 0
	global_load_lds_dwordx4 v130, s[46:47]
	s_waitcnt vmcnt(8)
	s_waitcnt lgkmcnt(0)
	s_setprio 1
	s_barrier
	s_waitcnt lgkmcnt(0)
	v_mfma_f32_16x16x32_bf16 v[126:129], v[138:141], v[170:173], v[126:129]
	v_mfma_f32_16x16x32_bf16 v[118:121], v[146:149], v[170:173], v[118:121]
	v_mfma_f32_16x16x32_bf16 v[110:113], v[138:141], v[178:181], v[110:113]
	v_mfma_f32_16x16x32_bf16 v[102:105], v[146:149], v[178:181], v[102:105]
	v_mfma_f32_16x16x32_bf16 v[94:97], v[138:141], v[186:189], v[94:97]
	v_mfma_f32_16x16x32_bf16 v[86:89], v[146:149], v[186:189], v[86:89]
	v_mfma_f32_16x16x32_bf16 v[78:81], v[138:141], v[198:201], v[78:81]
	v_mfma_f32_16x16x32_bf16 v[70:73], v[146:149], v[198:201], v[70:73]
	v_mfma_f32_16x16x32_bf16 v[126:129], v[142:145], v[174:177], v[126:129]
	v_mfma_f32_16x16x32_bf16 v[118:121], v[150:153], v[174:177], v[118:121]
	v_mfma_f32_16x16x32_bf16 v[110:113], v[142:145], v[182:185], v[110:113]
	v_mfma_f32_16x16x32_bf16 v[102:105], v[150:153], v[182:185], v[102:105]
	v_mfma_f32_16x16x32_bf16 v[94:97], v[142:145], v[194:197], v[94:97]
	v_mfma_f32_16x16x32_bf16 v[86:89], v[150:153], v[194:197], v[86:89]
	v_mfma_f32_16x16x32_bf16 v[78:81], v[142:145], v[202:205], v[78:81]
	v_mfma_f32_16x16x32_bf16 v[70:73], v[150:153], v[202:205], v[70:73]
	s_setprio 0
	s_setprio 1
	v_mfma_f32_16x16x32_bf16 v[54:57], v[154:157], v[170:173], v[54:57]
	v_mfma_f32_16x16x32_bf16 v[46:49], v[162:165], v[170:173], v[46:49]
	v_mfma_f32_16x16x32_bf16 v[38:41], v[154:157], v[178:181], v[38:41]
	v_mfma_f32_16x16x32_bf16 v[30:33], v[162:165], v[178:181], v[30:33]
	v_mfma_f32_16x16x32_bf16 v[22:25], v[154:157], v[186:189], v[22:25]
	v_mfma_f32_16x16x32_bf16 v[14:17], v[162:165], v[186:189], v[14:17]
	v_mfma_f32_16x16x32_bf16 v[6:9], v[154:157], v[198:201], v[6:9]
	v_mfma_f32_16x16x32_bf16 v[2:5], v[162:165], v[198:201], v[2:5]
	v_mfma_f32_16x16x32_bf16 v[54:57], v[158:161], v[174:177], v[54:57]
	v_mfma_f32_16x16x32_bf16 v[46:49], v[166:169], v[174:177], v[46:49]
	v_mfma_f32_16x16x32_bf16 v[38:41], v[158:161], v[182:185], v[38:41]
	v_mfma_f32_16x16x32_bf16 v[30:33], v[166:169], v[182:185], v[30:33]
	v_mfma_f32_16x16x32_bf16 v[22:25], v[158:161], v[194:197], v[22:25]
	v_mfma_f32_16x16x32_bf16 v[14:17], v[166:169], v[194:197], v[14:17]
	v_mfma_f32_16x16x32_bf16 v[6:9], v[158:161], v[202:205], v[6:9]
	v_mfma_f32_16x16x32_bf16 v[2:5], v[166:169], v[202:205], v[2:5]
	s_barrier
	s_setprio 0
	s_add_u32 s46, s52, 0x8000
	s_addc_u32 s47, s53, 0
	s_add_i32 s69, s69, s14
	s_mov_b32 m0, s69
	ds_read_b128 v[170:173], v136 offset:49152
	ds_read_b128 v[174:177], v136 offset:50176
	ds_read_b128 v[178:181], v136 offset:51200
	ds_read_b128 v[182:185], v136 offset:52224
	ds_read_b128 v[186:189], v136 offset:53248
	ds_read_b128 v[194:197], v136 offset:54272
	ds_read_b128 v[198:201], v136 offset:55296
	ds_read_b128 v[202:205], v136 offset:56320
	v_mov_b32_e32 v131, v1
	global_load_lds_dwordx4 v135, s[46:47]
	s_add_i32 m0, s69, 0x2000
	s_nop 0
	global_load_lds_dwordx4 v134, s[46:47]
	s_add_u32 s46, s52, 0xc000
	s_addc_u32 s47, s53, 0
	s_add_i32 s52, s70, s14
	s_mov_b32 m0, s52
	s_nop 0
	global_load_lds_dwordx4 v135, s[46:47]
	s_add_i32 m0, s52, 0x2000
	s_nop 0
	global_load_lds_dwordx4 v134, s[46:47]
	s_mov_b32 m0, s58
	v_lshl_add_u64 v[190:191], s[50:51], 0, v[0:1]
	v_lshl_add_u64 v[190:191], v[190:191], 0, s[16:17]
	global_load_lds_dwordx4 v[190:191], off
	s_mov_b32 m0, s59
	v_lshl_add_u64 v[190:191], s[50:51], 0, v[130:131]
	v_lshl_add_u64 v[190:191], v[190:191], 0, s[16:17]
	global_load_lds_dwordx4 v[190:191], off
	s_waitcnt vmcnt(8)
	s_waitcnt lgkmcnt(0)
	s_setprio 1
	s_barrier
	s_waitcnt lgkmcnt(0)
	v_mfma_f32_16x16x32_bf16 v[122:125], v[138:141], v[170:173], v[122:125]
	v_mfma_f32_16x16x32_bf16 v[114:117], v[146:149], v[170:173], v[114:117]
	v_mfma_f32_16x16x32_bf16 v[106:109], v[138:141], v[178:181], v[106:109]
	v_mfma_f32_16x16x32_bf16 v[98:101], v[146:149], v[178:181], v[98:101]
	v_mfma_f32_16x16x32_bf16 v[90:93], v[138:141], v[186:189], v[90:93]
	v_mfma_f32_16x16x32_bf16 v[82:85], v[146:149], v[186:189], v[82:85]
	v_mfma_f32_16x16x32_bf16 v[74:77], v[138:141], v[198:201], v[74:77]
	v_mfma_f32_16x16x32_bf16 v[66:69], v[146:149], v[198:201], v[66:69]
	v_mfma_f32_16x16x32_bf16 v[122:125], v[142:145], v[174:177], v[122:125]
	v_mfma_f32_16x16x32_bf16 v[114:117], v[150:153], v[174:177], v[114:117]
	v_mfma_f32_16x16x32_bf16 v[106:109], v[142:145], v[182:185], v[106:109]
	v_mfma_f32_16x16x32_bf16 v[98:101], v[150:153], v[182:185], v[98:101]
	v_mfma_f32_16x16x32_bf16 v[90:93], v[142:145], v[194:197], v[90:93]
	v_mfma_f32_16x16x32_bf16 v[82:85], v[150:153], v[194:197], v[82:85]
	v_mfma_f32_16x16x32_bf16 v[74:77], v[142:145], v[202:205], v[74:77]
	v_mfma_f32_16x16x32_bf16 v[66:69], v[150:153], v[202:205], v[66:69]
	s_setprio 0
	s_setprio 1
	v_mfma_f32_16x16x32_bf16 v[50:53], v[154:157], v[170:173], v[50:53]
	v_mfma_f32_16x16x32_bf16 v[42:45], v[162:165], v[170:173], v[42:45]
	v_mfma_f32_16x16x32_bf16 v[34:37], v[154:157], v[178:181], v[34:37]
	v_mfma_f32_16x16x32_bf16 v[26:29], v[162:165], v[178:181], v[26:29]
	v_mfma_f32_16x16x32_bf16 v[18:21], v[154:157], v[186:189], v[18:21]
	v_mfma_f32_16x16x32_bf16 v[10:13], v[162:165], v[186:189], v[10:13]
	v_mfma_f32_16x16x32_bf16 v[58:61], v[154:157], v[198:201], v[58:61]
	v_mfma_f32_16x16x32_bf16 v[62:65], v[162:165], v[198:201], v[62:65]
	v_mfma_f32_16x16x32_bf16 v[50:53], v[158:161], v[174:177], v[50:53]
	v_mfma_f32_16x16x32_bf16 v[42:45], v[166:169], v[174:177], v[42:45]
	v_mfma_f32_16x16x32_bf16 v[34:37], v[158:161], v[182:185], v[34:37]
	v_mfma_f32_16x16x32_bf16 v[26:29], v[166:169], v[182:185], v[26:29]
	v_mfma_f32_16x16x32_bf16 v[18:21], v[158:161], v[194:197], v[18:21]
	v_mfma_f32_16x16x32_bf16 v[10:13], v[166:169], v[194:197], v[10:13]
	v_mfma_f32_16x16x32_bf16 v[58:61], v[158:161], v[202:205], v[58:61]
	v_mfma_f32_16x16x32_bf16 v[62:65], v[166:169], v[202:205], v[62:65]
	s_barrier
	s_setprio 0
	s_add_u32 s45, s45, 0x10000
	s_addc_u32 s67, s67, 0
	s_cmp_ge_i32 s68, s55
	s_mov_b64 s[46:47], s[48:49]
	s_mov_b32 s50, s68
	s_cbranch_scc0 .LBB0_306

.LBB0_379:
	s_add_u32 s34, s26, 0x10000
	s_addc_u32 s35, s27, 0
	s_and_b64 s[30:31], s[46:47], exec
	s_cselect_b32 s53, s43, s35
	s_cselect_b32 s52, s42, s34
	s_add_u32 s65, s28, 0x10000
	s_addc_u32 s66, s29, 0
	s_add_u32 s30, s52, 0x8000
	s_addc_u32 s31, s53, 0
	s_add_i32 s67, 0, 0x10000
	s_and_b64 s[34:35], s[46:47], exec
	s_cselect_b32 s35, s45, s66
	s_cselect_b32 s34, s44, s65
	s_add_i32 s70, 0, 0x14000
	v_add_u32_e32 v114, s67, v236
	v_add_u32_e32 v115, s70, v236
	ds_read_b128 v[2:5], v114
	s_waitcnt lgkmcnt(0)
	ds_read_b128 v[6:9], v114 offset:1024
	ds_read_b128 v[10:13], v114 offset:2048
	ds_read_b128 v[14:17], v114 offset:3072
	ds_read_b128 v[18:21], v115
	ds_read_b128 v[22:25], v115 offset:1024
	ds_read_b128 v[26:29], v115 offset:2048
	ds_read_b128 v[30:33], v115 offset:3072
	s_add_u32 s68, s26, 0xc000
	s_addc_u32 s69, s27, 0
	s_add_i32 s65, s20, 0xc000
	s_mov_b32 m0, s65
	s_add_i32 s66, s20, 0xe000
	ds_read_b128 v[34:37], v237
	ds_read_b128 v[38:41], v237 offset:1024
	ds_read_b128 v[42:45], v237 offset:2048
	ds_read_b128 v[46:49], v237 offset:3072
	ds_read_b128 v[50:53], v237 offset:4096
	ds_read_b128 v[54:57], v237 offset:5120
	ds_read_b128 v[58:61], v237 offset:6144
	ds_read_b128 v[62:65], v237 offset:7168
	s_nop 0
	global_load_lds_dwordx4 v235, s[68:69]
	s_mov_b32 m0, s66
	s_nop 0
	global_load_lds_dwordx4 v226, s[68:69]
	s_waitcnt vmcnt(8)
	s_waitcnt lgkmcnt(0)
	s_setprio 1
	s_barrier
	s_waitcnt lgkmcnt(0)
	v_mfma_f32_16x16x32_bf16 v[90:93], v[2:5], v[58:61], 0
	v_mfma_f32_16x16x32_bf16 v[66:69], v[2:5], v[34:37], 0
	v_mfma_f32_16x16x32_bf16 v[70:73], v[10:13], v[34:37], 0
	v_mfma_f32_16x16x32_bf16 v[74:77], v[2:5], v[42:45], 0
	v_mfma_f32_16x16x32_bf16 v[78:81], v[10:13], v[42:45], 0
	v_mfma_f32_16x16x32_bf16 v[82:85], v[2:5], v[50:53], 0
	v_mfma_f32_16x16x32_bf16 v[86:89], v[10:13], v[50:53], 0
	v_mfma_f32_16x16x32_bf16 v[98:101], v[6:9], v[62:65], v[90:93]
	v_mfma_f32_16x16x32_bf16 v[90:93], v[10:13], v[58:61], 0
	v_mfma_f32_16x16x32_bf16 v[66:69], v[6:9], v[38:41], v[66:69]
	v_mfma_f32_16x16x32_bf16 v[70:73], v[14:17], v[38:41], v[70:73]
	v_mfma_f32_16x16x32_bf16 v[74:77], v[6:9], v[46:49], v[74:77]
	v_mfma_f32_16x16x32_bf16 v[78:81], v[14:17], v[46:49], v[78:81]
	v_mfma_f32_16x16x32_bf16 v[82:85], v[6:9], v[54:57], v[82:85]
	v_mfma_f32_16x16x32_bf16 v[86:89], v[14:17], v[54:57], v[86:89]
	v_mfma_f32_16x16x32_bf16 v[102:105], v[14:17], v[62:65], v[90:93]
	s_setprio 0
	s_setprio 1
	v_mfma_f32_16x16x32_bf16 v[90:93], v[18:21], v[34:37], 0
	v_mfma_f32_16x16x32_bf16 v[34:37], v[26:29], v[34:37], 0
	v_mfma_f32_16x16x32_bf16 v[118:121], v[22:25], v[38:41], v[90:93]
	v_mfma_f32_16x16x32_bf16 v[34:37], v[30:33], v[38:41], v[34:37]
	v_mfma_f32_16x16x32_bf16 v[38:41], v[18:21], v[42:45], 0
	v_mfma_f32_16x16x32_bf16 v[42:45], v[26:29], v[42:45], 0
	v_mfma_f32_16x16x32_bf16 v[38:41], v[22:25], v[46:49], v[38:41]
	v_mfma_f32_16x16x32_bf16 v[42:45], v[30:33], v[46:49], v[42:45]
	v_mfma_f32_16x16x32_bf16 v[46:49], v[18:21], v[50:53], 0
	v_mfma_f32_16x16x32_bf16 v[50:53], v[26:29], v[50:53], 0
	v_mfma_f32_16x16x32_bf16 v[46:49], v[22:25], v[54:57], v[46:49]
	v_mfma_f32_16x16x32_bf16 v[50:53], v[30:33], v[54:57], v[50:53]
	v_mfma_f32_16x16x32_bf16 v[54:57], v[18:21], v[58:61], 0
	v_mfma_f32_16x16x32_bf16 v[58:61], v[26:29], v[58:61], 0
	v_mfma_f32_16x16x32_bf16 v[54:57], v[22:25], v[62:65], v[54:57]
	v_mfma_f32_16x16x32_bf16 v[58:61], v[30:33], v[62:65], v[58:61]
	s_barrier
	s_setprio 0
	s_add_i32 s67, s67, s18
	s_add_i32 s68, s67, 0x2000
	s_mov_b32 m0, s67
	s_add_u32 s72, s34, 0x4000
	ds_read_b128 v[62:65], v237 offset:16384
	ds_read_b128 v[90:93], v237 offset:17408
	ds_read_b128 v[94:97], v237 offset:18432
	ds_read_b128 v[106:109], v237 offset:19456
	ds_read_b128 v[110:113], v237 offset:20480
	ds_read_b128 v[122:125], v237 offset:21504
	ds_read_b128 v[126:129], v237 offset:22528
	ds_read_b128 v[130:133], v237 offset:23552
	s_addc_u32 s73, s35, 0
	global_load_lds_dwordx4 v227, s[34:35]
	s_mov_b32 m0, s68
	s_add_i32 s69, s70, s18
	s_add_i32 s70, s69, 0x2000
	global_load_lds_dwordx4 v0, s[34:35]
	s_mov_b32 m0, s69
	s_nop 0
	global_load_lds_dwordx4 v227, s[72:73]
	s_mov_b32 m0, s70
	s_nop 0
	global_load_lds_dwordx4 v0, s[72:73]
	s_mov_b32 m0, s20
	s_nop 0
	global_load_lds_dwordx4 v235, s[52:53]
	s_mov_b32 m0, s25
	s_nop 0
	global_load_lds_dwordx4 v226, s[52:53]
	s_waitcnt vmcnt(8)
	s_waitcnt lgkmcnt(0)
	s_setprio 1
	s_barrier
	s_waitcnt lgkmcnt(0)
	v_mfma_f32_16x16x32_bf16 v[134:137], v[2:5], v[62:65], 0
	v_mfma_f32_16x16x32_bf16 v[142:145], v[2:5], v[94:97], 0
	v_mfma_f32_16x16x32_bf16 v[150:153], v[2:5], v[110:113], 0
	v_mfma_f32_16x16x32_bf16 v[2:5], v[2:5], v[126:129], 0
	v_mfma_f32_16x16x32_bf16 v[134:137], v[6:9], v[90:93], v[134:137]
	v_mfma_f32_16x16x32_bf16 v[142:145], v[6:9], v[106:109], v[142:145]
	v_mfma_f32_16x16x32_bf16 v[150:153], v[6:9], v[122:125], v[150:153]
	v_mfma_f32_16x16x32_bf16 v[2:5], v[6:9], v[130:133], v[2:5]
	v_mfma_f32_16x16x32_bf16 v[6:9], v[10:13], v[126:129], 0
	v_mfma_f32_16x16x32_bf16 v[138:141], v[10:13], v[62:65], 0
	v_mfma_f32_16x16x32_bf16 v[146:149], v[10:13], v[94:97], 0
	v_mfma_f32_16x16x32_bf16 v[154:157], v[10:13], v[110:113], 0
	v_mfma_f32_16x16x32_bf16 v[6:9], v[14:17], v[130:133], v[6:9]
	v_mfma_f32_16x16x32_bf16 v[138:141], v[14:17], v[90:93], v[138:141]
	v_mfma_f32_16x16x32_bf16 v[146:149], v[14:17], v[106:109], v[146:149]
	v_mfma_f32_16x16x32_bf16 v[154:157], v[14:17], v[122:125], v[154:157]
	s_setprio 0
	s_setprio 1
	v_mfma_f32_16x16x32_bf16 v[10:13], v[18:21], v[62:65], 0
	v_mfma_f32_16x16x32_bf16 v[158:161], v[22:25], v[90:93], v[10:13]
	v_mfma_f32_16x16x32_bf16 v[10:13], v[26:29], v[62:65], 0
	v_mfma_f32_16x16x32_bf16 v[162:165], v[30:33], v[90:93], v[10:13]
	v_mfma_f32_16x16x32_bf16 v[10:13], v[18:21], v[94:97], 0
	v_mfma_f32_16x16x32_bf16 v[174:177], v[22:25], v[106:109], v[10:13]
	v_mfma_f32_16x16x32_bf16 v[10:13], v[26:29], v[94:97], 0
	v_mfma_f32_16x16x32_bf16 v[178:181], v[30:33], v[106:109], v[10:13]
	v_mfma_f32_16x16x32_bf16 v[10:13], v[18:21], v[110:113], 0
	v_mfma_f32_16x16x32_bf16 v[182:185], v[22:25], v[122:125], v[10:13]
	v_mfma_f32_16x16x32_bf16 v[10:13], v[26:29], v[110:113], 0
	v_mfma_f32_16x16x32_bf16 v[122:125], v[30:33], v[122:125], v[10:13]
	v_mfma_f32_16x16x32_bf16 v[10:13], v[18:21], v[126:129], 0
	v_mfma_f32_16x16x32_bf16 v[186:189], v[22:25], v[130:133], v[10:13]
	v_mfma_f32_16x16x32_bf16 v[10:13], v[26:29], v[126:129], 0
	v_mfma_f32_16x16x32_bf16 v[130:133], v[30:33], v[130:133], v[10:13]
	s_barrier
	s_setprio 0
	s_add_i32 s71, 0, 0x18000
	s_add_i32 s74, 0, 0x1c000
	v_add_u32_e32 v116, s71, v236
	v_add_u32_e32 v117, s74, v236
	s_nop 0
	ds_read_b128 v[10:13], v116
	ds_read_b128 v[14:17], v116 offset:1024
	ds_read_b128 v[18:21], v116 offset:2048
	ds_read_b128 v[22:25], v116 offset:3072
	ds_read_b128 v[194:197], v117
	ds_read_b128 v[198:201], v117 offset:1024
	ds_read_b128 v[202:205], v117 offset:2048
	ds_read_b128 v[206:209], v117 offset:3072
	s_add_u32 s52, s52, 0x4000
	s_addc_u32 s53, s53, 0
	s_mov_b32 m0, s54
	ds_read_b128 v[26:29], v237 offset:32768
	ds_read_b128 v[30:33], v237 offset:33792
	ds_read_b128 v[62:65], v237 offset:34816
	ds_read_b128 v[210:213], v237 offset:35840
	ds_read_b128 v[214:217], v237 offset:36864
	ds_read_b128 v[218:221], v237 offset:37888
	ds_read_b128 v[222:225], v237 offset:38912
	ds_read_b128 v[238:241], v237 offset:39936
	s_nop 0
	global_load_lds_dwordx4 v235, s[52:53]
	s_mov_b32 m0, s55
	s_nop 0
	global_load_lds_dwordx4 v226, s[52:53]
	s_waitcnt vmcnt(8)
	s_waitcnt lgkmcnt(0)
	s_setprio 1
	s_barrier
	s_waitcnt lgkmcnt(0)
	v_mfma_f32_16x16x32_bf16 v[66:69], v[10:13], v[26:29], v[66:69]
	v_mfma_f32_16x16x32_bf16 v[166:169], v[14:17], v[30:33], v[66:69]
	v_mfma_f32_16x16x32_bf16 v[66:69], v[18:21], v[26:29], v[70:73]
	v_mfma_f32_16x16x32_bf16 v[170:173], v[22:25], v[30:33], v[66:69]
	v_mfma_f32_16x16x32_bf16 v[66:69], v[10:13], v[62:65], v[74:77]
	v_mfma_f32_16x16x32_bf16 v[110:113], v[14:17], v[210:213], v[66:69]
	v_mfma_f32_16x16x32_bf16 v[66:69], v[18:21], v[62:65], v[78:81]
	v_mfma_f32_16x16x32_bf16 v[106:109], v[22:25], v[210:213], v[66:69]
	v_mfma_f32_16x16x32_bf16 v[66:69], v[10:13], v[214:217], v[82:85]
	v_mfma_f32_16x16x32_bf16 v[94:97], v[14:17], v[218:221], v[66:69]
	v_mfma_f32_16x16x32_bf16 v[66:69], v[18:21], v[214:217], v[86:89]
	v_mfma_f32_16x16x32_bf16 v[90:93], v[22:25], v[218:221], v[66:69]
	v_mfma_f32_16x16x32_bf16 v[66:69], v[10:13], v[222:225], v[98:101]
	v_mfma_f32_16x16x32_bf16 v[78:81], v[14:17], v[238:241], v[66:69]
	v_mfma_f32_16x16x32_bf16 v[66:69], v[18:21], v[222:225], v[102:105]
	v_mfma_f32_16x16x32_bf16 v[70:73], v[22:25], v[238:241], v[66:69]
	s_setprio 0
	s_setprio 1
	v_mfma_f32_16x16x32_bf16 v[66:69], v[194:197], v[26:29], v[118:121]
	v_mfma_f32_16x16x32_bf16 v[26:29], v[202:205], v[26:29], v[34:37]
	v_mfma_f32_16x16x32_bf16 v[118:121], v[206:209], v[30:33], v[26:29]
	v_mfma_f32_16x16x32_bf16 v[26:29], v[194:197], v[62:65], v[38:41]
	v_mfma_f32_16x16x32_bf16 v[102:105], v[198:201], v[210:213], v[26:29]
	v_mfma_f32_16x16x32_bf16 v[26:29], v[202:205], v[62:65], v[42:45]
	v_mfma_f32_16x16x32_bf16 v[98:101], v[206:209], v[210:213], v[26:29]
	v_mfma_f32_16x16x32_bf16 v[26:29], v[194:197], v[214:217], v[46:49]
	v_mfma_f32_16x16x32_bf16 v[86:89], v[198:201], v[218:221], v[26:29]
	v_mfma_f32_16x16x32_bf16 v[26:29], v[202:205], v[214:217], v[50:53]
	v_mfma_f32_16x16x32_bf16 v[82:85], v[206:209], v[218:221], v[26:29]
	v_mfma_f32_16x16x32_bf16 v[26:29], v[194:197], v[222:225], v[54:57]
	v_mfma_f32_16x16x32_bf16 v[62:65], v[198:201], v[238:241], v[26:29]
	v_mfma_f32_16x16x32_bf16 v[26:29], v[202:205], v[222:225], v[58:61]
	v_mfma_f32_16x16x32_bf16 v[126:129], v[198:201], v[30:33], v[66:69]
	v_mfma_f32_16x16x32_bf16 v[54:57], v[206:209], v[238:241], v[26:29]
	s_barrier
	s_setprio 0
	s_add_u32 s72, s34, 0x8000
	s_addc_u32 s73, s35, 0
	s_add_i32 s52, s71, s18
	s_add_i32 s53, s52, 0x2000
	s_mov_b32 m0, s52
	s_add_u32 s34, s34, 0xc000
	ds_read_b128 v[34:37], v237 offset:49152
	ds_read_b128 v[38:41], v237 offset:50176
	ds_read_b128 v[210:213], v237 offset:51200
	ds_read_b128 v[214:217], v237 offset:52224
	ds_read_b128 v[218:221], v237 offset:53248
	ds_read_b128 v[222:225], v237 offset:54272
	ds_read_b128 v[238:241], v237 offset:55296
	ds_read_b128 v[242:245], v237 offset:56320
	s_addc_u32 s35, s35, 0
	global_load_lds_dwordx4 v227, s[72:73]
	s_mov_b32 m0, s53
	s_add_i32 s71, s74, s18
	s_nop 0
	global_load_lds_dwordx4 v0, s[72:73]
	s_mov_b32 m0, s71
	s_add_i32 s72, s71, 0x2000
	s_nop 0
	global_load_lds_dwordx4 v227, s[34:35]
	s_mov_b32 m0, s72
	s_nop 0
	global_load_lds_dwordx4 v0, s[34:35]
	s_mov_b32 m0, s58
	s_nop 0
	global_load_lds_dwordx4 v235, s[30:31]
	s_mov_b32 m0, s59
	s_nop 0
	global_load_lds_dwordx4 v226, s[30:31]
	s_waitcnt vmcnt(8)
	s_waitcnt lgkmcnt(0)
	s_setprio 1
	s_barrier
	s_waitcnt lgkmcnt(0)
	v_mfma_f32_16x16x32_bf16 v[26:29], v[10:13], v[34:37], v[134:137]
	v_mfma_f32_16x16x32_bf16 v[74:77], v[14:17], v[38:41], v[26:29]
	v_mfma_f32_16x16x32_bf16 v[26:29], v[18:21], v[34:37], v[138:141]
	v_mfma_f32_16x16x32_bf16 v[66:69], v[22:25], v[38:41], v[26:29]
	v_mfma_f32_16x16x32_bf16 v[26:29], v[10:13], v[210:213], v[142:145]
	v_mfma_f32_16x16x32_bf16 v[46:49], v[14:17], v[214:217], v[26:29]
	v_mfma_f32_16x16x32_bf16 v[26:29], v[18:21], v[210:213], v[146:149]
	v_mfma_f32_16x16x32_bf16 v[42:45], v[22:25], v[214:217], v[26:29]
	v_mfma_f32_16x16x32_bf16 v[26:29], v[10:13], v[218:221], v[150:153]
	v_mfma_f32_16x16x32_bf16 v[2:5], v[10:13], v[238:241], v[2:5]
	v_mfma_f32_16x16x32_bf16 v[30:33], v[14:17], v[222:225], v[26:29]
	v_mfma_f32_16x16x32_bf16 v[26:29], v[18:21], v[218:221], v[154:157]
	v_mfma_f32_16x16x32_bf16 v[14:17], v[14:17], v[242:245], v[2:5]
	v_mfma_f32_16x16x32_bf16 v[2:5], v[18:21], v[238:241], v[6:9]
	v_mfma_f32_16x16x32_bf16 v[26:29], v[22:25], v[222:225], v[26:29]
	v_mfma_f32_16x16x32_bf16 v[10:13], v[22:25], v[242:245], v[2:5]
	s_setprio 0
	s_setprio 1
	v_mfma_f32_16x16x32_bf16 v[2:5], v[194:197], v[34:37], v[158:161]
	v_mfma_f32_16x16x32_bf16 v[58:61], v[198:201], v[38:41], v[2:5]
	v_mfma_f32_16x16x32_bf16 v[2:5], v[202:205], v[34:37], v[162:165]
	v_mfma_f32_16x16x32_bf16 v[50:53], v[206:209], v[38:41], v[2:5]
	v_mfma_f32_16x16x32_bf16 v[2:5], v[194:197], v[210:213], v[174:177]
	v_mfma_f32_16x16x32_bf16 v[38:41], v[198:201], v[214:217], v[2:5]
	v_mfma_f32_16x16x32_bf16 v[2:5], v[202:205], v[210:213], v[178:181]
	v_mfma_f32_16x16x32_bf16 v[34:37], v[206:209], v[214:217], v[2:5]
	v_mfma_f32_16x16x32_bf16 v[2:5], v[194:197], v[218:221], v[182:185]
	v_mfma_f32_16x16x32_bf16 v[22:25], v[198:201], v[222:225], v[2:5]
	v_mfma_f32_16x16x32_bf16 v[2:5], v[202:205], v[218:221], v[122:125]
	v_mfma_f32_16x16x32_bf16 v[18:21], v[206:209], v[222:225], v[2:5]
	v_mfma_f32_16x16x32_bf16 v[2:5], v[194:197], v[238:241], v[186:189]
	v_mfma_f32_16x16x32_bf16 v[6:9], v[198:201], v[242:245], v[2:5]
	v_mfma_f32_16x16x32_bf16 v[2:5], v[202:205], v[238:241], v[130:133]
	v_mfma_f32_16x16x32_bf16 v[2:5], v[206:209], v[242:245], v[2:5]
	s_barrier
	s_setprio 0
	s_andn2_b64 vcc, exec, s[48:49]
	s_cbranch_vccnz .LBB0_382
	s_add_u32 s73, s28, 0x20000
	s_addc_u32 s74, s29, 0
	s_add_u32 s26, s26, 0x1c000
	s_addc_u32 s27, s27, 0
	s_mov_b32 s75, 4
.LBB0_381:
	ds_read_b128 v[122:125], v114
	ds_read_b128 v[130:133], v114 offset:1024
	ds_read_b128 v[134:137], v114 offset:2048
	ds_read_b128 v[138:141], v114 offset:3072
	ds_read_b128 v[142:145], v115
	ds_read_b128 v[146:149], v115 offset:1024
	ds_read_b128 v[150:153], v115 offset:2048
	ds_read_b128 v[154:157], v115 offset:3072
	s_add_u32 s28, s26, 0x4000
	s_addc_u32 s29, s27, 0
	s_cmp_eq_u32 s56, s75
	s_cselect_b32 s34, s42, s28
	s_cselect_b32 s35, s43, s29
	s_cselect_b32 s30, s44, s73
	s_cselect_b32 s31, s45, s74
	s_add_u32 s28, s34, 0x8000
	s_addc_u32 s29, s35, 0
	s_mov_b32 m0, s65
	ds_read_b128 v[158:161], v237
	ds_read_b128 v[162:165], v237 offset:1024
	ds_read_b128 v[174:177], v237 offset:2048
	ds_read_b128 v[178:181], v237 offset:3072
	ds_read_b128 v[182:185], v237 offset:4096
	ds_read_b128 v[186:189], v237 offset:5120
	ds_read_b128 v[194:197], v237 offset:6144
	ds_read_b128 v[198:201], v237 offset:7168
	s_nop 0
	global_load_lds_dwordx4 v235, s[26:27]
	s_mov_b32 m0, s66
	s_nop 0
	global_load_lds_dwordx4 v226, s[26:27]
	s_waitcnt vmcnt(8)
	s_waitcnt lgkmcnt(0)
	s_setprio 1
	s_barrier
	s_waitcnt lgkmcnt(0)
	v_mfma_f32_16x16x32_bf16 v[166:169], v[122:125], v[158:161], v[166:169]
	v_mfma_f32_16x16x32_bf16 v[170:173], v[134:137], v[158:161], v[170:173]
	v_mfma_f32_16x16x32_bf16 v[110:113], v[122:125], v[174:177], v[110:113]
	v_mfma_f32_16x16x32_bf16 v[106:109], v[134:137], v[174:177], v[106:109]
	v_mfma_f32_16x16x32_bf16 v[94:97], v[122:125], v[182:185], v[94:97]
	v_mfma_f32_16x16x32_bf16 v[90:93], v[134:137], v[182:185], v[90:93]
	v_mfma_f32_16x16x32_bf16 v[78:81], v[122:125], v[194:197], v[78:81]
	v_mfma_f32_16x16x32_bf16 v[70:73], v[134:137], v[194:197], v[70:73]
	v_mfma_f32_16x16x32_bf16 v[166:169], v[130:133], v[162:165], v[166:169]
	v_mfma_f32_16x16x32_bf16 v[170:173], v[138:141], v[162:165], v[170:173]
	v_mfma_f32_16x16x32_bf16 v[110:113], v[130:133], v[178:181], v[110:113]
	v_mfma_f32_16x16x32_bf16 v[106:109], v[138:141], v[178:181], v[106:109]
	v_mfma_f32_16x16x32_bf16 v[94:97], v[130:133], v[186:189], v[94:97]
	v_mfma_f32_16x16x32_bf16 v[90:93], v[138:141], v[186:189], v[90:93]
	v_mfma_f32_16x16x32_bf16 v[78:81], v[130:133], v[198:201], v[78:81]
	v_mfma_f32_16x16x32_bf16 v[70:73], v[138:141], v[198:201], v[70:73]
	s_setprio 0
	s_setprio 1
	v_mfma_f32_16x16x32_bf16 v[126:129], v[142:145], v[158:161], v[126:129]
	v_mfma_f32_16x16x32_bf16 v[118:121], v[150:153], v[158:161], v[118:121]
	v_mfma_f32_16x16x32_bf16 v[102:105], v[142:145], v[174:177], v[102:105]
	v_mfma_f32_16x16x32_bf16 v[98:101], v[150:153], v[174:177], v[98:101]
	v_mfma_f32_16x16x32_bf16 v[86:89], v[142:145], v[182:185], v[86:89]
	v_mfma_f32_16x16x32_bf16 v[82:85], v[150:153], v[182:185], v[82:85]
	v_mfma_f32_16x16x32_bf16 v[62:65], v[142:145], v[194:197], v[62:65]
	v_mfma_f32_16x16x32_bf16 v[54:57], v[150:153], v[194:197], v[54:57]
	v_mfma_f32_16x16x32_bf16 v[126:129], v[146:149], v[162:165], v[126:129]
	v_mfma_f32_16x16x32_bf16 v[118:121], v[154:157], v[162:165], v[118:121]
	v_mfma_f32_16x16x32_bf16 v[102:105], v[146:149], v[178:181], v[102:105]
	v_mfma_f32_16x16x32_bf16 v[98:101], v[154:157], v[178:181], v[98:101]
	v_mfma_f32_16x16x32_bf16 v[86:89], v[146:149], v[186:189], v[86:89]
	v_mfma_f32_16x16x32_bf16 v[82:85], v[154:157], v[186:189], v[82:85]
	v_mfma_f32_16x16x32_bf16 v[62:65], v[146:149], v[198:201], v[62:65]
	v_mfma_f32_16x16x32_bf16 v[54:57], v[154:157], v[198:201], v[54:57]
	s_barrier
	s_setprio 0
	s_mov_b32 m0, s67
	ds_read_b128 v[158:161], v237 offset:16384
	ds_read_b128 v[162:165], v237 offset:17408
	ds_read_b128 v[174:177], v237 offset:18432
	ds_read_b128 v[178:181], v237 offset:19456
	ds_read_b128 v[182:185], v237 offset:20480
	ds_read_b128 v[186:189], v237 offset:21504
	ds_read_b128 v[194:197], v237 offset:22528
	ds_read_b128 v[198:201], v237 offset:23552
	s_add_u32 s76, s30, 0x4000
	global_load_lds_dwordx4 v227, s[30:31]
	s_mov_b32 m0, s68
	s_addc_u32 s77, s31, 0
	global_load_lds_dwordx4 v0, s[30:31]
	s_mov_b32 m0, s69
	s_nop 0
	global_load_lds_dwordx4 v227, s[76:77]
	s_mov_b32 m0, s70
	s_nop 0
	global_load_lds_dwordx4 v0, s[76:77]
	s_mov_b32 m0, s20
	s_nop 0
	global_load_lds_dwordx4 v235, s[34:35]
	s_mov_b32 m0, s25
	s_nop 0
	global_load_lds_dwordx4 v226, s[34:35]
	s_waitcnt vmcnt(8)
	s_waitcnt lgkmcnt(0)
	s_setprio 1
	s_barrier
	s_waitcnt lgkmcnt(0)
	v_mfma_f32_16x16x32_bf16 v[74:77], v[122:125], v[158:161], v[74:77]
	v_mfma_f32_16x16x32_bf16 v[66:69], v[134:137], v[158:161], v[66:69]
	v_mfma_f32_16x16x32_bf16 v[46:49], v[122:125], v[174:177], v[46:49]
	v_mfma_f32_16x16x32_bf16 v[42:45], v[134:137], v[174:177], v[42:45]
	v_mfma_f32_16x16x32_bf16 v[30:33], v[122:125], v[182:185], v[30:33]
	v_mfma_f32_16x16x32_bf16 v[26:29], v[134:137], v[182:185], v[26:29]
	v_mfma_f32_16x16x32_bf16 v[14:17], v[122:125], v[194:197], v[14:17]
	v_mfma_f32_16x16x32_bf16 v[10:13], v[134:137], v[194:197], v[10:13]
	v_mfma_f32_16x16x32_bf16 v[74:77], v[130:133], v[162:165], v[74:77]
	v_mfma_f32_16x16x32_bf16 v[66:69], v[138:141], v[162:165], v[66:69]
	v_mfma_f32_16x16x32_bf16 v[46:49], v[130:133], v[178:181], v[46:49]
	v_mfma_f32_16x16x32_bf16 v[42:45], v[138:141], v[178:181], v[42:45]
	v_mfma_f32_16x16x32_bf16 v[30:33], v[130:133], v[186:189], v[30:33]
	v_mfma_f32_16x16x32_bf16 v[26:29], v[138:141], v[186:189], v[26:29]
	v_mfma_f32_16x16x32_bf16 v[14:17], v[130:133], v[198:201], v[14:17]
	v_mfma_f32_16x16x32_bf16 v[10:13], v[138:141], v[198:201], v[10:13]
	s_setprio 0
	s_setprio 1
	v_mfma_f32_16x16x32_bf16 v[58:61], v[142:145], v[158:161], v[58:61]
	v_mfma_f32_16x16x32_bf16 v[50:53], v[150:153], v[158:161], v[50:53]
	v_mfma_f32_16x16x32_bf16 v[38:41], v[142:145], v[174:177], v[38:41]
	v_mfma_f32_16x16x32_bf16 v[34:37], v[150:153], v[174:177], v[34:37]
	v_mfma_f32_16x16x32_bf16 v[22:25], v[142:145], v[182:185], v[22:25]
	v_mfma_f32_16x16x32_bf16 v[18:21], v[150:153], v[182:185], v[18:21]
	v_mfma_f32_16x16x32_bf16 v[6:9], v[142:145], v[194:197], v[6:9]
	v_mfma_f32_16x16x32_bf16 v[2:5], v[150:153], v[194:197], v[2:5]
	v_mfma_f32_16x16x32_bf16 v[58:61], v[146:149], v[162:165], v[58:61]
	v_mfma_f32_16x16x32_bf16 v[50:53], v[154:157], v[162:165], v[50:53]
	v_mfma_f32_16x16x32_bf16 v[38:41], v[146:149], v[178:181], v[38:41]
	v_mfma_f32_16x16x32_bf16 v[34:37], v[154:157], v[178:181], v[34:37]
	v_mfma_f32_16x16x32_bf16 v[22:25], v[146:149], v[186:189], v[22:25]
	v_mfma_f32_16x16x32_bf16 v[18:21], v[154:157], v[186:189], v[18:21]
	v_mfma_f32_16x16x32_bf16 v[6:9], v[146:149], v[198:201], v[6:9]
	v_mfma_f32_16x16x32_bf16 v[2:5], v[154:157], v[198:201], v[2:5]
	s_barrier
	s_setprio 0
	ds_read_b128 v[122:125], v116
	ds_read_b128 v[130:133], v116 offset:1024
	ds_read_b128 v[134:137], v116 offset:2048
	ds_read_b128 v[138:141], v116 offset:3072
	ds_read_b128 v[142:145], v117
	ds_read_b128 v[146:149], v117 offset:1024
	ds_read_b128 v[150:153], v117 offset:2048
	ds_read_b128 v[154:157], v117 offset:3072
	s_add_u32 s34, s34, 0x4000
	s_addc_u32 s35, s35, 0
	s_mov_b32 m0, s54
	ds_read_b128 v[158:161], v237 offset:32768
	ds_read_b128 v[162:165], v237 offset:33792
	ds_read_b128 v[174:177], v237 offset:34816
	ds_read_b128 v[178:181], v237 offset:35840
	ds_read_b128 v[182:185], v237 offset:36864
	ds_read_b128 v[186:189], v237 offset:37888
	ds_read_b128 v[194:197], v237 offset:38912
	ds_read_b128 v[198:201], v237 offset:39936
	s_nop 0
	global_load_lds_dwordx4 v235, s[34:35]
	s_mov_b32 m0, s55
	s_nop 0
	global_load_lds_dwordx4 v226, s[34:35]
	s_waitcnt vmcnt(8)
	s_waitcnt lgkmcnt(0)
	s_setprio 1
	s_barrier
	s_waitcnt lgkmcnt(0)
	v_mfma_f32_16x16x32_bf16 v[166:169], v[122:125], v[158:161], v[166:169]
	v_mfma_f32_16x16x32_bf16 v[170:173], v[134:137], v[158:161], v[170:173]
	v_mfma_f32_16x16x32_bf16 v[110:113], v[122:125], v[174:177], v[110:113]
	v_mfma_f32_16x16x32_bf16 v[106:109], v[134:137], v[174:177], v[106:109]
	v_mfma_f32_16x16x32_bf16 v[94:97], v[122:125], v[182:185], v[94:97]
	v_mfma_f32_16x16x32_bf16 v[90:93], v[134:137], v[182:185], v[90:93]
	v_mfma_f32_16x16x32_bf16 v[78:81], v[122:125], v[194:197], v[78:81]
	v_mfma_f32_16x16x32_bf16 v[70:73], v[134:137], v[194:197], v[70:73]
	v_mfma_f32_16x16x32_bf16 v[166:169], v[130:133], v[162:165], v[166:169]
	v_mfma_f32_16x16x32_bf16 v[170:173], v[138:141], v[162:165], v[170:173]
	v_mfma_f32_16x16x32_bf16 v[110:113], v[130:133], v[178:181], v[110:113]
	v_mfma_f32_16x16x32_bf16 v[106:109], v[138:141], v[178:181], v[106:109]
	v_mfma_f32_16x16x32_bf16 v[94:97], v[130:133], v[186:189], v[94:97]
	v_mfma_f32_16x16x32_bf16 v[90:93], v[138:141], v[186:189], v[90:93]
	v_mfma_f32_16x16x32_bf16 v[78:81], v[130:133], v[198:201], v[78:81]
	v_mfma_f32_16x16x32_bf16 v[70:73], v[138:141], v[198:201], v[70:73]
	s_setprio 0
	s_setprio 1
	v_mfma_f32_16x16x32_bf16 v[126:129], v[142:145], v[158:161], v[126:129]
	v_mfma_f32_16x16x32_bf16 v[118:121], v[150:153], v[158:161], v[118:121]
	v_mfma_f32_16x16x32_bf16 v[102:105], v[142:145], v[174:177], v[102:105]
	v_mfma_f32_16x16x32_bf16 v[98:101], v[150:153], v[174:177], v[98:101]
	v_mfma_f32_16x16x32_bf16 v[86:89], v[142:145], v[182:185], v[86:89]
	v_mfma_f32_16x16x32_bf16 v[82:85], v[150:153], v[182:185], v[82:85]
	v_mfma_f32_16x16x32_bf16 v[62:65], v[142:145], v[194:197], v[62:65]
	v_mfma_f32_16x16x32_bf16 v[54:57], v[150:153], v[194:197], v[54:57]
	v_mfma_f32_16x16x32_bf16 v[126:129], v[146:149], v[162:165], v[126:129]
	v_mfma_f32_16x16x32_bf16 v[118:121], v[154:157], v[162:165], v[118:121]
	v_mfma_f32_16x16x32_bf16 v[102:105], v[146:149], v[178:181], v[102:105]
	v_mfma_f32_16x16x32_bf16 v[98:101], v[154:157], v[178:181], v[98:101]
	v_mfma_f32_16x16x32_bf16 v[86:89], v[146:149], v[186:189], v[86:89]
	v_mfma_f32_16x16x32_bf16 v[82:85], v[154:157], v[186:189], v[82:85]
	v_mfma_f32_16x16x32_bf16 v[62:65], v[146:149], v[198:201], v[62:65]
	v_mfma_f32_16x16x32_bf16 v[54:57], v[154:157], v[198:201], v[54:57]
	s_barrier
	s_setprio 0
	s_add_u32 s34, s30, 0x8000
	s_mov_b32 m0, s52
	s_addc_u32 s35, s31, 0
	ds_read_b128 v[158:161], v237 offset:49152
	ds_read_b128 v[162:165], v237 offset:50176
	ds_read_b128 v[174:177], v237 offset:51200
	ds_read_b128 v[178:181], v237 offset:52224
	ds_read_b128 v[182:185], v237 offset:53248
	ds_read_b128 v[186:189], v237 offset:54272
	ds_read_b128 v[194:197], v237 offset:55296
	ds_read_b128 v[198:201], v237 offset:56320
	s_add_u32 s30, s30, 0xc000
	global_load_lds_dwordx4 v227, s[34:35]
	s_mov_b32 m0, s53
	s_addc_u32 s31, s31, 0
	global_load_lds_dwordx4 v0, s[34:35]
	s_mov_b32 m0, s71
	s_nop 0
	global_load_lds_dwordx4 v227, s[30:31]
	s_mov_b32 m0, s72
	s_nop 0
	global_load_lds_dwordx4 v0, s[30:31]
	s_mov_b32 m0, s58
	s_nop 0
	global_load_lds_dwordx4 v235, s[28:29]
	s_mov_b32 m0, s59
	s_nop 0
	global_load_lds_dwordx4 v226, s[28:29]
	s_waitcnt vmcnt(8)
	s_waitcnt lgkmcnt(0)
	s_setprio 1
	s_barrier
	s_waitcnt lgkmcnt(0)
	v_mfma_f32_16x16x32_bf16 v[74:77], v[122:125], v[158:161], v[74:77]
	v_mfma_f32_16x16x32_bf16 v[66:69], v[134:137], v[158:161], v[66:69]
	v_mfma_f32_16x16x32_bf16 v[46:49], v[122:125], v[174:177], v[46:49]
	v_mfma_f32_16x16x32_bf16 v[42:45], v[134:137], v[174:177], v[42:45]
	v_mfma_f32_16x16x32_bf16 v[30:33], v[122:125], v[182:185], v[30:33]
	v_mfma_f32_16x16x32_bf16 v[26:29], v[134:137], v[182:185], v[26:29]
	v_mfma_f32_16x16x32_bf16 v[14:17], v[122:125], v[194:197], v[14:17]
	v_mfma_f32_16x16x32_bf16 v[10:13], v[134:137], v[194:197], v[10:13]
	v_mfma_f32_16x16x32_bf16 v[74:77], v[130:133], v[162:165], v[74:77]
	v_mfma_f32_16x16x32_bf16 v[66:69], v[138:141], v[162:165], v[66:69]
	v_mfma_f32_16x16x32_bf16 v[46:49], v[130:133], v[178:181], v[46:49]
	v_mfma_f32_16x16x32_bf16 v[42:45], v[138:141], v[178:181], v[42:45]
	v_mfma_f32_16x16x32_bf16 v[30:33], v[130:133], v[186:189], v[30:33]
	v_mfma_f32_16x16x32_bf16 v[26:29], v[138:141], v[186:189], v[26:29]
	v_mfma_f32_16x16x32_bf16 v[14:17], v[130:133], v[198:201], v[14:17]
	v_mfma_f32_16x16x32_bf16 v[10:13], v[138:141], v[198:201], v[10:13]
	s_setprio 0
	s_setprio 1
	v_mfma_f32_16x16x32_bf16 v[58:61], v[142:145], v[158:161], v[58:61]
	v_mfma_f32_16x16x32_bf16 v[50:53], v[150:153], v[158:161], v[50:53]
	v_mfma_f32_16x16x32_bf16 v[38:41], v[142:145], v[174:177], v[38:41]
	v_mfma_f32_16x16x32_bf16 v[34:37], v[150:153], v[174:177], v[34:37]
	v_mfma_f32_16x16x32_bf16 v[22:25], v[142:145], v[182:185], v[22:25]
	v_mfma_f32_16x16x32_bf16 v[18:21], v[150:153], v[182:185], v[18:21]
	v_mfma_f32_16x16x32_bf16 v[6:9], v[142:145], v[194:197], v[6:9]
	v_mfma_f32_16x16x32_bf16 v[2:5], v[150:153], v[194:197], v[2:5]
	v_mfma_f32_16x16x32_bf16 v[58:61], v[146:149], v[162:165], v[58:61]
	v_mfma_f32_16x16x32_bf16 v[50:53], v[154:157], v[162:165], v[50:53]
	v_mfma_f32_16x16x32_bf16 v[38:41], v[146:149], v[178:181], v[38:41]
	v_mfma_f32_16x16x32_bf16 v[34:37], v[154:157], v[178:181], v[34:37]
	v_mfma_f32_16x16x32_bf16 v[22:25], v[146:149], v[186:189], v[22:25]
	v_mfma_f32_16x16x32_bf16 v[18:21], v[154:157], v[186:189], v[18:21]
	v_mfma_f32_16x16x32_bf16 v[6:9], v[146:149], v[198:201], v[6:9]
	v_mfma_f32_16x16x32_bf16 v[2:5], v[154:157], v[198:201], v[2:5]
	s_barrier
	s_setprio 0
	s_add_i32 s28, s75, 2
	s_add_u32 s73, s73, 0x10000
	s_addc_u32 s74, s74, 0
	s_add_u32 s26, s26, 0x10000
	s_addc_u32 s27, s27, 0
	s_cmp_lt_i32 s75, s56
	s_mov_b32 s75, s28
	s_cbranch_scc1 .LBB0_381

.LBB0_454:
	s_or_b64 exec, exec, s[34:35]
	s_add_i32 s11, s11, 2
	s_add_u32 s18, s28, 0x4000
	s_addc_u32 s20, s29, 0
	s_and_b64 s[14:15], s[30:31], exec
	s_cselect_b32 s64, s18, s46
	s_cselect_b32 s65, s20, s47
	s_cselect_b32 s35, s2, s63
	s_cselect_b32 s34, s1, s62
	s_add_u32 s30, s64, 0x8000
	s_addc_u32 s31, s65, 0
	s_add_u32 s38, s34, 0x8000
	s_addc_u32 s39, s35, 0
	s_add_i32 s14, 0, 0x10000
	v_add_u32_e32 v149, s14, v146
	s_add_i32 s18, 0, 0x14000
	ds_read_b128 v[132:135], v149
	ds_read_b128 v[136:139], v149 offset:1024
	ds_read_b128 v[150:153], v149 offset:2048
	ds_read_b128 v[154:157], v149 offset:3072
	v_add_u32_e32 v149, s18, v146
	ds_read_b128 v[158:161], v149
	ds_read_b128 v[162:165], v149 offset:1024
	ds_read_b128 v[166:169], v149 offset:2048
	ds_read_b128 v[170:173], v149 offset:3072
	s_add_i32 m0, s71, 0xc000
	ds_read_b128 v[174:177], v148
	ds_read_b128 v[178:181], v148 offset:1024
	ds_read_b128 v[182:185], v148 offset:2048
	ds_read_b128 v[186:189], v148 offset:3072
	ds_read_b128 v[194:197], v148 offset:4096
	ds_read_b128 v[198:201], v148 offset:5120
	ds_read_b128 v[202:205], v148 offset:6144
	ds_read_b128 v[206:209], v148 offset:7168
	s_nop 0
	global_load_lds_dwordx4 v142, s[28:29]
	s_add_i32 m0, s71, 0xe000
	s_nop 0
	global_load_lds_dwordx4 v144, s[28:29]
	s_waitcnt vmcnt(8)
	s_waitcnt lgkmcnt(0)
	s_setprio 1
	s_barrier
	s_waitcnt lgkmcnt(0)
	v_mfma_f32_16x16x32_bf16 v[66:69], v[132:135], v[174:177], v[66:69]
	v_mfma_f32_16x16x32_bf16 v[70:73], v[150:153], v[174:177], v[70:73]
	v_mfma_f32_16x16x32_bf16 v[58:61], v[132:135], v[182:185], v[58:61]
	v_mfma_f32_16x16x32_bf16 v[62:65], v[150:153], v[182:185], v[62:65]
	v_mfma_f32_16x16x32_bf16 v[50:53], v[132:135], v[194:197], v[50:53]
	v_mfma_f32_16x16x32_bf16 v[54:57], v[150:153], v[194:197], v[54:57]
	v_mfma_f32_16x16x32_bf16 v[42:45], v[132:135], v[202:205], v[42:45]
	v_mfma_f32_16x16x32_bf16 v[46:49], v[150:153], v[202:205], v[46:49]
	v_mfma_f32_16x16x32_bf16 v[66:69], v[136:139], v[178:181], v[66:69]
	v_mfma_f32_16x16x32_bf16 v[70:73], v[154:157], v[178:181], v[70:73]
	v_mfma_f32_16x16x32_bf16 v[58:61], v[136:139], v[186:189], v[58:61]
	v_mfma_f32_16x16x32_bf16 v[62:65], v[154:157], v[186:189], v[62:65]
	v_mfma_f32_16x16x32_bf16 v[50:53], v[136:139], v[198:201], v[50:53]
	v_mfma_f32_16x16x32_bf16 v[54:57], v[154:157], v[198:201], v[54:57]
	v_mfma_f32_16x16x32_bf16 v[42:45], v[136:139], v[206:209], v[42:45]
	v_mfma_f32_16x16x32_bf16 v[46:49], v[154:157], v[206:209], v[46:49]
	s_setprio 0
	s_setprio 1
	v_mfma_f32_16x16x32_bf16 v[126:129], v[158:161], v[174:177], v[126:129]
	v_mfma_f32_16x16x32_bf16 v[122:125], v[166:169], v[174:177], v[122:125]
	v_mfma_f32_16x16x32_bf16 v[118:121], v[158:161], v[182:185], v[118:121]
	v_mfma_f32_16x16x32_bf16 v[114:117], v[166:169], v[182:185], v[114:117]
	v_mfma_f32_16x16x32_bf16 v[110:113], v[158:161], v[194:197], v[110:113]
	v_mfma_f32_16x16x32_bf16 v[106:109], v[166:169], v[194:197], v[106:109]
	v_mfma_f32_16x16x32_bf16 v[94:97], v[158:161], v[202:205], v[94:97]
	v_mfma_f32_16x16x32_bf16 v[90:93], v[166:169], v[202:205], v[90:93]
	v_mfma_f32_16x16x32_bf16 v[126:129], v[162:165], v[178:181], v[126:129]
	v_mfma_f32_16x16x32_bf16 v[122:125], v[170:173], v[178:181], v[122:125]
	v_mfma_f32_16x16x32_bf16 v[118:121], v[162:165], v[186:189], v[118:121]
	v_mfma_f32_16x16x32_bf16 v[114:117], v[170:173], v[186:189], v[114:117]
	v_mfma_f32_16x16x32_bf16 v[110:113], v[162:165], v[198:201], v[110:113]
	v_mfma_f32_16x16x32_bf16 v[106:109], v[170:173], v[198:201], v[106:109]
	v_mfma_f32_16x16x32_bf16 v[94:97], v[162:165], v[206:209], v[94:97]
	v_mfma_f32_16x16x32_bf16 v[90:93], v[170:173], v[206:209], v[90:93]
	s_barrier
	s_setprio 0
	s_add_i32 s14, s14, s70
	s_mov_b32 m0, s14
	ds_read_b128 v[174:177], v148 offset:16384
	ds_read_b128 v[178:181], v148 offset:17408
	ds_read_b128 v[182:185], v148 offset:18432
	ds_read_b128 v[186:189], v148 offset:19456
	ds_read_b128 v[194:197], v148 offset:20480
	ds_read_b128 v[198:201], v148 offset:21504
	ds_read_b128 v[202:205], v148 offset:22528
	ds_read_b128 v[206:209], v148 offset:23552
	s_nop 0
	global_load_lds_dwordx4 v143, s[34:35]
	s_add_i32 m0, s14, 0x2000
	s_add_u32 s14, s34, 0x4000
	s_addc_u32 s15, s35, 0
	s_add_i32 s18, s18, s70
	s_nop 0
	global_load_lds_dwordx4 v145, s[34:35]
	s_mov_b32 m0, s18
	s_nop 0
	global_load_lds_dwordx4 v143, s[14:15]
	s_add_i32 m0, s18, 0x2000
	s_nop 0
	global_load_lds_dwordx4 v145, s[14:15]
	s_mov_b32 m0, s71
	s_nop 0
	global_load_lds_dwordx4 v142, s[64:65]
	s_mov_b32 m0, s72
	s_nop 0
	global_load_lds_dwordx4 v144, s[64:65]
	s_waitcnt vmcnt(8)
	s_waitcnt lgkmcnt(0)
	s_setprio 1
	s_barrier
	s_waitcnt lgkmcnt(0)
	v_mfma_f32_16x16x32_bf16 v[26:29], v[132:135], v[174:177], v[26:29]
	v_mfma_f32_16x16x32_bf16 v[30:33], v[150:153], v[174:177], v[30:33]
	v_mfma_f32_16x16x32_bf16 v[18:21], v[132:135], v[182:185], v[18:21]
	v_mfma_f32_16x16x32_bf16 v[22:25], v[150:153], v[182:185], v[22:25]
	v_mfma_f32_16x16x32_bf16 v[10:13], v[132:135], v[194:197], v[10:13]
	v_mfma_f32_16x16x32_bf16 v[14:17], v[150:153], v[194:197], v[14:17]
	v_mfma_f32_16x16x32_bf16 v[2:5], v[132:135], v[202:205], v[2:5]
	v_mfma_f32_16x16x32_bf16 v[6:9], v[150:153], v[202:205], v[6:9]
	v_mfma_f32_16x16x32_bf16 v[26:29], v[136:139], v[178:181], v[26:29]
	v_mfma_f32_16x16x32_bf16 v[30:33], v[154:157], v[178:181], v[30:33]
	v_mfma_f32_16x16x32_bf16 v[18:21], v[136:139], v[186:189], v[18:21]
	v_mfma_f32_16x16x32_bf16 v[22:25], v[154:157], v[186:189], v[22:25]
	v_mfma_f32_16x16x32_bf16 v[10:13], v[136:139], v[198:201], v[10:13]
	v_mfma_f32_16x16x32_bf16 v[14:17], v[154:157], v[198:201], v[14:17]
	v_mfma_f32_16x16x32_bf16 v[2:5], v[136:139], v[206:209], v[2:5]
	v_mfma_f32_16x16x32_bf16 v[6:9], v[154:157], v[206:209], v[6:9]
	s_setprio 0
	s_setprio 1
	v_mfma_f32_16x16x32_bf16 v[102:105], v[158:161], v[174:177], v[102:105]
	v_mfma_f32_16x16x32_bf16 v[98:101], v[166:169], v[174:177], v[98:101]
	v_mfma_f32_16x16x32_bf16 v[82:85], v[158:161], v[182:185], v[82:85]
	v_mfma_f32_16x16x32_bf16 v[86:89], v[166:169], v[182:185], v[86:89]
	v_mfma_f32_16x16x32_bf16 v[78:81], v[158:161], v[194:197], v[78:81]
	v_mfma_f32_16x16x32_bf16 v[74:77], v[166:169], v[194:197], v[74:77]
	v_mfma_f32_16x16x32_bf16 v[34:37], v[158:161], v[202:205], v[34:37]
	v_mfma_f32_16x16x32_bf16 v[38:41], v[166:169], v[202:205], v[38:41]
	v_mfma_f32_16x16x32_bf16 v[102:105], v[162:165], v[178:181], v[102:105]
	v_mfma_f32_16x16x32_bf16 v[98:101], v[170:173], v[178:181], v[98:101]
	v_mfma_f32_16x16x32_bf16 v[82:85], v[162:165], v[186:189], v[82:85]
	v_mfma_f32_16x16x32_bf16 v[86:89], v[170:173], v[186:189], v[86:89]
	v_mfma_f32_16x16x32_bf16 v[78:81], v[162:165], v[198:201], v[78:81]
	v_mfma_f32_16x16x32_bf16 v[74:77], v[170:173], v[198:201], v[74:77]
	v_mfma_f32_16x16x32_bf16 v[34:37], v[162:165], v[206:209], v[34:37]
	v_mfma_f32_16x16x32_bf16 v[38:41], v[170:173], v[206:209], v[38:41]
	s_barrier
	s_setprio 0
	s_add_i32 s18, 0, 0x18000
	v_add_u32_e32 v149, s18, v146
	s_add_i32 s20, 0, 0x1c000
	ds_read_b128 v[132:135], v149
	ds_read_b128 v[136:139], v149 offset:1024
	ds_read_b128 v[150:153], v149 offset:2048
	ds_read_b128 v[154:157], v149 offset:3072
	v_add_u32_e32 v149, s20, v146
	ds_read_b128 v[158:161], v149
	ds_read_b128 v[162:165], v149 offset:1024
	ds_read_b128 v[166:169], v149 offset:2048
	ds_read_b128 v[170:173], v149 offset:3072
	s_add_u32 s14, s64, 0x4000
	s_addc_u32 s15, s65, 0
	s_mov_b32 m0, s73
	ds_read_b128 v[174:177], v148 offset:32768
	ds_read_b128 v[178:181], v148 offset:33792
	ds_read_b128 v[182:185], v148 offset:34816
	ds_read_b128 v[186:189], v148 offset:35840
	ds_read_b128 v[194:197], v148 offset:36864
	ds_read_b128 v[198:201], v148 offset:37888
	ds_read_b128 v[202:205], v148 offset:38912
	ds_read_b128 v[206:209], v148 offset:39936
	s_nop 0
	global_load_lds_dwordx4 v142, s[14:15]
	s_mov_b32 m0, s74
	s_nop 0
	global_load_lds_dwordx4 v144, s[14:15]
	s_waitcnt vmcnt(8)
	s_waitcnt lgkmcnt(0)
	s_setprio 1
	s_barrier
	s_waitcnt lgkmcnt(0)
	v_mfma_f32_16x16x32_bf16 v[66:69], v[132:135], v[174:177], v[66:69]
	v_mfma_f32_16x16x32_bf16 v[70:73], v[150:153], v[174:177], v[70:73]
	v_mfma_f32_16x16x32_bf16 v[58:61], v[132:135], v[182:185], v[58:61]
	v_mfma_f32_16x16x32_bf16 v[62:65], v[150:153], v[182:185], v[62:65]
	v_mfma_f32_16x16x32_bf16 v[50:53], v[132:135], v[194:197], v[50:53]
	v_mfma_f32_16x16x32_bf16 v[54:57], v[150:153], v[194:197], v[54:57]
	v_mfma_f32_16x16x32_bf16 v[42:45], v[132:135], v[202:205], v[42:45]
	v_mfma_f32_16x16x32_bf16 v[46:49], v[150:153], v[202:205], v[46:49]
	v_mfma_f32_16x16x32_bf16 v[66:69], v[136:139], v[178:181], v[66:69]
	v_mfma_f32_16x16x32_bf16 v[70:73], v[154:157], v[178:181], v[70:73]
	v_mfma_f32_16x16x32_bf16 v[58:61], v[136:139], v[186:189], v[58:61]
	v_mfma_f32_16x16x32_bf16 v[62:65], v[154:157], v[186:189], v[62:65]
	v_mfma_f32_16x16x32_bf16 v[50:53], v[136:139], v[198:201], v[50:53]
	v_mfma_f32_16x16x32_bf16 v[54:57], v[154:157], v[198:201], v[54:57]
	v_mfma_f32_16x16x32_bf16 v[42:45], v[136:139], v[206:209], v[42:45]
	v_mfma_f32_16x16x32_bf16 v[46:49], v[154:157], v[206:209], v[46:49]
	s_setprio 0
	s_setprio 1
	v_mfma_f32_16x16x32_bf16 v[126:129], v[158:161], v[174:177], v[126:129]
	v_mfma_f32_16x16x32_bf16 v[122:125], v[166:169], v[174:177], v[122:125]
	v_mfma_f32_16x16x32_bf16 v[118:121], v[158:161], v[182:185], v[118:121]
	v_mfma_f32_16x16x32_bf16 v[114:117], v[166:169], v[182:185], v[114:117]
	v_mfma_f32_16x16x32_bf16 v[110:113], v[158:161], v[194:197], v[110:113]
	v_mfma_f32_16x16x32_bf16 v[106:109], v[166:169], v[194:197], v[106:109]
	v_mfma_f32_16x16x32_bf16 v[94:97], v[158:161], v[202:205], v[94:97]
	v_mfma_f32_16x16x32_bf16 v[90:93], v[166:169], v[202:205], v[90:93]
	v_mfma_f32_16x16x32_bf16 v[126:129], v[162:165], v[178:181], v[126:129]
	v_mfma_f32_16x16x32_bf16 v[122:125], v[170:173], v[178:181], v[122:125]
	v_mfma_f32_16x16x32_bf16 v[118:121], v[162:165], v[186:189], v[118:121]
	v_mfma_f32_16x16x32_bf16 v[114:117], v[170:173], v[186:189], v[114:117]
	v_mfma_f32_16x16x32_bf16 v[110:113], v[162:165], v[198:201], v[110:113]
	v_mfma_f32_16x16x32_bf16 v[106:109], v[170:173], v[198:201], v[106:109]
	v_mfma_f32_16x16x32_bf16 v[94:97], v[162:165], v[206:209], v[94:97]
	v_mfma_f32_16x16x32_bf16 v[90:93], v[170:173], v[206:209], v[90:93]
	s_barrier
	s_setprio 0
	s_add_i32 s14, s18, s70
	s_mov_b32 m0, s14
	ds_read_b128 v[174:177], v148 offset:49152
	ds_read_b128 v[178:181], v148 offset:50176
	ds_read_b128 v[182:185], v148 offset:51200
	ds_read_b128 v[186:189], v148 offset:52224
	ds_read_b128 v[194:197], v148 offset:53248
	ds_read_b128 v[198:201], v148 offset:54272
	ds_read_b128 v[202:205], v148 offset:55296
	ds_read_b128 v[206:209], v148 offset:56320
	s_nop 0
	global_load_lds_dwordx4 v143, s[38:39]
	s_add_i32 m0, s14, 0x2000
	s_add_u32 s14, s34, 0xc000
	s_addc_u32 s15, s35, 0
	s_add_i32 s18, s20, s70
	s_nop 0
	global_load_lds_dwordx4 v145, s[38:39]
	s_mov_b32 m0, s18
	s_nop 0
	global_load_lds_dwordx4 v143, s[14:15]
	s_add_i32 m0, s18, 0x2000
	s_nop 0
	global_load_lds_dwordx4 v145, s[14:15]
	s_mov_b32 m0, s81
	s_nop 0
	global_load_lds_dwordx4 v142, s[30:31]
	s_mov_b32 m0, s82
	s_nop 0
	global_load_lds_dwordx4 v144, s[30:31]
	s_waitcnt vmcnt(8)
	s_waitcnt lgkmcnt(0)
	s_setprio 1
	s_barrier
	s_waitcnt lgkmcnt(0)
	v_mfma_f32_16x16x32_bf16 v[26:29], v[132:135], v[174:177], v[26:29]
	v_mfma_f32_16x16x32_bf16 v[30:33], v[150:153], v[174:177], v[30:33]
	v_mfma_f32_16x16x32_bf16 v[18:21], v[132:135], v[182:185], v[18:21]
	v_mfma_f32_16x16x32_bf16 v[22:25], v[150:153], v[182:185], v[22:25]
	v_mfma_f32_16x16x32_bf16 v[10:13], v[132:135], v[194:197], v[10:13]
	v_mfma_f32_16x16x32_bf16 v[14:17], v[150:153], v[194:197], v[14:17]
	v_mfma_f32_16x16x32_bf16 v[2:5], v[132:135], v[202:205], v[2:5]
	v_mfma_f32_16x16x32_bf16 v[6:9], v[150:153], v[202:205], v[6:9]
	v_mfma_f32_16x16x32_bf16 v[26:29], v[136:139], v[178:181], v[26:29]
	v_mfma_f32_16x16x32_bf16 v[30:33], v[154:157], v[178:181], v[30:33]
	v_mfma_f32_16x16x32_bf16 v[18:21], v[136:139], v[186:189], v[18:21]
	v_mfma_f32_16x16x32_bf16 v[22:25], v[154:157], v[186:189], v[22:25]
	v_mfma_f32_16x16x32_bf16 v[10:13], v[136:139], v[198:201], v[10:13]
	v_mfma_f32_16x16x32_bf16 v[14:17], v[154:157], v[198:201], v[14:17]
	v_mfma_f32_16x16x32_bf16 v[2:5], v[136:139], v[206:209], v[2:5]
	v_mfma_f32_16x16x32_bf16 v[6:9], v[154:157], v[206:209], v[6:9]
	s_setprio 0
	s_setprio 1
	v_mfma_f32_16x16x32_bf16 v[102:105], v[158:161], v[174:177], v[102:105]
	v_mfma_f32_16x16x32_bf16 v[98:101], v[166:169], v[174:177], v[98:101]
	v_mfma_f32_16x16x32_bf16 v[82:85], v[158:161], v[182:185], v[82:85]
	v_mfma_f32_16x16x32_bf16 v[86:89], v[166:169], v[182:185], v[86:89]
	v_mfma_f32_16x16x32_bf16 v[78:81], v[158:161], v[194:197], v[78:81]
	v_mfma_f32_16x16x32_bf16 v[74:77], v[166:169], v[194:197], v[74:77]
	v_mfma_f32_16x16x32_bf16 v[34:37], v[158:161], v[202:205], v[34:37]
	v_mfma_f32_16x16x32_bf16 v[38:41], v[166:169], v[202:205], v[38:41]
	v_mfma_f32_16x16x32_bf16 v[102:105], v[162:165], v[178:181], v[102:105]
	v_mfma_f32_16x16x32_bf16 v[98:101], v[170:173], v[178:181], v[98:101]
	v_mfma_f32_16x16x32_bf16 v[82:85], v[162:165], v[186:189], v[82:85]
	v_mfma_f32_16x16x32_bf16 v[86:89], v[170:173], v[186:189], v[86:89]
	v_mfma_f32_16x16x32_bf16 v[78:81], v[162:165], v[198:201], v[78:81]
	v_mfma_f32_16x16x32_bf16 v[74:77], v[170:173], v[198:201], v[74:77]
	v_mfma_f32_16x16x32_bf16 v[34:37], v[162:165], v[206:209], v[34:37]
	v_mfma_f32_16x16x32_bf16 v[38:41], v[170:173], v[206:209], v[38:41]
	s_barrier
	s_setprio 0
	s_add_u32 s1, s1, 0x10000
	s_addc_u32 s2, s2, 0
	s_add_u32 s28, s28, 0x10000
	s_addc_u32 s29, s29, 0
	s_cmp_ge_i32 s11, s78
	s_cbranch_scc1 .LBB0_457

.LBB0_498:
	s_add_i32 s83, s52, 2
	s_add_u32 s50, s48, 0x100
	s_addc_u32 s51, s49, 0
	s_add_i32 s84, 0, 0x10000
	s_cmp_eq_u32 s71, s52
	s_cselect_b32 s53, s43, s51
	s_cselect_b32 s52, s42, s50
	v_add_u32_e32 v131, s84, v137
	s_cselect_b32 s55, s47, s82
	s_cselect_b32 s54, s46, s81
	s_add_i32 s85, 0, 0x14000
	ds_read_b128 v[142:145], v131
	ds_read_b128 v[146:149], v131 offset:1024
	ds_read_b128 v[150:153], v131 offset:2048
	ds_read_b128 v[154:157], v131 offset:3072
	v_add_u32_e32 v131, s85, v137
	ds_read_b128 v[158:161], v131
	ds_read_b128 v[162:165], v131 offset:1024
	ds_read_b128 v[166:169], v131 offset:2048
	ds_read_b128 v[170:173], v131 offset:3072
	s_add_u32 s48, s48, s74
	s_addc_u32 s49, s49, s75
	s_add_i32 m0, s62, 0xc000
	ds_read_b128 v[174:177], v138
	ds_read_b128 v[178:181], v138 offset:1024
	ds_read_b128 v[182:185], v138 offset:2048
	ds_read_b128 v[186:189], v138 offset:3072
	ds_read_b128 v[194:197], v138 offset:4096
	ds_read_b128 v[198:201], v138 offset:5120
	ds_read_b128 v[202:205], v138 offset:6144
	ds_read_b128 v[206:209], v138 offset:7168
	s_nop 0
	global_load_lds_dwordx4 v130, s[48:49]
	s_add_i32 m0, s62, 0xe000
	s_nop 0
	global_load_lds_dwordx4 v132, s[48:49]
	s_waitcnt vmcnt(8)
	s_waitcnt lgkmcnt(0)
	s_setprio 1
	s_barrier
	s_waitcnt lgkmcnt(0)
	v_mfma_f32_16x16x32_bf16 v[118:121], v[142:145], v[174:177], v[118:121]
	v_mfma_f32_16x16x32_bf16 v[114:117], v[150:153], v[174:177], v[114:117]
	v_mfma_f32_16x16x32_bf16 v[102:105], v[142:145], v[182:185], v[102:105]
	v_mfma_f32_16x16x32_bf16 v[98:101], v[150:153], v[182:185], v[98:101]
	v_mfma_f32_16x16x32_bf16 v[86:89], v[142:145], v[194:197], v[86:89]
	v_mfma_f32_16x16x32_bf16 v[82:85], v[150:153], v[194:197], v[82:85]
	v_mfma_f32_16x16x32_bf16 v[70:73], v[142:145], v[202:205], v[70:73]
	v_mfma_f32_16x16x32_bf16 v[66:69], v[150:153], v[202:205], v[66:69]
	v_mfma_f32_16x16x32_bf16 v[118:121], v[146:149], v[178:181], v[118:121]
	v_mfma_f32_16x16x32_bf16 v[114:117], v[154:157], v[178:181], v[114:117]
	v_mfma_f32_16x16x32_bf16 v[102:105], v[146:149], v[186:189], v[102:105]
	v_mfma_f32_16x16x32_bf16 v[98:101], v[154:157], v[186:189], v[98:101]
	v_mfma_f32_16x16x32_bf16 v[86:89], v[146:149], v[198:201], v[86:89]
	v_mfma_f32_16x16x32_bf16 v[82:85], v[154:157], v[198:201], v[82:85]
	v_mfma_f32_16x16x32_bf16 v[70:73], v[146:149], v[206:209], v[70:73]
	v_mfma_f32_16x16x32_bf16 v[66:69], v[154:157], v[206:209], v[66:69]
	s_setprio 0
	s_setprio 1
	v_mfma_f32_16x16x32_bf16 v[46:49], v[158:161], v[174:177], v[46:49]
	v_mfma_f32_16x16x32_bf16 v[42:45], v[166:169], v[174:177], v[42:45]
	v_mfma_f32_16x16x32_bf16 v[30:33], v[158:161], v[182:185], v[30:33]
	v_mfma_f32_16x16x32_bf16 v[26:29], v[166:169], v[182:185], v[26:29]
	v_mfma_f32_16x16x32_bf16 v[14:17], v[158:161], v[194:197], v[14:17]
	v_mfma_f32_16x16x32_bf16 v[10:13], v[166:169], v[194:197], v[10:13]
	v_mfma_f32_16x16x32_bf16 v[6:9], v[158:161], v[202:205], v[6:9]
	v_mfma_f32_16x16x32_bf16 v[2:5], v[166:169], v[202:205], v[2:5]
	v_mfma_f32_16x16x32_bf16 v[46:49], v[162:165], v[178:181], v[46:49]
	v_mfma_f32_16x16x32_bf16 v[42:45], v[170:173], v[178:181], v[42:45]
	v_mfma_f32_16x16x32_bf16 v[30:33], v[162:165], v[186:189], v[30:33]
	v_mfma_f32_16x16x32_bf16 v[26:29], v[170:173], v[186:189], v[26:29]
	v_mfma_f32_16x16x32_bf16 v[14:17], v[162:165], v[198:201], v[14:17]
	v_mfma_f32_16x16x32_bf16 v[10:13], v[170:173], v[198:201], v[10:13]
	v_mfma_f32_16x16x32_bf16 v[6:9], v[162:165], v[206:209], v[6:9]
	v_mfma_f32_16x16x32_bf16 v[2:5], v[170:173], v[206:209], v[2:5]
	s_barrier
	s_setprio 0
	s_add_i32 s48, s84, s61
	s_mov_b32 m0, s48
	ds_read_b128 v[174:177], v138 offset:16384
	ds_read_b128 v[178:181], v138 offset:17408
	ds_read_b128 v[182:185], v138 offset:18432
	ds_read_b128 v[186:189], v138 offset:19456
	ds_read_b128 v[194:197], v138 offset:20480
	ds_read_b128 v[198:201], v138 offset:21504
	ds_read_b128 v[202:205], v138 offset:22528
	ds_read_b128 v[206:209], v138 offset:23552
	s_nop 0
	global_load_lds_dwordx4 v0, s[54:55]
	s_add_i32 m0, s48, 0x2000
	s_add_u32 s48, s54, s28
	s_addc_u32 s49, s55, s29
	s_add_i32 s84, s85, s61
	s_nop 0
	global_load_lds_dwordx4 v134, s[54:55]
	s_mov_b32 m0, s84
	s_nop 0
	global_load_lds_dwordx4 v0, s[48:49]
	s_add_i32 m0, s84, 0x2000
	s_nop 0
	global_load_lds_dwordx4 v134, s[48:49]
	s_mov_b32 m0, s62
	s_nop 0
	global_load_lds_dwordx4 v130, s[52:53]
	s_mov_b32 m0, s63
	s_nop 0
	global_load_lds_dwordx4 v132, s[52:53]
	s_waitcnt vmcnt(8)
	s_waitcnt lgkmcnt(0)
	s_setprio 1
	s_barrier
	s_waitcnt lgkmcnt(0)
	v_mfma_f32_16x16x32_bf16 v[126:129], v[142:145], v[174:177], v[126:129]
	v_mfma_f32_16x16x32_bf16 v[122:125], v[150:153], v[174:177], v[122:125]
	v_mfma_f32_16x16x32_bf16 v[110:113], v[142:145], v[182:185], v[110:113]
	v_mfma_f32_16x16x32_bf16 v[106:109], v[150:153], v[182:185], v[106:109]
	v_mfma_f32_16x16x32_bf16 v[94:97], v[142:145], v[194:197], v[94:97]
	v_mfma_f32_16x16x32_bf16 v[90:93], v[150:153], v[194:197], v[90:93]
	v_mfma_f32_16x16x32_bf16 v[78:81], v[142:145], v[202:205], v[78:81]
	v_mfma_f32_16x16x32_bf16 v[74:77], v[150:153], v[202:205], v[74:77]
	v_mfma_f32_16x16x32_bf16 v[126:129], v[146:149], v[178:181], v[126:129]
	v_mfma_f32_16x16x32_bf16 v[122:125], v[154:157], v[178:181], v[122:125]
	v_mfma_f32_16x16x32_bf16 v[110:113], v[146:149], v[186:189], v[110:113]
	v_mfma_f32_16x16x32_bf16 v[106:109], v[154:157], v[186:189], v[106:109]
	v_mfma_f32_16x16x32_bf16 v[94:97], v[146:149], v[198:201], v[94:97]
	v_mfma_f32_16x16x32_bf16 v[90:93], v[154:157], v[198:201], v[90:93]
	v_mfma_f32_16x16x32_bf16 v[78:81], v[146:149], v[206:209], v[78:81]
	v_mfma_f32_16x16x32_bf16 v[74:77], v[154:157], v[206:209], v[74:77]
	s_setprio 0
	s_setprio 1
	v_mfma_f32_16x16x32_bf16 v[54:57], v[158:161], v[174:177], v[54:57]
	v_mfma_f32_16x16x32_bf16 v[50:53], v[166:169], v[174:177], v[50:53]
	v_mfma_f32_16x16x32_bf16 v[38:41], v[158:161], v[182:185], v[38:41]
	v_mfma_f32_16x16x32_bf16 v[34:37], v[166:169], v[182:185], v[34:37]
	v_mfma_f32_16x16x32_bf16 v[22:25], v[158:161], v[194:197], v[22:25]
	v_mfma_f32_16x16x32_bf16 v[18:21], v[166:169], v[194:197], v[18:21]
	v_mfma_f32_16x16x32_bf16 v[58:61], v[158:161], v[202:205], v[58:61]
	v_mfma_f32_16x16x32_bf16 v[62:65], v[166:169], v[202:205], v[62:65]
	v_mfma_f32_16x16x32_bf16 v[54:57], v[162:165], v[178:181], v[54:57]
	v_mfma_f32_16x16x32_bf16 v[50:53], v[170:173], v[178:181], v[50:53]
	v_mfma_f32_16x16x32_bf16 v[38:41], v[162:165], v[186:189], v[38:41]
	v_mfma_f32_16x16x32_bf16 v[34:37], v[170:173], v[186:189], v[34:37]
	v_mfma_f32_16x16x32_bf16 v[22:25], v[162:165], v[198:201], v[22:25]
	v_mfma_f32_16x16x32_bf16 v[18:21], v[170:173], v[198:201], v[18:21]
	v_mfma_f32_16x16x32_bf16 v[58:61], v[162:165], v[206:209], v[58:61]
	v_mfma_f32_16x16x32_bf16 v[62:65], v[170:173], v[206:209], v[62:65]
	s_barrier
	s_setprio 0
	s_add_i32 s86, 0, 0x18000
	v_add_u32_e32 v131, s86, v137
	s_add_i32 s87, 0, 0x1c000
	ds_read_b128 v[142:145], v131
	ds_read_b128 v[146:149], v131 offset:1024
	ds_read_b128 v[150:153], v131 offset:2048
	ds_read_b128 v[154:157], v131 offset:3072
	v_add_u32_e32 v131, s87, v137
	ds_read_b128 v[158:161], v131
	ds_read_b128 v[162:165], v131 offset:1024
	ds_read_b128 v[166:169], v131 offset:2048
	ds_read_b128 v[170:173], v131 offset:3072
	s_add_u32 s84, s52, s28
	s_addc_u32 s85, s53, s29
	s_mov_b32 m0, s64
	ds_read_b128 v[174:177], v138 offset:32768
	ds_read_b128 v[178:181], v138 offset:33792
	ds_read_b128 v[182:185], v138 offset:34816
	ds_read_b128 v[186:189], v138 offset:35840
	ds_read_b128 v[194:197], v138 offset:36864
	ds_read_b128 v[198:201], v138 offset:37888
	ds_read_b128 v[202:205], v138 offset:38912
	ds_read_b128 v[206:209], v138 offset:39936
	s_nop 0
	global_load_lds_dwordx4 v130, s[84:85]
	s_mov_b32 m0, s65
	s_nop 0
	global_load_lds_dwordx4 v132, s[84:85]
	s_waitcnt vmcnt(8)
	s_waitcnt lgkmcnt(0)
	s_setprio 1
	s_barrier
	s_waitcnt lgkmcnt(0)
	v_mfma_f32_16x16x32_bf16 v[118:121], v[142:145], v[174:177], v[118:121]
	v_mfma_f32_16x16x32_bf16 v[114:117], v[150:153], v[174:177], v[114:117]
	v_mfma_f32_16x16x32_bf16 v[102:105], v[142:145], v[182:185], v[102:105]
	v_mfma_f32_16x16x32_bf16 v[98:101], v[150:153], v[182:185], v[98:101]
	v_mfma_f32_16x16x32_bf16 v[86:89], v[142:145], v[194:197], v[86:89]
	v_mfma_f32_16x16x32_bf16 v[82:85], v[150:153], v[194:197], v[82:85]
	v_mfma_f32_16x16x32_bf16 v[70:73], v[142:145], v[202:205], v[70:73]
	v_mfma_f32_16x16x32_bf16 v[66:69], v[150:153], v[202:205], v[66:69]
	v_mfma_f32_16x16x32_bf16 v[118:121], v[146:149], v[178:181], v[118:121]
	v_mfma_f32_16x16x32_bf16 v[114:117], v[154:157], v[178:181], v[114:117]
	v_mfma_f32_16x16x32_bf16 v[102:105], v[146:149], v[186:189], v[102:105]
	v_mfma_f32_16x16x32_bf16 v[98:101], v[154:157], v[186:189], v[98:101]
	v_mfma_f32_16x16x32_bf16 v[86:89], v[146:149], v[198:201], v[86:89]
	v_mfma_f32_16x16x32_bf16 v[82:85], v[154:157], v[198:201], v[82:85]
	v_mfma_f32_16x16x32_bf16 v[70:73], v[146:149], v[206:209], v[70:73]
	v_mfma_f32_16x16x32_bf16 v[66:69], v[154:157], v[206:209], v[66:69]
	s_setprio 0
	s_setprio 1
	v_mfma_f32_16x16x32_bf16 v[46:49], v[158:161], v[174:177], v[46:49]
	v_mfma_f32_16x16x32_bf16 v[42:45], v[166:169], v[174:177], v[42:45]
	v_mfma_f32_16x16x32_bf16 v[30:33], v[158:161], v[182:185], v[30:33]
	v_mfma_f32_16x16x32_bf16 v[26:29], v[166:169], v[182:185], v[26:29]
	v_mfma_f32_16x16x32_bf16 v[14:17], v[158:161], v[194:197], v[14:17]
	v_mfma_f32_16x16x32_bf16 v[10:13], v[166:169], v[194:197], v[10:13]
	v_mfma_f32_16x16x32_bf16 v[6:9], v[158:161], v[202:205], v[6:9]
	v_mfma_f32_16x16x32_bf16 v[2:5], v[166:169], v[202:205], v[2:5]
	v_mfma_f32_16x16x32_bf16 v[46:49], v[162:165], v[178:181], v[46:49]
	v_mfma_f32_16x16x32_bf16 v[42:45], v[170:173], v[178:181], v[42:45]
	v_mfma_f32_16x16x32_bf16 v[30:33], v[162:165], v[186:189], v[30:33]
	v_mfma_f32_16x16x32_bf16 v[26:29], v[170:173], v[186:189], v[26:29]
	v_mfma_f32_16x16x32_bf16 v[14:17], v[162:165], v[198:201], v[14:17]
	v_mfma_f32_16x16x32_bf16 v[10:13], v[170:173], v[198:201], v[10:13]
	v_mfma_f32_16x16x32_bf16 v[6:9], v[162:165], v[206:209], v[6:9]
	v_mfma_f32_16x16x32_bf16 v[2:5], v[170:173], v[206:209], v[2:5]
	s_barrier
	s_setprio 0
	ds_read_b128 v[174:177], v138 offset:49152
	ds_read_b128 v[178:181], v138 offset:50176
	ds_read_b128 v[182:185], v138 offset:51200
	ds_read_b128 v[186:189], v138 offset:52224
	ds_read_b128 v[194:197], v138 offset:53248
	ds_read_b128 v[198:201], v138 offset:54272
	ds_read_b128 v[202:205], v138 offset:55296
	ds_read_b128 v[206:209], v138 offset:56320
	s_add_i32 s84, s86, s61
	v_lshl_add_u64 v[190:191], s[54:55], 0, v[0:1]
	v_lshl_add_u64 v[190:191], v[190:191], 0, s[16:17]
	s_mov_b32 m0, s84
	v_mov_b32_e32 v135, v1
	global_load_lds_dwordx4 v[190:191], off
	s_add_i32 m0, s84, 0x2000
	v_lshl_add_u64 v[190:191], s[54:55], 0, v[134:135]
	v_lshl_add_u64 v[190:191], v[190:191], 0, s[16:17]
	global_load_lds_dwordx4 v[190:191], off
	s_add_i32 s54, s87, s61
	v_lshl_add_u64 v[190:191], s[48:49], 0, v[0:1]
	v_lshl_add_u64 v[190:191], v[190:191], 0, s[16:17]
	s_mov_b32 m0, s54
	v_mov_b32_e32 v131, v1
	global_load_lds_dwordx4 v[190:191], off
	s_add_i32 m0, s54, 0x2000
	v_lshl_add_u64 v[190:191], s[48:49], 0, v[134:135]
	v_lshl_add_u64 v[190:191], v[190:191], 0, s[16:17]
	global_load_lds_dwordx4 v[190:191], off
	s_mov_b32 m0, s66
	v_lshl_add_u64 v[190:191], s[52:53], 0, v[130:131]
	v_lshl_add_u64 v[190:191], v[190:191], 0, s[16:17]
	v_mov_b32_e32 v133, v1
	global_load_lds_dwordx4 v[190:191], off
	s_mov_b32 m0, s67
	v_lshl_add_u64 v[190:191], s[52:53], 0, v[132:133]
	v_lshl_add_u64 v[190:191], v[190:191], 0, s[16:17]
	global_load_lds_dwordx4 v[190:191], off
	s_waitcnt vmcnt(8)
	s_waitcnt lgkmcnt(0)
	s_setprio 1
	s_barrier
	s_waitcnt lgkmcnt(0)
	v_mfma_f32_16x16x32_bf16 v[126:129], v[142:145], v[174:177], v[126:129]
	v_mfma_f32_16x16x32_bf16 v[122:125], v[150:153], v[174:177], v[122:125]
	v_mfma_f32_16x16x32_bf16 v[110:113], v[142:145], v[182:185], v[110:113]
	v_mfma_f32_16x16x32_bf16 v[106:109], v[150:153], v[182:185], v[106:109]
	v_mfma_f32_16x16x32_bf16 v[94:97], v[142:145], v[194:197], v[94:97]
	v_mfma_f32_16x16x32_bf16 v[90:93], v[150:153], v[194:197], v[90:93]
	v_mfma_f32_16x16x32_bf16 v[78:81], v[142:145], v[202:205], v[78:81]
	v_mfma_f32_16x16x32_bf16 v[74:77], v[150:153], v[202:205], v[74:77]
	v_mfma_f32_16x16x32_bf16 v[126:129], v[146:149], v[178:181], v[126:129]
	v_mfma_f32_16x16x32_bf16 v[122:125], v[154:157], v[178:181], v[122:125]
	v_mfma_f32_16x16x32_bf16 v[110:113], v[146:149], v[186:189], v[110:113]
	v_mfma_f32_16x16x32_bf16 v[106:109], v[154:157], v[186:189], v[106:109]
	v_mfma_f32_16x16x32_bf16 v[94:97], v[146:149], v[198:201], v[94:97]
	v_mfma_f32_16x16x32_bf16 v[90:93], v[154:157], v[198:201], v[90:93]
	v_mfma_f32_16x16x32_bf16 v[78:81], v[146:149], v[206:209], v[78:81]
	v_mfma_f32_16x16x32_bf16 v[74:77], v[154:157], v[206:209], v[74:77]
	s_setprio 0
	s_setprio 1
	v_mfma_f32_16x16x32_bf16 v[54:57], v[158:161], v[174:177], v[54:57]
	v_mfma_f32_16x16x32_bf16 v[50:53], v[166:169], v[174:177], v[50:53]
	v_mfma_f32_16x16x32_bf16 v[38:41], v[158:161], v[182:185], v[38:41]
	v_mfma_f32_16x16x32_bf16 v[34:37], v[166:169], v[182:185], v[34:37]
	v_mfma_f32_16x16x32_bf16 v[22:25], v[158:161], v[194:197], v[22:25]
	v_mfma_f32_16x16x32_bf16 v[18:21], v[166:169], v[194:197], v[18:21]
	v_mfma_f32_16x16x32_bf16 v[58:61], v[158:161], v[202:205], v[58:61]
	v_mfma_f32_16x16x32_bf16 v[62:65], v[166:169], v[202:205], v[62:65]
	v_mfma_f32_16x16x32_bf16 v[54:57], v[162:165], v[178:181], v[54:57]
	v_mfma_f32_16x16x32_bf16 v[50:53], v[170:173], v[178:181], v[50:53]
	v_mfma_f32_16x16x32_bf16 v[38:41], v[162:165], v[186:189], v[38:41]
	v_mfma_f32_16x16x32_bf16 v[34:37], v[170:173], v[186:189], v[34:37]
	v_mfma_f32_16x16x32_bf16 v[22:25], v[162:165], v[198:201], v[22:25]
	v_mfma_f32_16x16x32_bf16 v[18:21], v[170:173], v[198:201], v[18:21]
	v_mfma_f32_16x16x32_bf16 v[58:61], v[162:165], v[206:209], v[58:61]
	v_mfma_f32_16x16x32_bf16 v[62:65], v[170:173], v[206:209], v[62:65]
	s_barrier
	s_setprio 0
	s_add_u32 s81, s81, 0x100
	s_addc_u32 s82, s82, 0
	s_cmp_ge_i32 s83, s68
	s_mov_b64 s[48:49], s[50:51]
	s_mov_b32 s52, s83
	s_cbranch_scc0 .LBB0_498

.LBB0_531:
	s_add_i32 s81, s52, 2
	s_add_u32 s50, s48, 0x100
	s_addc_u32 s51, s49, 0
	s_add_i32 s82, 0, 0x10000
	s_cmp_eq_u32 s71, s52
	s_cselect_b32 s53, s43, s51
	s_cselect_b32 s52, s42, s50
	v_add_u32_e32 v131, s82, v137
	s_cselect_b32 s55, s45, s80
	s_cselect_b32 s54, s44, s47
	s_add_i32 s83, 0, 0x14000
	ds_read_b128 v[142:145], v131
	ds_read_b128 v[146:149], v131 offset:1024
	ds_read_b128 v[150:153], v131 offset:2048
	ds_read_b128 v[154:157], v131 offset:3072
	v_add_u32_e32 v131, s83, v137
	ds_read_b128 v[158:161], v131
	ds_read_b128 v[162:165], v131 offset:1024
	ds_read_b128 v[166:169], v131 offset:2048
	ds_read_b128 v[170:173], v131 offset:3072
	s_add_u32 s48, s48, s74
	s_addc_u32 s49, s49, s75
	s_add_i32 m0, s62, 0xc000
	ds_read_b128 v[174:177], v138
	ds_read_b128 v[178:181], v138 offset:1024
	ds_read_b128 v[182:185], v138 offset:2048
	ds_read_b128 v[186:189], v138 offset:3072
	ds_read_b128 v[194:197], v138 offset:4096
	ds_read_b128 v[198:201], v138 offset:5120
	ds_read_b128 v[202:205], v138 offset:6144
	ds_read_b128 v[206:209], v138 offset:7168
	s_nop 0
	global_load_lds_dwordx4 v130, s[48:49]
	s_add_i32 m0, s62, 0xe000
	s_nop 0
	global_load_lds_dwordx4 v132, s[48:49]
	s_waitcnt vmcnt(8)
	s_waitcnt lgkmcnt(0)
	s_setprio 1
	s_barrier
	s_waitcnt lgkmcnt(0)
	v_mfma_f32_16x16x32_bf16 v[118:121], v[142:145], v[174:177], v[118:121]
	v_mfma_f32_16x16x32_bf16 v[114:117], v[150:153], v[174:177], v[114:117]
	v_mfma_f32_16x16x32_bf16 v[102:105], v[142:145], v[182:185], v[102:105]
	v_mfma_f32_16x16x32_bf16 v[98:101], v[150:153], v[182:185], v[98:101]
	v_mfma_f32_16x16x32_bf16 v[86:89], v[142:145], v[194:197], v[86:89]
	v_mfma_f32_16x16x32_bf16 v[82:85], v[150:153], v[194:197], v[82:85]
	v_mfma_f32_16x16x32_bf16 v[70:73], v[142:145], v[202:205], v[70:73]
	v_mfma_f32_16x16x32_bf16 v[66:69], v[150:153], v[202:205], v[66:69]
	v_mfma_f32_16x16x32_bf16 v[118:121], v[146:149], v[178:181], v[118:121]
	v_mfma_f32_16x16x32_bf16 v[114:117], v[154:157], v[178:181], v[114:117]
	v_mfma_f32_16x16x32_bf16 v[102:105], v[146:149], v[186:189], v[102:105]
	v_mfma_f32_16x16x32_bf16 v[98:101], v[154:157], v[186:189], v[98:101]
	v_mfma_f32_16x16x32_bf16 v[86:89], v[146:149], v[198:201], v[86:89]
	v_mfma_f32_16x16x32_bf16 v[82:85], v[154:157], v[198:201], v[82:85]
	v_mfma_f32_16x16x32_bf16 v[70:73], v[146:149], v[206:209], v[70:73]
	v_mfma_f32_16x16x32_bf16 v[66:69], v[154:157], v[206:209], v[66:69]
	s_setprio 0
	s_setprio 1
	v_mfma_f32_16x16x32_bf16 v[46:49], v[158:161], v[174:177], v[46:49]
	v_mfma_f32_16x16x32_bf16 v[42:45], v[166:169], v[174:177], v[42:45]
	v_mfma_f32_16x16x32_bf16 v[30:33], v[158:161], v[182:185], v[30:33]
	v_mfma_f32_16x16x32_bf16 v[26:29], v[166:169], v[182:185], v[26:29]
	v_mfma_f32_16x16x32_bf16 v[14:17], v[158:161], v[194:197], v[14:17]
	v_mfma_f32_16x16x32_bf16 v[10:13], v[166:169], v[194:197], v[10:13]
	v_mfma_f32_16x16x32_bf16 v[6:9], v[158:161], v[202:205], v[6:9]
	v_mfma_f32_16x16x32_bf16 v[2:5], v[166:169], v[202:205], v[2:5]
	v_mfma_f32_16x16x32_bf16 v[46:49], v[162:165], v[178:181], v[46:49]
	v_mfma_f32_16x16x32_bf16 v[42:45], v[170:173], v[178:181], v[42:45]
	v_mfma_f32_16x16x32_bf16 v[30:33], v[162:165], v[186:189], v[30:33]
	v_mfma_f32_16x16x32_bf16 v[26:29], v[170:173], v[186:189], v[26:29]
	v_mfma_f32_16x16x32_bf16 v[14:17], v[162:165], v[198:201], v[14:17]
	v_mfma_f32_16x16x32_bf16 v[10:13], v[170:173], v[198:201], v[10:13]
	v_mfma_f32_16x16x32_bf16 v[6:9], v[162:165], v[206:209], v[6:9]
	v_mfma_f32_16x16x32_bf16 v[2:5], v[170:173], v[206:209], v[2:5]
	s_barrier
	s_setprio 0
	s_add_i32 s48, s82, s61
	s_mov_b32 m0, s48
	ds_read_b128 v[174:177], v138 offset:16384
	ds_read_b128 v[178:181], v138 offset:17408
	ds_read_b128 v[182:185], v138 offset:18432
	ds_read_b128 v[186:189], v138 offset:19456
	ds_read_b128 v[194:197], v138 offset:20480
	ds_read_b128 v[198:201], v138 offset:21504
	ds_read_b128 v[202:205], v138 offset:22528
	ds_read_b128 v[206:209], v138 offset:23552
	s_nop 0
	global_load_lds_dwordx4 v0, s[54:55]
	s_add_i32 m0, s48, 0x2000
	s_add_u32 s48, s54, s26
	s_addc_u32 s49, s55, s27
	s_add_i32 s82, s83, s61
	s_nop 0
	global_load_lds_dwordx4 v134, s[54:55]
	s_mov_b32 m0, s82
	s_nop 0
	global_load_lds_dwordx4 v0, s[48:49]
	s_add_i32 m0, s82, 0x2000
	s_nop 0
	global_load_lds_dwordx4 v134, s[48:49]
	s_mov_b32 m0, s62
	s_nop 0
	global_load_lds_dwordx4 v130, s[52:53]
	s_mov_b32 m0, s63
	s_nop 0
	global_load_lds_dwordx4 v132, s[52:53]
	s_waitcnt vmcnt(8)
	s_waitcnt lgkmcnt(0)
	s_setprio 1
	s_barrier
	s_waitcnt lgkmcnt(0)
	v_mfma_f32_16x16x32_bf16 v[126:129], v[142:145], v[174:177], v[126:129]
	v_mfma_f32_16x16x32_bf16 v[122:125], v[150:153], v[174:177], v[122:125]
	v_mfma_f32_16x16x32_bf16 v[110:113], v[142:145], v[182:185], v[110:113]
	v_mfma_f32_16x16x32_bf16 v[106:109], v[150:153], v[182:185], v[106:109]
	v_mfma_f32_16x16x32_bf16 v[94:97], v[142:145], v[194:197], v[94:97]
	v_mfma_f32_16x16x32_bf16 v[90:93], v[150:153], v[194:197], v[90:93]
	v_mfma_f32_16x16x32_bf16 v[78:81], v[142:145], v[202:205], v[78:81]
	v_mfma_f32_16x16x32_bf16 v[74:77], v[150:153], v[202:205], v[74:77]
	v_mfma_f32_16x16x32_bf16 v[126:129], v[146:149], v[178:181], v[126:129]
	v_mfma_f32_16x16x32_bf16 v[122:125], v[154:157], v[178:181], v[122:125]
	v_mfma_f32_16x16x32_bf16 v[110:113], v[146:149], v[186:189], v[110:113]
	v_mfma_f32_16x16x32_bf16 v[106:109], v[154:157], v[186:189], v[106:109]
	v_mfma_f32_16x16x32_bf16 v[94:97], v[146:149], v[198:201], v[94:97]
	v_mfma_f32_16x16x32_bf16 v[90:93], v[154:157], v[198:201], v[90:93]
	v_mfma_f32_16x16x32_bf16 v[78:81], v[146:149], v[206:209], v[78:81]
	v_mfma_f32_16x16x32_bf16 v[74:77], v[154:157], v[206:209], v[74:77]
	s_setprio 0
	s_setprio 1
	v_mfma_f32_16x16x32_bf16 v[54:57], v[158:161], v[174:177], v[54:57]
	v_mfma_f32_16x16x32_bf16 v[50:53], v[166:169], v[174:177], v[50:53]
	v_mfma_f32_16x16x32_bf16 v[38:41], v[158:161], v[182:185], v[38:41]
	v_mfma_f32_16x16x32_bf16 v[34:37], v[166:169], v[182:185], v[34:37]
	v_mfma_f32_16x16x32_bf16 v[22:25], v[158:161], v[194:197], v[22:25]
	v_mfma_f32_16x16x32_bf16 v[18:21], v[166:169], v[194:197], v[18:21]
	v_mfma_f32_16x16x32_bf16 v[58:61], v[158:161], v[202:205], v[58:61]
	v_mfma_f32_16x16x32_bf16 v[62:65], v[166:169], v[202:205], v[62:65]
	v_mfma_f32_16x16x32_bf16 v[54:57], v[162:165], v[178:181], v[54:57]
	v_mfma_f32_16x16x32_bf16 v[50:53], v[170:173], v[178:181], v[50:53]
	v_mfma_f32_16x16x32_bf16 v[38:41], v[162:165], v[186:189], v[38:41]
	v_mfma_f32_16x16x32_bf16 v[34:37], v[170:173], v[186:189], v[34:37]
	v_mfma_f32_16x16x32_bf16 v[22:25], v[162:165], v[198:201], v[22:25]
	v_mfma_f32_16x16x32_bf16 v[18:21], v[170:173], v[198:201], v[18:21]
	v_mfma_f32_16x16x32_bf16 v[58:61], v[162:165], v[206:209], v[58:61]
	v_mfma_f32_16x16x32_bf16 v[62:65], v[170:173], v[206:209], v[62:65]
	s_barrier
	s_setprio 0
	s_add_i32 s84, 0, 0x18000
	v_add_u32_e32 v131, s84, v137
	s_add_i32 s85, 0, 0x1c000
	ds_read_b128 v[142:145], v131
	ds_read_b128 v[146:149], v131 offset:1024
	ds_read_b128 v[150:153], v131 offset:2048
	ds_read_b128 v[154:157], v131 offset:3072
	v_add_u32_e32 v131, s85, v137
	ds_read_b128 v[158:161], v131
	ds_read_b128 v[162:165], v131 offset:1024
	ds_read_b128 v[166:169], v131 offset:2048
	ds_read_b128 v[170:173], v131 offset:3072
	s_add_u32 s82, s52, s26
	s_addc_u32 s83, s53, s27
	s_mov_b32 m0, s64
	ds_read_b128 v[174:177], v138 offset:32768
	ds_read_b128 v[178:181], v138 offset:33792
	ds_read_b128 v[182:185], v138 offset:34816
	ds_read_b128 v[186:189], v138 offset:35840
	ds_read_b128 v[194:197], v138 offset:36864
	ds_read_b128 v[198:201], v138 offset:37888
	ds_read_b128 v[202:205], v138 offset:38912
	ds_read_b128 v[206:209], v138 offset:39936
	s_nop 0
	global_load_lds_dwordx4 v130, s[82:83]
	s_mov_b32 m0, s65
	s_nop 0
	global_load_lds_dwordx4 v132, s[82:83]
	s_waitcnt vmcnt(8)
	s_waitcnt lgkmcnt(0)
	s_setprio 1
	s_barrier
	s_waitcnt lgkmcnt(0)
	v_mfma_f32_16x16x32_bf16 v[118:121], v[142:145], v[174:177], v[118:121]
	v_mfma_f32_16x16x32_bf16 v[114:117], v[150:153], v[174:177], v[114:117]
	v_mfma_f32_16x16x32_bf16 v[102:105], v[142:145], v[182:185], v[102:105]
	v_mfma_f32_16x16x32_bf16 v[98:101], v[150:153], v[182:185], v[98:101]
	v_mfma_f32_16x16x32_bf16 v[86:89], v[142:145], v[194:197], v[86:89]
	v_mfma_f32_16x16x32_bf16 v[82:85], v[150:153], v[194:197], v[82:85]
	v_mfma_f32_16x16x32_bf16 v[70:73], v[142:145], v[202:205], v[70:73]
	v_mfma_f32_16x16x32_bf16 v[66:69], v[150:153], v[202:205], v[66:69]
	v_mfma_f32_16x16x32_bf16 v[118:121], v[146:149], v[178:181], v[118:121]
	v_mfma_f32_16x16x32_bf16 v[114:117], v[154:157], v[178:181], v[114:117]
	v_mfma_f32_16x16x32_bf16 v[102:105], v[146:149], v[186:189], v[102:105]
	v_mfma_f32_16x16x32_bf16 v[98:101], v[154:157], v[186:189], v[98:101]
	v_mfma_f32_16x16x32_bf16 v[86:89], v[146:149], v[198:201], v[86:89]
	v_mfma_f32_16x16x32_bf16 v[82:85], v[154:157], v[198:201], v[82:85]
	v_mfma_f32_16x16x32_bf16 v[70:73], v[146:149], v[206:209], v[70:73]
	v_mfma_f32_16x16x32_bf16 v[66:69], v[154:157], v[206:209], v[66:69]
	s_setprio 0
	s_setprio 1
	v_mfma_f32_16x16x32_bf16 v[46:49], v[158:161], v[174:177], v[46:49]
	v_mfma_f32_16x16x32_bf16 v[42:45], v[166:169], v[174:177], v[42:45]
	v_mfma_f32_16x16x32_bf16 v[30:33], v[158:161], v[182:185], v[30:33]
	v_mfma_f32_16x16x32_bf16 v[26:29], v[166:169], v[182:185], v[26:29]
	v_mfma_f32_16x16x32_bf16 v[14:17], v[158:161], v[194:197], v[14:17]
	v_mfma_f32_16x16x32_bf16 v[10:13], v[166:169], v[194:197], v[10:13]
	v_mfma_f32_16x16x32_bf16 v[6:9], v[158:161], v[202:205], v[6:9]
	v_mfma_f32_16x16x32_bf16 v[2:5], v[166:169], v[202:205], v[2:5]
	v_mfma_f32_16x16x32_bf16 v[46:49], v[162:165], v[178:181], v[46:49]
	v_mfma_f32_16x16x32_bf16 v[42:45], v[170:173], v[178:181], v[42:45]
	v_mfma_f32_16x16x32_bf16 v[30:33], v[162:165], v[186:189], v[30:33]
	v_mfma_f32_16x16x32_bf16 v[26:29], v[170:173], v[186:189], v[26:29]
	v_mfma_f32_16x16x32_bf16 v[14:17], v[162:165], v[198:201], v[14:17]
	v_mfma_f32_16x16x32_bf16 v[10:13], v[170:173], v[198:201], v[10:13]
	v_mfma_f32_16x16x32_bf16 v[6:9], v[162:165], v[206:209], v[6:9]
	v_mfma_f32_16x16x32_bf16 v[2:5], v[170:173], v[206:209], v[2:5]
	s_barrier
	s_setprio 0
	ds_read_b128 v[174:177], v138 offset:49152
	ds_read_b128 v[178:181], v138 offset:50176
	ds_read_b128 v[182:185], v138 offset:51200
	ds_read_b128 v[186:189], v138 offset:52224
	ds_read_b128 v[194:197], v138 offset:53248
	ds_read_b128 v[198:201], v138 offset:54272
	ds_read_b128 v[202:205], v138 offset:55296
	ds_read_b128 v[206:209], v138 offset:56320
	s_add_i32 s82, s84, s61
	v_lshl_add_u64 v[190:191], s[54:55], 0, v[0:1]
	v_lshl_add_u64 v[190:191], v[190:191], 0, s[16:17]
	s_mov_b32 m0, s82
	v_mov_b32_e32 v135, v1
	global_load_lds_dwordx4 v[190:191], off
	s_add_i32 m0, s82, 0x2000
	v_lshl_add_u64 v[190:191], s[54:55], 0, v[134:135]
	v_lshl_add_u64 v[190:191], v[190:191], 0, s[16:17]
	global_load_lds_dwordx4 v[190:191], off
	s_add_i32 s54, s85, s61
	v_lshl_add_u64 v[190:191], s[48:49], 0, v[0:1]
	v_lshl_add_u64 v[190:191], v[190:191], 0, s[16:17]
	s_mov_b32 m0, s54
	v_mov_b32_e32 v131, v1
	global_load_lds_dwordx4 v[190:191], off
	s_add_i32 m0, s54, 0x2000
	v_lshl_add_u64 v[190:191], s[48:49], 0, v[134:135]
	v_lshl_add_u64 v[190:191], v[190:191], 0, s[16:17]
	global_load_lds_dwordx4 v[190:191], off
	s_mov_b32 m0, s66
	v_lshl_add_u64 v[190:191], s[52:53], 0, v[130:131]
	v_lshl_add_u64 v[190:191], v[190:191], 0, s[16:17]
	v_mov_b32_e32 v133, v1
	global_load_lds_dwordx4 v[190:191], off
	s_mov_b32 m0, s67
	v_lshl_add_u64 v[190:191], s[52:53], 0, v[132:133]
	v_lshl_add_u64 v[190:191], v[190:191], 0, s[16:17]
	global_load_lds_dwordx4 v[190:191], off
	s_waitcnt vmcnt(8)
	s_waitcnt lgkmcnt(0)
	s_setprio 1
	s_barrier
	s_waitcnt lgkmcnt(0)
	v_mfma_f32_16x16x32_bf16 v[126:129], v[142:145], v[174:177], v[126:129]
	v_mfma_f32_16x16x32_bf16 v[122:125], v[150:153], v[174:177], v[122:125]
	v_mfma_f32_16x16x32_bf16 v[110:113], v[142:145], v[182:185], v[110:113]
	v_mfma_f32_16x16x32_bf16 v[106:109], v[150:153], v[182:185], v[106:109]
	v_mfma_f32_16x16x32_bf16 v[94:97], v[142:145], v[194:197], v[94:97]
	v_mfma_f32_16x16x32_bf16 v[90:93], v[150:153], v[194:197], v[90:93]
	v_mfma_f32_16x16x32_bf16 v[78:81], v[142:145], v[202:205], v[78:81]
	v_mfma_f32_16x16x32_bf16 v[74:77], v[150:153], v[202:205], v[74:77]
	v_mfma_f32_16x16x32_bf16 v[126:129], v[146:149], v[178:181], v[126:129]
	v_mfma_f32_16x16x32_bf16 v[122:125], v[154:157], v[178:181], v[122:125]
	v_mfma_f32_16x16x32_bf16 v[110:113], v[146:149], v[186:189], v[110:113]
	v_mfma_f32_16x16x32_bf16 v[106:109], v[154:157], v[186:189], v[106:109]
	v_mfma_f32_16x16x32_bf16 v[94:97], v[146:149], v[198:201], v[94:97]
	v_mfma_f32_16x16x32_bf16 v[90:93], v[154:157], v[198:201], v[90:93]
	v_mfma_f32_16x16x32_bf16 v[78:81], v[146:149], v[206:209], v[78:81]
	v_mfma_f32_16x16x32_bf16 v[74:77], v[154:157], v[206:209], v[74:77]
	s_setprio 0
	s_setprio 1
	v_mfma_f32_16x16x32_bf16 v[54:57], v[158:161], v[174:177], v[54:57]
	v_mfma_f32_16x16x32_bf16 v[50:53], v[166:169], v[174:177], v[50:53]
	v_mfma_f32_16x16x32_bf16 v[38:41], v[158:161], v[182:185], v[38:41]
	v_mfma_f32_16x16x32_bf16 v[34:37], v[166:169], v[182:185], v[34:37]
	v_mfma_f32_16x16x32_bf16 v[22:25], v[158:161], v[194:197], v[22:25]
	v_mfma_f32_16x16x32_bf16 v[18:21], v[166:169], v[194:197], v[18:21]
	v_mfma_f32_16x16x32_bf16 v[58:61], v[158:161], v[202:205], v[58:61]
	v_mfma_f32_16x16x32_bf16 v[62:65], v[166:169], v[202:205], v[62:65]
	v_mfma_f32_16x16x32_bf16 v[54:57], v[162:165], v[178:181], v[54:57]
	v_mfma_f32_16x16x32_bf16 v[50:53], v[170:173], v[178:181], v[50:53]
	v_mfma_f32_16x16x32_bf16 v[38:41], v[162:165], v[186:189], v[38:41]
	v_mfma_f32_16x16x32_bf16 v[34:37], v[170:173], v[186:189], v[34:37]
	v_mfma_f32_16x16x32_bf16 v[22:25], v[162:165], v[198:201], v[22:25]
	v_mfma_f32_16x16x32_bf16 v[18:21], v[170:173], v[198:201], v[18:21]
	v_mfma_f32_16x16x32_bf16 v[58:61], v[162:165], v[206:209], v[58:61]
	v_mfma_f32_16x16x32_bf16 v[62:65], v[170:173], v[206:209], v[62:65]
	s_barrier
	s_setprio 0
	s_add_u32 s47, s47, 0x100
	s_addc_u32 s80, s80, 0
	s_cmp_ge_i32 s81, s68
	s_mov_b64 s[48:49], s[50:51]
	s_mov_b32 s52, s81
	s_cbranch_scc0 .LBB0_531

.LBB0_707:
	s_add_i32 s74, s52, 2
	s_add_u32 s50, s48, 0x100
	s_addc_u32 s51, s49, 0
	s_add_i32 s75, 0, 0x10000
	s_cmp_eq_u32 s64, s52
	s_cselect_b32 s53, s41, s51
	s_cselect_b32 s52, s40, s50
	v_add_u32_e32 v139, s75, v148
	s_cselect_b32 s55, s47, s73
	s_cselect_b32 s54, s46, s72
	s_add_i32 s76, 0, 0x14000
	ds_read_b128 v[130:133], v139
	ds_read_b128 v[134:137], v139 offset:1024
	ds_read_b128 v[140:143], v139 offset:2048
	ds_read_b128 v[150:153], v139 offset:3072
	v_add_u32_e32 v139, s76, v148
	ds_read_b128 v[154:157], v139
	ds_read_b128 v[158:161], v139 offset:1024
	ds_read_b128 v[162:165], v139 offset:2048
	ds_read_b128 v[166:169], v139 offset:3072
	s_add_u32 s48, s48, s66
	s_addc_u32 s49, s49, s67
	s_add_i32 m0, s15, 0xc000
	ds_read_b128 v[170:173], v149
	ds_read_b128 v[174:177], v149 offset:1024
	ds_read_b128 v[178:181], v149 offset:2048
	ds_read_b128 v[182:185], v149 offset:3072
	ds_read_b128 v[186:189], v149 offset:4096
	ds_read_b128 v[194:197], v149 offset:5120
	ds_read_b128 v[198:201], v149 offset:6144
	ds_read_b128 v[202:205], v149 offset:7168
	s_nop 0
	global_load_lds_dwordx4 v0, s[48:49]
	s_add_i32 m0, s15, 0xe000
	s_nop 0
	global_load_lds_dwordx4 v138, s[48:49]
	s_waitcnt vmcnt(8)
	s_waitcnt lgkmcnt(0)
	s_setprio 1
	s_barrier
	s_waitcnt lgkmcnt(0)
	v_mfma_f32_16x16x32_bf16 v[122:125], v[130:133], v[170:173], v[122:125]
	v_mfma_f32_16x16x32_bf16 v[126:129], v[140:143], v[170:173], v[126:129]
	v_mfma_f32_16x16x32_bf16 v[118:121], v[130:133], v[178:181], v[118:121]
	v_mfma_f32_16x16x32_bf16 v[114:117], v[140:143], v[178:181], v[114:117]
	v_mfma_f32_16x16x32_bf16 v[102:105], v[130:133], v[186:189], v[102:105]
	v_mfma_f32_16x16x32_bf16 v[98:101], v[140:143], v[186:189], v[98:101]
	v_mfma_f32_16x16x32_bf16 v[86:89], v[130:133], v[198:201], v[86:89]
	v_mfma_f32_16x16x32_bf16 v[82:85], v[140:143], v[198:201], v[82:85]
	v_mfma_f32_16x16x32_bf16 v[122:125], v[134:137], v[174:177], v[122:125]
	v_mfma_f32_16x16x32_bf16 v[126:129], v[150:153], v[174:177], v[126:129]
	v_mfma_f32_16x16x32_bf16 v[118:121], v[134:137], v[182:185], v[118:121]
	v_mfma_f32_16x16x32_bf16 v[114:117], v[150:153], v[182:185], v[114:117]
	v_mfma_f32_16x16x32_bf16 v[102:105], v[134:137], v[194:197], v[102:105]
	v_mfma_f32_16x16x32_bf16 v[98:101], v[150:153], v[194:197], v[98:101]
	v_mfma_f32_16x16x32_bf16 v[86:89], v[134:137], v[202:205], v[86:89]
	v_mfma_f32_16x16x32_bf16 v[82:85], v[150:153], v[202:205], v[82:85]
	s_setprio 0
	s_setprio 1
	v_mfma_f32_16x16x32_bf16 v[58:61], v[154:157], v[170:173], v[58:61]
	v_mfma_f32_16x16x32_bf16 v[62:65], v[162:165], v[170:173], v[62:65]
	v_mfma_f32_16x16x32_bf16 v[54:57], v[154:157], v[178:181], v[54:57]
	v_mfma_f32_16x16x32_bf16 v[50:53], v[162:165], v[178:181], v[50:53]
	v_mfma_f32_16x16x32_bf16 v[38:41], v[154:157], v[186:189], v[38:41]
	v_mfma_f32_16x16x32_bf16 v[34:37], v[162:165], v[186:189], v[34:37]
	v_mfma_f32_16x16x32_bf16 v[14:17], v[154:157], v[198:201], v[14:17]
	v_mfma_f32_16x16x32_bf16 v[10:13], v[162:165], v[198:201], v[10:13]
	v_mfma_f32_16x16x32_bf16 v[58:61], v[158:161], v[174:177], v[58:61]
	v_mfma_f32_16x16x32_bf16 v[62:65], v[166:169], v[174:177], v[62:65]
	v_mfma_f32_16x16x32_bf16 v[54:57], v[158:161], v[182:185], v[54:57]
	v_mfma_f32_16x16x32_bf16 v[50:53], v[166:169], v[182:185], v[50:53]
	v_mfma_f32_16x16x32_bf16 v[38:41], v[158:161], v[194:197], v[38:41]
	v_mfma_f32_16x16x32_bf16 v[34:37], v[166:169], v[194:197], v[34:37]
	v_mfma_f32_16x16x32_bf16 v[14:17], v[158:161], v[202:205], v[14:17]
	v_mfma_f32_16x16x32_bf16 v[10:13], v[166:169], v[202:205], v[10:13]
	s_barrier
	s_setprio 0
	s_add_i32 s48, s75, s14
	s_mov_b32 m0, s48
	ds_read_b128 v[170:173], v149 offset:16384
	ds_read_b128 v[174:177], v149 offset:17408
	ds_read_b128 v[178:181], v149 offset:18432
	ds_read_b128 v[182:185], v149 offset:19456
	ds_read_b128 v[186:189], v149 offset:20480
	ds_read_b128 v[194:197], v149 offset:21504
	ds_read_b128 v[198:201], v149 offset:22528
	ds_read_b128 v[202:205], v149 offset:23552
	s_nop 0
	global_load_lds_dwordx4 v147, s[54:55]
	s_add_i32 m0, s48, 0x2000
	s_add_u32 s48, s54, 0x4000
	s_addc_u32 s49, s55, 0
	s_add_i32 s75, s76, s14
	s_nop 0
	global_load_lds_dwordx4 v146, s[54:55]
	s_mov_b32 m0, s75
	s_nop 0
	global_load_lds_dwordx4 v147, s[48:49]
	s_add_i32 m0, s75, 0x2000
	s_nop 0
	global_load_lds_dwordx4 v146, s[48:49]
	s_mov_b32 m0, s15
	s_nop 0
	global_load_lds_dwordx4 v0, s[52:53]
	s_mov_b32 m0, s18
	s_nop 0
	global_load_lds_dwordx4 v138, s[52:53]
	s_waitcnt vmcnt(8)
	s_waitcnt lgkmcnt(0)
	s_setprio 1
	s_barrier
	s_waitcnt lgkmcnt(0)
	v_mfma_f32_16x16x32_bf16 v[110:113], v[130:133], v[170:173], v[110:113]
	v_mfma_f32_16x16x32_bf16 v[106:109], v[140:143], v[170:173], v[106:109]
	v_mfma_f32_16x16x32_bf16 v[94:97], v[130:133], v[178:181], v[94:97]
	v_mfma_f32_16x16x32_bf16 v[90:93], v[140:143], v[178:181], v[90:93]
	v_mfma_f32_16x16x32_bf16 v[78:81], v[130:133], v[186:189], v[78:81]
	v_mfma_f32_16x16x32_bf16 v[74:77], v[140:143], v[186:189], v[74:77]
	v_mfma_f32_16x16x32_bf16 v[70:73], v[130:133], v[198:201], v[70:73]
	v_mfma_f32_16x16x32_bf16 v[66:69], v[140:143], v[198:201], v[66:69]
	v_mfma_f32_16x16x32_bf16 v[110:113], v[134:137], v[174:177], v[110:113]
	v_mfma_f32_16x16x32_bf16 v[106:109], v[150:153], v[174:177], v[106:109]
	v_mfma_f32_16x16x32_bf16 v[94:97], v[134:137], v[182:185], v[94:97]
	v_mfma_f32_16x16x32_bf16 v[90:93], v[150:153], v[182:185], v[90:93]
	v_mfma_f32_16x16x32_bf16 v[78:81], v[134:137], v[194:197], v[78:81]
	v_mfma_f32_16x16x32_bf16 v[74:77], v[150:153], v[194:197], v[74:77]
	v_mfma_f32_16x16x32_bf16 v[70:73], v[134:137], v[202:205], v[70:73]
	v_mfma_f32_16x16x32_bf16 v[66:69], v[150:153], v[202:205], v[66:69]
	s_setprio 0
	s_setprio 1
	v_mfma_f32_16x16x32_bf16 v[46:49], v[154:157], v[170:173], v[46:49]
	v_mfma_f32_16x16x32_bf16 v[42:45], v[162:165], v[170:173], v[42:45]
	v_mfma_f32_16x16x32_bf16 v[26:29], v[154:157], v[178:181], v[26:29]
	v_mfma_f32_16x16x32_bf16 v[22:25], v[162:165], v[178:181], v[22:25]
	v_mfma_f32_16x16x32_bf16 v[6:9], v[154:157], v[186:189], v[6:9]
	v_mfma_f32_16x16x32_bf16 v[2:5], v[162:165], v[186:189], v[2:5]
	v_mfma_f32_16x16x32_bf16 v[18:21], v[154:157], v[198:201], v[18:21]
	v_mfma_f32_16x16x32_bf16 v[30:33], v[162:165], v[198:201], v[30:33]
	v_mfma_f32_16x16x32_bf16 v[46:49], v[158:161], v[174:177], v[46:49]
	v_mfma_f32_16x16x32_bf16 v[42:45], v[166:169], v[174:177], v[42:45]
	v_mfma_f32_16x16x32_bf16 v[26:29], v[158:161], v[182:185], v[26:29]
	v_mfma_f32_16x16x32_bf16 v[22:25], v[166:169], v[182:185], v[22:25]
	v_mfma_f32_16x16x32_bf16 v[6:9], v[158:161], v[194:197], v[6:9]
	v_mfma_f32_16x16x32_bf16 v[2:5], v[166:169], v[194:197], v[2:5]
	v_mfma_f32_16x16x32_bf16 v[18:21], v[158:161], v[202:205], v[18:21]
	v_mfma_f32_16x16x32_bf16 v[30:33], v[166:169], v[202:205], v[30:33]
	s_barrier
	s_setprio 0
	s_add_i32 s75, 0, 0x18000
	v_add_u32_e32 v139, s75, v148
	s_add_i32 s76, 0, 0x1c000
	ds_read_b128 v[130:133], v139
	ds_read_b128 v[134:137], v139 offset:1024
	ds_read_b128 v[140:143], v139 offset:2048
	ds_read_b128 v[150:153], v139 offset:3072
	v_add_u32_e32 v139, s76, v148
	ds_read_b128 v[154:157], v139
	ds_read_b128 v[158:161], v139 offset:1024
	ds_read_b128 v[162:165], v139 offset:2048
	ds_read_b128 v[166:169], v139 offset:3072
	s_add_u32 s48, s52, s26
	s_addc_u32 s49, s53, s27
	s_mov_b32 m0, s20
	ds_read_b128 v[170:173], v149 offset:32768
	ds_read_b128 v[174:177], v149 offset:33792
	ds_read_b128 v[178:181], v149 offset:34816
	ds_read_b128 v[182:185], v149 offset:35840
	ds_read_b128 v[186:189], v149 offset:36864
	ds_read_b128 v[194:197], v149 offset:37888
	ds_read_b128 v[198:201], v149 offset:38912
	ds_read_b128 v[202:205], v149 offset:39936
	s_nop 0
	global_load_lds_dwordx4 v0, s[48:49]
	s_mov_b32 m0, s21
	s_nop 0
	global_load_lds_dwordx4 v138, s[48:49]
	s_waitcnt vmcnt(8)
	s_waitcnt lgkmcnt(0)
	s_setprio 1
	s_barrier
	s_waitcnt lgkmcnt(0)
	v_mfma_f32_16x16x32_bf16 v[122:125], v[130:133], v[170:173], v[122:125]
	v_mfma_f32_16x16x32_bf16 v[126:129], v[140:143], v[170:173], v[126:129]
	v_mfma_f32_16x16x32_bf16 v[118:121], v[130:133], v[178:181], v[118:121]
	v_mfma_f32_16x16x32_bf16 v[114:117], v[140:143], v[178:181], v[114:117]
	v_mfma_f32_16x16x32_bf16 v[102:105], v[130:133], v[186:189], v[102:105]
	v_mfma_f32_16x16x32_bf16 v[98:101], v[140:143], v[186:189], v[98:101]
	v_mfma_f32_16x16x32_bf16 v[86:89], v[130:133], v[198:201], v[86:89]
	v_mfma_f32_16x16x32_bf16 v[82:85], v[140:143], v[198:201], v[82:85]
	v_mfma_f32_16x16x32_bf16 v[122:125], v[134:137], v[174:177], v[122:125]
	v_mfma_f32_16x16x32_bf16 v[126:129], v[150:153], v[174:177], v[126:129]
	v_mfma_f32_16x16x32_bf16 v[118:121], v[134:137], v[182:185], v[118:121]
	v_mfma_f32_16x16x32_bf16 v[114:117], v[150:153], v[182:185], v[114:117]
	v_mfma_f32_16x16x32_bf16 v[102:105], v[134:137], v[194:197], v[102:105]
	v_mfma_f32_16x16x32_bf16 v[98:101], v[150:153], v[194:197], v[98:101]
	v_mfma_f32_16x16x32_bf16 v[86:89], v[134:137], v[202:205], v[86:89]
	v_mfma_f32_16x16x32_bf16 v[82:85], v[150:153], v[202:205], v[82:85]
	s_setprio 0
	s_setprio 1
	v_mfma_f32_16x16x32_bf16 v[58:61], v[154:157], v[170:173], v[58:61]
	v_mfma_f32_16x16x32_bf16 v[62:65], v[162:165], v[170:173], v[62:65]
	v_mfma_f32_16x16x32_bf16 v[54:57], v[154:157], v[178:181], v[54:57]
	v_mfma_f32_16x16x32_bf16 v[50:53], v[162:165], v[178:181], v[50:53]
	v_mfma_f32_16x16x32_bf16 v[38:41], v[154:157], v[186:189], v[38:41]
	v_mfma_f32_16x16x32_bf16 v[34:37], v[162:165], v[186:189], v[34:37]
	v_mfma_f32_16x16x32_bf16 v[14:17], v[154:157], v[198:201], v[14:17]
	v_mfma_f32_16x16x32_bf16 v[10:13], v[162:165], v[198:201], v[10:13]
	v_mfma_f32_16x16x32_bf16 v[58:61], v[158:161], v[174:177], v[58:61]
	v_mfma_f32_16x16x32_bf16 v[62:65], v[166:169], v[174:177], v[62:65]
	v_mfma_f32_16x16x32_bf16 v[54:57], v[158:161], v[182:185], v[54:57]
	v_mfma_f32_16x16x32_bf16 v[50:53], v[166:169], v[182:185], v[50:53]
	v_mfma_f32_16x16x32_bf16 v[38:41], v[158:161], v[194:197], v[38:41]
	v_mfma_f32_16x16x32_bf16 v[34:37], v[166:169], v[194:197], v[34:37]
	v_mfma_f32_16x16x32_bf16 v[14:17], v[158:161], v[202:205], v[14:17]
	v_mfma_f32_16x16x32_bf16 v[10:13], v[166:169], v[202:205], v[10:13]
	s_barrier
	s_setprio 0
	s_add_u32 s48, s54, 0x8000
	s_addc_u32 s49, s55, 0
	s_add_i32 s75, s75, s14
	s_mov_b32 m0, s75
	ds_read_b128 v[170:173], v149 offset:49152
	ds_read_b128 v[174:177], v149 offset:50176
	ds_read_b128 v[178:181], v149 offset:51200
	ds_read_b128 v[182:185], v149 offset:52224
	ds_read_b128 v[186:189], v149 offset:53248
	ds_read_b128 v[194:197], v149 offset:54272
	ds_read_b128 v[198:201], v149 offset:55296
	ds_read_b128 v[202:205], v149 offset:56320
	v_mov_b32_e32 v139, v1
	global_load_lds_dwordx4 v147, s[48:49]
	s_add_i32 m0, s75, 0x2000
	s_nop 0
	global_load_lds_dwordx4 v146, s[48:49]
	s_add_u32 s48, s54, 0xc000
	s_addc_u32 s49, s55, 0
	s_add_i32 s54, s76, s14
	s_mov_b32 m0, s54
	s_nop 0
	global_load_lds_dwordx4 v147, s[48:49]
	s_add_i32 m0, s54, 0x2000
	s_nop 0
	global_load_lds_dwordx4 v146, s[48:49]
	s_mov_b32 m0, s62
	v_lshl_add_u64 v[190:191], s[52:53], 0, v[0:1]
	v_lshl_add_u64 v[190:191], v[190:191], 0, s[16:17]
	global_load_lds_dwordx4 v[190:191], off
	s_mov_b32 m0, s63
	v_lshl_add_u64 v[190:191], s[52:53], 0, v[138:139]
	v_lshl_add_u64 v[190:191], v[190:191], 0, s[16:17]
	global_load_lds_dwordx4 v[190:191], off
	s_waitcnt vmcnt(8)
	s_waitcnt lgkmcnt(0)
	s_setprio 1
	s_barrier
	s_waitcnt lgkmcnt(0)
	v_mfma_f32_16x16x32_bf16 v[110:113], v[130:133], v[170:173], v[110:113]
	v_mfma_f32_16x16x32_bf16 v[106:109], v[140:143], v[170:173], v[106:109]
	v_mfma_f32_16x16x32_bf16 v[94:97], v[130:133], v[178:181], v[94:97]
	v_mfma_f32_16x16x32_bf16 v[90:93], v[140:143], v[178:181], v[90:93]
	v_mfma_f32_16x16x32_bf16 v[78:81], v[130:133], v[186:189], v[78:81]
	v_mfma_f32_16x16x32_bf16 v[74:77], v[140:143], v[186:189], v[74:77]
	v_mfma_f32_16x16x32_bf16 v[70:73], v[130:133], v[198:201], v[70:73]
	v_mfma_f32_16x16x32_bf16 v[66:69], v[140:143], v[198:201], v[66:69]
	v_mfma_f32_16x16x32_bf16 v[110:113], v[134:137], v[174:177], v[110:113]
	v_mfma_f32_16x16x32_bf16 v[106:109], v[150:153], v[174:177], v[106:109]
	v_mfma_f32_16x16x32_bf16 v[94:97], v[134:137], v[182:185], v[94:97]
	v_mfma_f32_16x16x32_bf16 v[90:93], v[150:153], v[182:185], v[90:93]
	v_mfma_f32_16x16x32_bf16 v[78:81], v[134:137], v[194:197], v[78:81]
	v_mfma_f32_16x16x32_bf16 v[74:77], v[150:153], v[194:197], v[74:77]
	v_mfma_f32_16x16x32_bf16 v[70:73], v[134:137], v[202:205], v[70:73]
	v_mfma_f32_16x16x32_bf16 v[66:69], v[150:153], v[202:205], v[66:69]
	s_setprio 0
	s_setprio 1
	v_mfma_f32_16x16x32_bf16 v[46:49], v[154:157], v[170:173], v[46:49]
	v_mfma_f32_16x16x32_bf16 v[42:45], v[162:165], v[170:173], v[42:45]
	v_mfma_f32_16x16x32_bf16 v[26:29], v[154:157], v[178:181], v[26:29]
	v_mfma_f32_16x16x32_bf16 v[22:25], v[162:165], v[178:181], v[22:25]
	v_mfma_f32_16x16x32_bf16 v[6:9], v[154:157], v[186:189], v[6:9]
	v_mfma_f32_16x16x32_bf16 v[2:5], v[162:165], v[186:189], v[2:5]
	v_mfma_f32_16x16x32_bf16 v[18:21], v[154:157], v[198:201], v[18:21]
	v_mfma_f32_16x16x32_bf16 v[30:33], v[162:165], v[198:201], v[30:33]
	v_mfma_f32_16x16x32_bf16 v[46:49], v[158:161], v[174:177], v[46:49]
	v_mfma_f32_16x16x32_bf16 v[42:45], v[166:169], v[174:177], v[42:45]
	v_mfma_f32_16x16x32_bf16 v[26:29], v[158:161], v[182:185], v[26:29]
	v_mfma_f32_16x16x32_bf16 v[22:25], v[166:169], v[182:185], v[22:25]
	v_mfma_f32_16x16x32_bf16 v[6:9], v[158:161], v[194:197], v[6:9]
	v_mfma_f32_16x16x32_bf16 v[2:5], v[166:169], v[194:197], v[2:5]
	v_mfma_f32_16x16x32_bf16 v[18:21], v[158:161], v[202:205], v[18:21]
	v_mfma_f32_16x16x32_bf16 v[30:33], v[166:169], v[202:205], v[30:33]
	s_barrier
	s_setprio 0
	s_add_u32 s72, s72, 0x10000
	s_addc_u32 s73, s73, 0
	s_cmp_ge_i32 s74, s59
	s_mov_b64 s[48:49], s[50:51]
	s_mov_b32 s52, s74
	s_cbranch_scc0 .LBB0_707

.LBB0_890:
	s_add_u32 s34, s26, 0x10000
	s_addc_u32 s35, s27, 0
	s_and_b64 s[30:31], s[48:49], exec
	s_cselect_b32 s47, s41, s35
	s_cselect_b32 s46, s40, s34
	s_add_u32 s65, s28, 0x10000
	s_addc_u32 s66, s29, 0
	s_add_u32 s30, s46, 0x8000
	s_addc_u32 s31, s47, 0
	s_add_i32 s67, 0, 0x10000
	s_and_b64 s[34:35], s[48:49], exec
	s_cselect_b32 s35, s45, s66
	s_cselect_b32 s34, s44, s65
	s_add_i32 s70, 0, 0x14000
	v_add_u32_e32 v114, s67, v236
	v_add_u32_e32 v115, s70, v236
	ds_read_b128 v[2:5], v114
	s_waitcnt lgkmcnt(0)
	ds_read_b128 v[6:9], v114 offset:1024
	ds_read_b128 v[10:13], v114 offset:2048
	ds_read_b128 v[14:17], v114 offset:3072
	ds_read_b128 v[18:21], v115
	ds_read_b128 v[22:25], v115 offset:1024
	ds_read_b128 v[26:29], v115 offset:2048
	ds_read_b128 v[30:33], v115 offset:3072
	s_add_u32 s68, s26, 0xc000
	s_addc_u32 s69, s27, 0
	s_add_i32 s65, s20, 0xc000
	s_mov_b32 m0, s65
	s_add_i32 s66, s20, 0xe000
	ds_read_b128 v[34:37], v237
	ds_read_b128 v[38:41], v237 offset:1024
	ds_read_b128 v[42:45], v237 offset:2048
	ds_read_b128 v[46:49], v237 offset:3072
	ds_read_b128 v[50:53], v237 offset:4096
	ds_read_b128 v[54:57], v237 offset:5120
	ds_read_b128 v[58:61], v237 offset:6144
	ds_read_b128 v[62:65], v237 offset:7168
	s_nop 0
	global_load_lds_dwordx4 v235, s[68:69]
	s_mov_b32 m0, s66
	s_nop 0
	global_load_lds_dwordx4 v226, s[68:69]
	s_waitcnt vmcnt(8)
	s_waitcnt lgkmcnt(0)
	s_setprio 1
	s_barrier
	s_waitcnt lgkmcnt(0)
	v_mfma_f32_16x16x32_bf16 v[90:93], v[2:5], v[58:61], 0
	v_mfma_f32_16x16x32_bf16 v[66:69], v[2:5], v[34:37], 0
	v_mfma_f32_16x16x32_bf16 v[70:73], v[10:13], v[34:37], 0
	v_mfma_f32_16x16x32_bf16 v[74:77], v[2:5], v[42:45], 0
	v_mfma_f32_16x16x32_bf16 v[78:81], v[10:13], v[42:45], 0
	v_mfma_f32_16x16x32_bf16 v[82:85], v[2:5], v[50:53], 0
	v_mfma_f32_16x16x32_bf16 v[86:89], v[10:13], v[50:53], 0
	v_mfma_f32_16x16x32_bf16 v[98:101], v[6:9], v[62:65], v[90:93]
	v_mfma_f32_16x16x32_bf16 v[90:93], v[10:13], v[58:61], 0
	v_mfma_f32_16x16x32_bf16 v[66:69], v[6:9], v[38:41], v[66:69]
	v_mfma_f32_16x16x32_bf16 v[70:73], v[14:17], v[38:41], v[70:73]
	v_mfma_f32_16x16x32_bf16 v[74:77], v[6:9], v[46:49], v[74:77]
	v_mfma_f32_16x16x32_bf16 v[78:81], v[14:17], v[46:49], v[78:81]
	v_mfma_f32_16x16x32_bf16 v[82:85], v[6:9], v[54:57], v[82:85]
	v_mfma_f32_16x16x32_bf16 v[86:89], v[14:17], v[54:57], v[86:89]
	v_mfma_f32_16x16x32_bf16 v[102:105], v[14:17], v[62:65], v[90:93]
	s_setprio 0
	s_setprio 1
	v_mfma_f32_16x16x32_bf16 v[90:93], v[18:21], v[34:37], 0
	v_mfma_f32_16x16x32_bf16 v[34:37], v[26:29], v[34:37], 0
	v_mfma_f32_16x16x32_bf16 v[118:121], v[22:25], v[38:41], v[90:93]
	v_mfma_f32_16x16x32_bf16 v[34:37], v[30:33], v[38:41], v[34:37]
	v_mfma_f32_16x16x32_bf16 v[38:41], v[18:21], v[42:45], 0
	v_mfma_f32_16x16x32_bf16 v[42:45], v[26:29], v[42:45], 0
	v_mfma_f32_16x16x32_bf16 v[38:41], v[22:25], v[46:49], v[38:41]
	v_mfma_f32_16x16x32_bf16 v[42:45], v[30:33], v[46:49], v[42:45]
	v_mfma_f32_16x16x32_bf16 v[46:49], v[18:21], v[50:53], 0
	v_mfma_f32_16x16x32_bf16 v[50:53], v[26:29], v[50:53], 0
	v_mfma_f32_16x16x32_bf16 v[46:49], v[22:25], v[54:57], v[46:49]
	v_mfma_f32_16x16x32_bf16 v[50:53], v[30:33], v[54:57], v[50:53]
	v_mfma_f32_16x16x32_bf16 v[54:57], v[18:21], v[58:61], 0
	v_mfma_f32_16x16x32_bf16 v[58:61], v[26:29], v[58:61], 0
	v_mfma_f32_16x16x32_bf16 v[54:57], v[22:25], v[62:65], v[54:57]
	v_mfma_f32_16x16x32_bf16 v[58:61], v[30:33], v[62:65], v[58:61]
	s_barrier
	s_setprio 0
	s_add_i32 s67, s67, s18
	s_add_i32 s68, s67, 0x2000
	s_mov_b32 m0, s67
	s_add_u32 s72, s34, 0x4000
	ds_read_b128 v[62:65], v237 offset:16384
	ds_read_b128 v[90:93], v237 offset:17408
	ds_read_b128 v[94:97], v237 offset:18432
	ds_read_b128 v[106:109], v237 offset:19456
	ds_read_b128 v[110:113], v237 offset:20480
	ds_read_b128 v[122:125], v237 offset:21504
	ds_read_b128 v[126:129], v237 offset:22528
	ds_read_b128 v[130:133], v237 offset:23552
	s_addc_u32 s73, s35, 0
	global_load_lds_dwordx4 v227, s[34:35]
	s_mov_b32 m0, s68
	s_add_i32 s69, s70, s18
	s_add_i32 s70, s69, 0x2000
	global_load_lds_dwordx4 v0, s[34:35]
	s_mov_b32 m0, s69
	s_nop 0
	global_load_lds_dwordx4 v227, s[72:73]
	s_mov_b32 m0, s70
	s_nop 0
	global_load_lds_dwordx4 v0, s[72:73]
	s_mov_b32 m0, s20
	s_nop 0
	global_load_lds_dwordx4 v235, s[46:47]
	s_mov_b32 m0, s25
	s_nop 0
	global_load_lds_dwordx4 v226, s[46:47]
	s_waitcnt vmcnt(8)
	s_waitcnt lgkmcnt(0)
	s_setprio 1
	s_barrier
	s_waitcnt lgkmcnt(0)
	v_mfma_f32_16x16x32_bf16 v[134:137], v[2:5], v[62:65], 0
	v_mfma_f32_16x16x32_bf16 v[142:145], v[2:5], v[94:97], 0
	v_mfma_f32_16x16x32_bf16 v[150:153], v[2:5], v[110:113], 0
	v_mfma_f32_16x16x32_bf16 v[2:5], v[2:5], v[126:129], 0
	v_mfma_f32_16x16x32_bf16 v[134:137], v[6:9], v[90:93], v[134:137]
	v_mfma_f32_16x16x32_bf16 v[142:145], v[6:9], v[106:109], v[142:145]
	v_mfma_f32_16x16x32_bf16 v[150:153], v[6:9], v[122:125], v[150:153]
	v_mfma_f32_16x16x32_bf16 v[2:5], v[6:9], v[130:133], v[2:5]
	v_mfma_f32_16x16x32_bf16 v[6:9], v[10:13], v[126:129], 0
	v_mfma_f32_16x16x32_bf16 v[138:141], v[10:13], v[62:65], 0
	v_mfma_f32_16x16x32_bf16 v[146:149], v[10:13], v[94:97], 0
	v_mfma_f32_16x16x32_bf16 v[154:157], v[10:13], v[110:113], 0
	v_mfma_f32_16x16x32_bf16 v[6:9], v[14:17], v[130:133], v[6:9]
	v_mfma_f32_16x16x32_bf16 v[138:141], v[14:17], v[90:93], v[138:141]
	v_mfma_f32_16x16x32_bf16 v[146:149], v[14:17], v[106:109], v[146:149]
	v_mfma_f32_16x16x32_bf16 v[154:157], v[14:17], v[122:125], v[154:157]
	s_setprio 0
	s_setprio 1
	v_mfma_f32_16x16x32_bf16 v[10:13], v[18:21], v[62:65], 0
	v_mfma_f32_16x16x32_bf16 v[158:161], v[22:25], v[90:93], v[10:13]
	v_mfma_f32_16x16x32_bf16 v[10:13], v[26:29], v[62:65], 0
	v_mfma_f32_16x16x32_bf16 v[162:165], v[30:33], v[90:93], v[10:13]
	v_mfma_f32_16x16x32_bf16 v[10:13], v[18:21], v[94:97], 0
	v_mfma_f32_16x16x32_bf16 v[174:177], v[22:25], v[106:109], v[10:13]
	v_mfma_f32_16x16x32_bf16 v[10:13], v[26:29], v[94:97], 0
	v_mfma_f32_16x16x32_bf16 v[178:181], v[30:33], v[106:109], v[10:13]
	v_mfma_f32_16x16x32_bf16 v[10:13], v[18:21], v[110:113], 0
	v_mfma_f32_16x16x32_bf16 v[182:185], v[22:25], v[122:125], v[10:13]
	v_mfma_f32_16x16x32_bf16 v[10:13], v[26:29], v[110:113], 0
	v_mfma_f32_16x16x32_bf16 v[122:125], v[30:33], v[122:125], v[10:13]
	v_mfma_f32_16x16x32_bf16 v[10:13], v[18:21], v[126:129], 0
	v_mfma_f32_16x16x32_bf16 v[186:189], v[22:25], v[130:133], v[10:13]
	v_mfma_f32_16x16x32_bf16 v[10:13], v[26:29], v[126:129], 0
	v_mfma_f32_16x16x32_bf16 v[130:133], v[30:33], v[130:133], v[10:13]
	s_barrier
	s_setprio 0
	s_add_i32 s71, 0, 0x18000
	s_add_i32 s74, 0, 0x1c000
	v_add_u32_e32 v116, s71, v236
	v_add_u32_e32 v117, s74, v236
	s_nop 0
	ds_read_b128 v[10:13], v116
	ds_read_b128 v[14:17], v116 offset:1024
	ds_read_b128 v[18:21], v116 offset:2048
	ds_read_b128 v[22:25], v116 offset:3072
	ds_read_b128 v[194:197], v117
	ds_read_b128 v[198:201], v117 offset:1024
	ds_read_b128 v[202:205], v117 offset:2048
	ds_read_b128 v[206:209], v117 offset:3072
	s_add_u32 s46, s46, 0x4000
	s_addc_u32 s47, s47, 0
	s_mov_b32 m0, s54
	ds_read_b128 v[26:29], v237 offset:32768
	ds_read_b128 v[30:33], v237 offset:33792
	ds_read_b128 v[62:65], v237 offset:34816
	ds_read_b128 v[210:213], v237 offset:35840
	ds_read_b128 v[214:217], v237 offset:36864
	ds_read_b128 v[218:221], v237 offset:37888
	ds_read_b128 v[222:225], v237 offset:38912
	ds_read_b128 v[238:241], v237 offset:39936
	s_nop 0
	global_load_lds_dwordx4 v235, s[46:47]
	s_mov_b32 m0, s55
	s_nop 0
	global_load_lds_dwordx4 v226, s[46:47]
	s_waitcnt vmcnt(8)
	s_waitcnt lgkmcnt(0)
	s_setprio 1
	s_barrier
	s_waitcnt lgkmcnt(0)
	v_mfma_f32_16x16x32_bf16 v[66:69], v[10:13], v[26:29], v[66:69]
	v_mfma_f32_16x16x32_bf16 v[166:169], v[14:17], v[30:33], v[66:69]
	v_mfma_f32_16x16x32_bf16 v[66:69], v[18:21], v[26:29], v[70:73]
	v_mfma_f32_16x16x32_bf16 v[170:173], v[22:25], v[30:33], v[66:69]
	v_mfma_f32_16x16x32_bf16 v[66:69], v[10:13], v[62:65], v[74:77]
	v_mfma_f32_16x16x32_bf16 v[110:113], v[14:17], v[210:213], v[66:69]
	v_mfma_f32_16x16x32_bf16 v[66:69], v[18:21], v[62:65], v[78:81]
	v_mfma_f32_16x16x32_bf16 v[106:109], v[22:25], v[210:213], v[66:69]
	v_mfma_f32_16x16x32_bf16 v[66:69], v[10:13], v[214:217], v[82:85]
	v_mfma_f32_16x16x32_bf16 v[94:97], v[14:17], v[218:221], v[66:69]
	v_mfma_f32_16x16x32_bf16 v[66:69], v[18:21], v[214:217], v[86:89]
	v_mfma_f32_16x16x32_bf16 v[90:93], v[22:25], v[218:221], v[66:69]
	v_mfma_f32_16x16x32_bf16 v[66:69], v[10:13], v[222:225], v[98:101]
	v_mfma_f32_16x16x32_bf16 v[78:81], v[14:17], v[238:241], v[66:69]
	v_mfma_f32_16x16x32_bf16 v[66:69], v[18:21], v[222:225], v[102:105]
	v_mfma_f32_16x16x32_bf16 v[70:73], v[22:25], v[238:241], v[66:69]
	s_setprio 0
	s_setprio 1
	v_mfma_f32_16x16x32_bf16 v[66:69], v[194:197], v[26:29], v[118:121]
	v_mfma_f32_16x16x32_bf16 v[26:29], v[202:205], v[26:29], v[34:37]
	v_mfma_f32_16x16x32_bf16 v[118:121], v[206:209], v[30:33], v[26:29]
	v_mfma_f32_16x16x32_bf16 v[26:29], v[194:197], v[62:65], v[38:41]
	v_mfma_f32_16x16x32_bf16 v[102:105], v[198:201], v[210:213], v[26:29]
	v_mfma_f32_16x16x32_bf16 v[26:29], v[202:205], v[62:65], v[42:45]
	v_mfma_f32_16x16x32_bf16 v[98:101], v[206:209], v[210:213], v[26:29]
	v_mfma_f32_16x16x32_bf16 v[26:29], v[194:197], v[214:217], v[46:49]
	v_mfma_f32_16x16x32_bf16 v[86:89], v[198:201], v[218:221], v[26:29]
	v_mfma_f32_16x16x32_bf16 v[26:29], v[202:205], v[214:217], v[50:53]
	v_mfma_f32_16x16x32_bf16 v[82:85], v[206:209], v[218:221], v[26:29]
	v_mfma_f32_16x16x32_bf16 v[26:29], v[194:197], v[222:225], v[54:57]
	v_mfma_f32_16x16x32_bf16 v[62:65], v[198:201], v[238:241], v[26:29]
	v_mfma_f32_16x16x32_bf16 v[26:29], v[202:205], v[222:225], v[58:61]
	v_mfma_f32_16x16x32_bf16 v[126:129], v[198:201], v[30:33], v[66:69]
	v_mfma_f32_16x16x32_bf16 v[54:57], v[206:209], v[238:241], v[26:29]
	s_barrier
	s_setprio 0
	s_add_u32 s72, s34, 0x8000
	s_addc_u32 s73, s35, 0
	s_add_i32 s46, s71, s18
	s_add_i32 s47, s46, 0x2000
	s_mov_b32 m0, s46
	s_add_u32 s34, s34, 0xc000
	ds_read_b128 v[34:37], v237 offset:49152
	ds_read_b128 v[38:41], v237 offset:50176
	ds_read_b128 v[210:213], v237 offset:51200
	ds_read_b128 v[214:217], v237 offset:52224
	ds_read_b128 v[218:221], v237 offset:53248
	ds_read_b128 v[222:225], v237 offset:54272
	ds_read_b128 v[238:241], v237 offset:55296
	ds_read_b128 v[242:245], v237 offset:56320
	s_addc_u32 s35, s35, 0
	global_load_lds_dwordx4 v227, s[72:73]
	s_mov_b32 m0, s47
	s_add_i32 s71, s74, s18
	s_nop 0
	global_load_lds_dwordx4 v0, s[72:73]
	s_mov_b32 m0, s71
	s_add_i32 s72, s71, 0x2000
	s_nop 0
	global_load_lds_dwordx4 v227, s[34:35]
	s_mov_b32 m0, s72
	s_nop 0
	global_load_lds_dwordx4 v0, s[34:35]
	s_mov_b32 m0, s58
	s_nop 0
	global_load_lds_dwordx4 v235, s[30:31]
	s_mov_b32 m0, s59
	s_nop 0
	global_load_lds_dwordx4 v226, s[30:31]
	s_waitcnt vmcnt(8)
	s_waitcnt lgkmcnt(0)
	s_setprio 1
	s_barrier
	s_waitcnt lgkmcnt(0)
	v_mfma_f32_16x16x32_bf16 v[26:29], v[10:13], v[34:37], v[134:137]
	v_mfma_f32_16x16x32_bf16 v[74:77], v[14:17], v[38:41], v[26:29]
	v_mfma_f32_16x16x32_bf16 v[26:29], v[18:21], v[34:37], v[138:141]
	v_mfma_f32_16x16x32_bf16 v[66:69], v[22:25], v[38:41], v[26:29]
	v_mfma_f32_16x16x32_bf16 v[26:29], v[10:13], v[210:213], v[142:145]
	v_mfma_f32_16x16x32_bf16 v[46:49], v[14:17], v[214:217], v[26:29]
	v_mfma_f32_16x16x32_bf16 v[26:29], v[18:21], v[210:213], v[146:149]
	v_mfma_f32_16x16x32_bf16 v[42:45], v[22:25], v[214:217], v[26:29]
	v_mfma_f32_16x16x32_bf16 v[26:29], v[10:13], v[218:221], v[150:153]
	v_mfma_f32_16x16x32_bf16 v[2:5], v[10:13], v[238:241], v[2:5]
	v_mfma_f32_16x16x32_bf16 v[30:33], v[14:17], v[222:225], v[26:29]
	v_mfma_f32_16x16x32_bf16 v[26:29], v[18:21], v[218:221], v[154:157]
	v_mfma_f32_16x16x32_bf16 v[14:17], v[14:17], v[242:245], v[2:5]
	v_mfma_f32_16x16x32_bf16 v[2:5], v[18:21], v[238:241], v[6:9]
	v_mfma_f32_16x16x32_bf16 v[26:29], v[22:25], v[222:225], v[26:29]
	v_mfma_f32_16x16x32_bf16 v[10:13], v[22:25], v[242:245], v[2:5]
	s_setprio 0
	s_setprio 1
	v_mfma_f32_16x16x32_bf16 v[2:5], v[194:197], v[34:37], v[158:161]
	v_mfma_f32_16x16x32_bf16 v[58:61], v[198:201], v[38:41], v[2:5]
	v_mfma_f32_16x16x32_bf16 v[2:5], v[202:205], v[34:37], v[162:165]
	v_mfma_f32_16x16x32_bf16 v[50:53], v[206:209], v[38:41], v[2:5]
	v_mfma_f32_16x16x32_bf16 v[2:5], v[194:197], v[210:213], v[174:177]
	v_mfma_f32_16x16x32_bf16 v[38:41], v[198:201], v[214:217], v[2:5]
	v_mfma_f32_16x16x32_bf16 v[2:5], v[202:205], v[210:213], v[178:181]
	v_mfma_f32_16x16x32_bf16 v[34:37], v[206:209], v[214:217], v[2:5]
	v_mfma_f32_16x16x32_bf16 v[2:5], v[194:197], v[218:221], v[182:185]
	v_mfma_f32_16x16x32_bf16 v[22:25], v[198:201], v[222:225], v[2:5]
	v_mfma_f32_16x16x32_bf16 v[2:5], v[202:205], v[218:221], v[122:125]
	v_mfma_f32_16x16x32_bf16 v[18:21], v[206:209], v[222:225], v[2:5]
	v_mfma_f32_16x16x32_bf16 v[2:5], v[194:197], v[238:241], v[186:189]
	v_mfma_f32_16x16x32_bf16 v[6:9], v[198:201], v[242:245], v[2:5]
	v_mfma_f32_16x16x32_bf16 v[2:5], v[202:205], v[238:241], v[130:133]
	v_mfma_f32_16x16x32_bf16 v[2:5], v[206:209], v[242:245], v[2:5]
	s_barrier
	s_setprio 0
	s_andn2_b64 vcc, exec, s[50:51]
	s_cbranch_vccnz .LBB0_893
	s_add_u32 s73, s28, 0x20000
	s_addc_u32 s74, s29, 0
	s_add_u32 s26, s26, 0x1c000
	s_addc_u32 s27, s27, 0
	s_mov_b32 s75, 4
.LBB0_892:
	ds_read_b128 v[122:125], v114
	ds_read_b128 v[130:133], v114 offset:1024
	ds_read_b128 v[134:137], v114 offset:2048
	ds_read_b128 v[138:141], v114 offset:3072
	ds_read_b128 v[142:145], v115
	ds_read_b128 v[146:149], v115 offset:1024
	ds_read_b128 v[150:153], v115 offset:2048
	ds_read_b128 v[154:157], v115 offset:3072
	s_add_u32 s28, s26, 0x4000
	s_addc_u32 s29, s27, 0
	s_cmp_eq_u32 s56, s75
	s_cselect_b32 s34, s40, s28
	s_cselect_b32 s35, s41, s29
	s_cselect_b32 s30, s44, s73
	s_cselect_b32 s31, s45, s74
	s_add_u32 s28, s34, 0x8000
	s_addc_u32 s29, s35, 0
	s_mov_b32 m0, s65
	ds_read_b128 v[158:161], v237
	ds_read_b128 v[162:165], v237 offset:1024
	ds_read_b128 v[174:177], v237 offset:2048
	ds_read_b128 v[178:181], v237 offset:3072
	ds_read_b128 v[182:185], v237 offset:4096
	ds_read_b128 v[186:189], v237 offset:5120
	ds_read_b128 v[194:197], v237 offset:6144
	ds_read_b128 v[198:201], v237 offset:7168
	s_nop 0
	global_load_lds_dwordx4 v235, s[26:27]
	s_mov_b32 m0, s66
	s_nop 0
	global_load_lds_dwordx4 v226, s[26:27]
	s_waitcnt vmcnt(8)
	s_waitcnt lgkmcnt(0)
	s_setprio 1
	s_barrier
	s_waitcnt lgkmcnt(0)
	v_mfma_f32_16x16x32_bf16 v[166:169], v[122:125], v[158:161], v[166:169]
	v_mfma_f32_16x16x32_bf16 v[170:173], v[134:137], v[158:161], v[170:173]
	v_mfma_f32_16x16x32_bf16 v[110:113], v[122:125], v[174:177], v[110:113]
	v_mfma_f32_16x16x32_bf16 v[106:109], v[134:137], v[174:177], v[106:109]
	v_mfma_f32_16x16x32_bf16 v[94:97], v[122:125], v[182:185], v[94:97]
	v_mfma_f32_16x16x32_bf16 v[90:93], v[134:137], v[182:185], v[90:93]
	v_mfma_f32_16x16x32_bf16 v[78:81], v[122:125], v[194:197], v[78:81]
	v_mfma_f32_16x16x32_bf16 v[70:73], v[134:137], v[194:197], v[70:73]
	v_mfma_f32_16x16x32_bf16 v[166:169], v[130:133], v[162:165], v[166:169]
	v_mfma_f32_16x16x32_bf16 v[170:173], v[138:141], v[162:165], v[170:173]
	v_mfma_f32_16x16x32_bf16 v[110:113], v[130:133], v[178:181], v[110:113]
	v_mfma_f32_16x16x32_bf16 v[106:109], v[138:141], v[178:181], v[106:109]
	v_mfma_f32_16x16x32_bf16 v[94:97], v[130:133], v[186:189], v[94:97]
	v_mfma_f32_16x16x32_bf16 v[90:93], v[138:141], v[186:189], v[90:93]
	v_mfma_f32_16x16x32_bf16 v[78:81], v[130:133], v[198:201], v[78:81]
	v_mfma_f32_16x16x32_bf16 v[70:73], v[138:141], v[198:201], v[70:73]
	s_setprio 0
	s_setprio 1
	v_mfma_f32_16x16x32_bf16 v[126:129], v[142:145], v[158:161], v[126:129]
	v_mfma_f32_16x16x32_bf16 v[118:121], v[150:153], v[158:161], v[118:121]
	v_mfma_f32_16x16x32_bf16 v[102:105], v[142:145], v[174:177], v[102:105]
	v_mfma_f32_16x16x32_bf16 v[98:101], v[150:153], v[174:177], v[98:101]
	v_mfma_f32_16x16x32_bf16 v[86:89], v[142:145], v[182:185], v[86:89]
	v_mfma_f32_16x16x32_bf16 v[82:85], v[150:153], v[182:185], v[82:85]
	v_mfma_f32_16x16x32_bf16 v[62:65], v[142:145], v[194:197], v[62:65]
	v_mfma_f32_16x16x32_bf16 v[54:57], v[150:153], v[194:197], v[54:57]
	v_mfma_f32_16x16x32_bf16 v[126:129], v[146:149], v[162:165], v[126:129]
	v_mfma_f32_16x16x32_bf16 v[118:121], v[154:157], v[162:165], v[118:121]
	v_mfma_f32_16x16x32_bf16 v[102:105], v[146:149], v[178:181], v[102:105]
	v_mfma_f32_16x16x32_bf16 v[98:101], v[154:157], v[178:181], v[98:101]
	v_mfma_f32_16x16x32_bf16 v[86:89], v[146:149], v[186:189], v[86:89]
	v_mfma_f32_16x16x32_bf16 v[82:85], v[154:157], v[186:189], v[82:85]
	v_mfma_f32_16x16x32_bf16 v[62:65], v[146:149], v[198:201], v[62:65]
	v_mfma_f32_16x16x32_bf16 v[54:57], v[154:157], v[198:201], v[54:57]
	s_barrier
	s_setprio 0
	s_mov_b32 m0, s67
	ds_read_b128 v[158:161], v237 offset:16384
	ds_read_b128 v[162:165], v237 offset:17408
	ds_read_b128 v[174:177], v237 offset:18432
	ds_read_b128 v[178:181], v237 offset:19456
	ds_read_b128 v[182:185], v237 offset:20480
	ds_read_b128 v[186:189], v237 offset:21504
	ds_read_b128 v[194:197], v237 offset:22528
	ds_read_b128 v[198:201], v237 offset:23552
	s_add_u32 s76, s30, 0x4000
	global_load_lds_dwordx4 v227, s[30:31]
	s_mov_b32 m0, s68
	s_addc_u32 s77, s31, 0
	global_load_lds_dwordx4 v0, s[30:31]
	s_mov_b32 m0, s69
	s_nop 0
	global_load_lds_dwordx4 v227, s[76:77]
	s_mov_b32 m0, s70
	s_nop 0
	global_load_lds_dwordx4 v0, s[76:77]
	s_mov_b32 m0, s20
	s_nop 0
	global_load_lds_dwordx4 v235, s[34:35]
	s_mov_b32 m0, s25
	s_nop 0
	global_load_lds_dwordx4 v226, s[34:35]
	s_waitcnt vmcnt(8)
	s_waitcnt lgkmcnt(0)
	s_setprio 1
	s_barrier
	s_waitcnt lgkmcnt(0)
	v_mfma_f32_16x16x32_bf16 v[74:77], v[122:125], v[158:161], v[74:77]
	v_mfma_f32_16x16x32_bf16 v[66:69], v[134:137], v[158:161], v[66:69]
	v_mfma_f32_16x16x32_bf16 v[46:49], v[122:125], v[174:177], v[46:49]
	v_mfma_f32_16x16x32_bf16 v[42:45], v[134:137], v[174:177], v[42:45]
	v_mfma_f32_16x16x32_bf16 v[30:33], v[122:125], v[182:185], v[30:33]
	v_mfma_f32_16x16x32_bf16 v[26:29], v[134:137], v[182:185], v[26:29]
	v_mfma_f32_16x16x32_bf16 v[14:17], v[122:125], v[194:197], v[14:17]
	v_mfma_f32_16x16x32_bf16 v[10:13], v[134:137], v[194:197], v[10:13]
	v_mfma_f32_16x16x32_bf16 v[74:77], v[130:133], v[162:165], v[74:77]
	v_mfma_f32_16x16x32_bf16 v[66:69], v[138:141], v[162:165], v[66:69]
	v_mfma_f32_16x16x32_bf16 v[46:49], v[130:133], v[178:181], v[46:49]
	v_mfma_f32_16x16x32_bf16 v[42:45], v[138:141], v[178:181], v[42:45]
	v_mfma_f32_16x16x32_bf16 v[30:33], v[130:133], v[186:189], v[30:33]
	v_mfma_f32_16x16x32_bf16 v[26:29], v[138:141], v[186:189], v[26:29]
	v_mfma_f32_16x16x32_bf16 v[14:17], v[130:133], v[198:201], v[14:17]
	v_mfma_f32_16x16x32_bf16 v[10:13], v[138:141], v[198:201], v[10:13]
	s_setprio 0
	s_setprio 1
	v_mfma_f32_16x16x32_bf16 v[58:61], v[142:145], v[158:161], v[58:61]
	v_mfma_f32_16x16x32_bf16 v[50:53], v[150:153], v[158:161], v[50:53]
	v_mfma_f32_16x16x32_bf16 v[38:41], v[142:145], v[174:177], v[38:41]
	v_mfma_f32_16x16x32_bf16 v[34:37], v[150:153], v[174:177], v[34:37]
	v_mfma_f32_16x16x32_bf16 v[22:25], v[142:145], v[182:185], v[22:25]
	v_mfma_f32_16x16x32_bf16 v[18:21], v[150:153], v[182:185], v[18:21]
	v_mfma_f32_16x16x32_bf16 v[6:9], v[142:145], v[194:197], v[6:9]
	v_mfma_f32_16x16x32_bf16 v[2:5], v[150:153], v[194:197], v[2:5]
	v_mfma_f32_16x16x32_bf16 v[58:61], v[146:149], v[162:165], v[58:61]
	v_mfma_f32_16x16x32_bf16 v[50:53], v[154:157], v[162:165], v[50:53]
	v_mfma_f32_16x16x32_bf16 v[38:41], v[146:149], v[178:181], v[38:41]
	v_mfma_f32_16x16x32_bf16 v[34:37], v[154:157], v[178:181], v[34:37]
	v_mfma_f32_16x16x32_bf16 v[22:25], v[146:149], v[186:189], v[22:25]
	v_mfma_f32_16x16x32_bf16 v[18:21], v[154:157], v[186:189], v[18:21]
	v_mfma_f32_16x16x32_bf16 v[6:9], v[146:149], v[198:201], v[6:9]
	v_mfma_f32_16x16x32_bf16 v[2:5], v[154:157], v[198:201], v[2:5]
	s_barrier
	s_setprio 0
	ds_read_b128 v[122:125], v116
	ds_read_b128 v[130:133], v116 offset:1024
	ds_read_b128 v[134:137], v116 offset:2048
	ds_read_b128 v[138:141], v116 offset:3072
	ds_read_b128 v[142:145], v117
	ds_read_b128 v[146:149], v117 offset:1024
	ds_read_b128 v[150:153], v117 offset:2048
	ds_read_b128 v[154:157], v117 offset:3072
	s_add_u32 s34, s34, 0x4000
	s_addc_u32 s35, s35, 0
	s_mov_b32 m0, s54
	ds_read_b128 v[158:161], v237 offset:32768
	ds_read_b128 v[162:165], v237 offset:33792
	ds_read_b128 v[174:177], v237 offset:34816
	ds_read_b128 v[178:181], v237 offset:35840
	ds_read_b128 v[182:185], v237 offset:36864
	ds_read_b128 v[186:189], v237 offset:37888
	ds_read_b128 v[194:197], v237 offset:38912
	ds_read_b128 v[198:201], v237 offset:39936
	s_nop 0
	global_load_lds_dwordx4 v235, s[34:35]
	s_mov_b32 m0, s55
	s_nop 0
	global_load_lds_dwordx4 v226, s[34:35]
	s_waitcnt vmcnt(8)
	s_waitcnt lgkmcnt(0)
	s_setprio 1
	s_barrier
	s_waitcnt lgkmcnt(0)
	v_mfma_f32_16x16x32_bf16 v[166:169], v[122:125], v[158:161], v[166:169]
	v_mfma_f32_16x16x32_bf16 v[170:173], v[134:137], v[158:161], v[170:173]
	v_mfma_f32_16x16x32_bf16 v[110:113], v[122:125], v[174:177], v[110:113]
	v_mfma_f32_16x16x32_bf16 v[106:109], v[134:137], v[174:177], v[106:109]
	v_mfma_f32_16x16x32_bf16 v[94:97], v[122:125], v[182:185], v[94:97]
	v_mfma_f32_16x16x32_bf16 v[90:93], v[134:137], v[182:185], v[90:93]
	v_mfma_f32_16x16x32_bf16 v[78:81], v[122:125], v[194:197], v[78:81]
	v_mfma_f32_16x16x32_bf16 v[70:73], v[134:137], v[194:197], v[70:73]
	v_mfma_f32_16x16x32_bf16 v[166:169], v[130:133], v[162:165], v[166:169]
	v_mfma_f32_16x16x32_bf16 v[170:173], v[138:141], v[162:165], v[170:173]
	v_mfma_f32_16x16x32_bf16 v[110:113], v[130:133], v[178:181], v[110:113]
	v_mfma_f32_16x16x32_bf16 v[106:109], v[138:141], v[178:181], v[106:109]
	v_mfma_f32_16x16x32_bf16 v[94:97], v[130:133], v[186:189], v[94:97]
	v_mfma_f32_16x16x32_bf16 v[90:93], v[138:141], v[186:189], v[90:93]
	v_mfma_f32_16x16x32_bf16 v[78:81], v[130:133], v[198:201], v[78:81]
	v_mfma_f32_16x16x32_bf16 v[70:73], v[138:141], v[198:201], v[70:73]
	s_setprio 0
	s_setprio 1
	v_mfma_f32_16x16x32_bf16 v[126:129], v[142:145], v[158:161], v[126:129]
	v_mfma_f32_16x16x32_bf16 v[118:121], v[150:153], v[158:161], v[118:121]
	v_mfma_f32_16x16x32_bf16 v[102:105], v[142:145], v[174:177], v[102:105]
	v_mfma_f32_16x16x32_bf16 v[98:101], v[150:153], v[174:177], v[98:101]
	v_mfma_f32_16x16x32_bf16 v[86:89], v[142:145], v[182:185], v[86:89]
	v_mfma_f32_16x16x32_bf16 v[82:85], v[150:153], v[182:185], v[82:85]
	v_mfma_f32_16x16x32_bf16 v[62:65], v[142:145], v[194:197], v[62:65]
	v_mfma_f32_16x16x32_bf16 v[54:57], v[150:153], v[194:197], v[54:57]
	v_mfma_f32_16x16x32_bf16 v[126:129], v[146:149], v[162:165], v[126:129]
	v_mfma_f32_16x16x32_bf16 v[118:121], v[154:157], v[162:165], v[118:121]
	v_mfma_f32_16x16x32_bf16 v[102:105], v[146:149], v[178:181], v[102:105]
	v_mfma_f32_16x16x32_bf16 v[98:101], v[154:157], v[178:181], v[98:101]
	v_mfma_f32_16x16x32_bf16 v[86:89], v[146:149], v[186:189], v[86:89]
	v_mfma_f32_16x16x32_bf16 v[82:85], v[154:157], v[186:189], v[82:85]
	v_mfma_f32_16x16x32_bf16 v[62:65], v[146:149], v[198:201], v[62:65]
	v_mfma_f32_16x16x32_bf16 v[54:57], v[154:157], v[198:201], v[54:57]
	s_barrier
	s_setprio 0
	s_add_u32 s34, s30, 0x8000
	s_mov_b32 m0, s46
	s_addc_u32 s35, s31, 0
	ds_read_b128 v[158:161], v237 offset:49152
	ds_read_b128 v[162:165], v237 offset:50176
	ds_read_b128 v[174:177], v237 offset:51200
	ds_read_b128 v[178:181], v237 offset:52224
	ds_read_b128 v[182:185], v237 offset:53248
	ds_read_b128 v[186:189], v237 offset:54272
	ds_read_b128 v[194:197], v237 offset:55296
	ds_read_b128 v[198:201], v237 offset:56320
	s_add_u32 s30, s30, 0xc000
	global_load_lds_dwordx4 v227, s[34:35]
	s_mov_b32 m0, s47
	s_addc_u32 s31, s31, 0
	global_load_lds_dwordx4 v0, s[34:35]
	s_mov_b32 m0, s71
	s_nop 0
	global_load_lds_dwordx4 v227, s[30:31]
	s_mov_b32 m0, s72
	s_nop 0
	global_load_lds_dwordx4 v0, s[30:31]
	s_mov_b32 m0, s58
	s_nop 0
	global_load_lds_dwordx4 v235, s[28:29]
	s_mov_b32 m0, s59
	s_nop 0
	global_load_lds_dwordx4 v226, s[28:29]
	s_waitcnt vmcnt(8)
	s_waitcnt lgkmcnt(0)
	s_setprio 1
	s_barrier
	s_waitcnt lgkmcnt(0)
	v_mfma_f32_16x16x32_bf16 v[74:77], v[122:125], v[158:161], v[74:77]
	v_mfma_f32_16x16x32_bf16 v[66:69], v[134:137], v[158:161], v[66:69]
	v_mfma_f32_16x16x32_bf16 v[46:49], v[122:125], v[174:177], v[46:49]
	v_mfma_f32_16x16x32_bf16 v[42:45], v[134:137], v[174:177], v[42:45]
	v_mfma_f32_16x16x32_bf16 v[30:33], v[122:125], v[182:185], v[30:33]
	v_mfma_f32_16x16x32_bf16 v[26:29], v[134:137], v[182:185], v[26:29]
	v_mfma_f32_16x16x32_bf16 v[14:17], v[122:125], v[194:197], v[14:17]
	v_mfma_f32_16x16x32_bf16 v[10:13], v[134:137], v[194:197], v[10:13]
	v_mfma_f32_16x16x32_bf16 v[74:77], v[130:133], v[162:165], v[74:77]
	v_mfma_f32_16x16x32_bf16 v[66:69], v[138:141], v[162:165], v[66:69]
	v_mfma_f32_16x16x32_bf16 v[46:49], v[130:133], v[178:181], v[46:49]
	v_mfma_f32_16x16x32_bf16 v[42:45], v[138:141], v[178:181], v[42:45]
	v_mfma_f32_16x16x32_bf16 v[30:33], v[130:133], v[186:189], v[30:33]
	v_mfma_f32_16x16x32_bf16 v[26:29], v[138:141], v[186:189], v[26:29]
	v_mfma_f32_16x16x32_bf16 v[14:17], v[130:133], v[198:201], v[14:17]
	v_mfma_f32_16x16x32_bf16 v[10:13], v[138:141], v[198:201], v[10:13]
	s_setprio 0
	s_setprio 1
	v_mfma_f32_16x16x32_bf16 v[58:61], v[142:145], v[158:161], v[58:61]
	v_mfma_f32_16x16x32_bf16 v[50:53], v[150:153], v[158:161], v[50:53]
	v_mfma_f32_16x16x32_bf16 v[38:41], v[142:145], v[174:177], v[38:41]
	v_mfma_f32_16x16x32_bf16 v[34:37], v[150:153], v[174:177], v[34:37]
	v_mfma_f32_16x16x32_bf16 v[22:25], v[142:145], v[182:185], v[22:25]
	v_mfma_f32_16x16x32_bf16 v[18:21], v[150:153], v[182:185], v[18:21]
	v_mfma_f32_16x16x32_bf16 v[6:9], v[142:145], v[194:197], v[6:9]
	v_mfma_f32_16x16x32_bf16 v[2:5], v[150:153], v[194:197], v[2:5]
	v_mfma_f32_16x16x32_bf16 v[58:61], v[146:149], v[162:165], v[58:61]
	v_mfma_f32_16x16x32_bf16 v[50:53], v[154:157], v[162:165], v[50:53]
	v_mfma_f32_16x16x32_bf16 v[38:41], v[146:149], v[178:181], v[38:41]
	v_mfma_f32_16x16x32_bf16 v[34:37], v[154:157], v[178:181], v[34:37]
	v_mfma_f32_16x16x32_bf16 v[22:25], v[146:149], v[186:189], v[22:25]
	v_mfma_f32_16x16x32_bf16 v[18:21], v[154:157], v[186:189], v[18:21]
	v_mfma_f32_16x16x32_bf16 v[6:9], v[146:149], v[198:201], v[6:9]
	v_mfma_f32_16x16x32_bf16 v[2:5], v[154:157], v[198:201], v[2:5]
	s_barrier
	s_setprio 0
	s_add_i32 s28, s75, 2
	s_add_u32 s73, s73, 0x10000
	s_addc_u32 s74, s74, 0
	s_add_u32 s26, s26, 0x10000
	s_addc_u32 s27, s27, 0
	s_cmp_lt_i32 s75, s56
	s_mov_b32 s75, s28
	s_cbranch_scc1 .LBB0_892

.LBB0_965:
	s_add_u32 s34, s28, 0x10000
	s_addc_u32 s35, s29, 0
	s_and_b64 s[30:31], s[48:49], exec
	s_cselect_b32 s57, s43, s35
	s_cselect_b32 s56, s42, s34
	s_add_u32 s58, s26, 0x100
	s_addc_u32 s59, s27, 0
	s_add_u32 s30, s56, 0x8000
	s_addc_u32 s31, s57, 0
	s_add_i32 s74, 0, 0x10000
	s_and_b64 s[34:35], s[48:49], exec
	s_cselect_b32 s35, s55, s59
	s_cselect_b32 s34, s54, s58
	s_add_i32 s76, 0, 0x14000
	v_add_u32_e32 v132, s74, v218
	v_add_u32_e32 v133, s76, v218
	ds_read_b128 v[2:5], v132
	ds_read_b128 v[6:9], v132 offset:1024
	ds_read_b128 v[10:13], v132 offset:2048
	ds_read_b128 v[14:17], v132 offset:3072
	ds_read_b128 v[18:21], v133
	ds_read_b128 v[22:25], v133 offset:1024
	ds_read_b128 v[26:29], v133 offset:2048
	ds_read_b128 v[30:33], v133 offset:3072
	s_add_u32 s58, s28, 0xc000
	s_addc_u32 s59, s29, 0
	s_add_i32 s72, s18, 0xc000
	s_mov_b32 m0, s72
	s_add_i32 s73, s18, 0xe000
	ds_read_b128 v[34:37], v219
	ds_read_b128 v[38:41], v219 offset:1024
	ds_read_b128 v[42:45], v219 offset:2048
	ds_read_b128 v[46:49], v219 offset:3072
	ds_read_b128 v[50:53], v219 offset:4096
	ds_read_b128 v[54:57], v219 offset:5120
	ds_read_b128 v[58:61], v219 offset:6144
	ds_read_b128 v[62:65], v219 offset:7168
	s_nop 0
	global_load_lds_dwordx4 v217, s[58:59]
	s_mov_b32 m0, s73
	s_nop 0
	global_load_lds_dwordx4 v216, s[58:59]
	s_waitcnt vmcnt(8)
	s_waitcnt lgkmcnt(0)
	s_setprio 1
	s_barrier
	s_waitcnt lgkmcnt(0)
	v_mfma_f32_16x16x32_bf16 v[86:89], v[10:13], v[50:53], 0
	v_mfma_f32_16x16x32_bf16 v[90:93], v[14:17], v[54:57], v[86:89]
	v_mfma_f32_16x16x32_bf16 v[86:89], v[2:5], v[58:61], 0
	v_mfma_f32_16x16x32_bf16 v[66:69], v[2:5], v[34:37], 0
	v_mfma_f32_16x16x32_bf16 v[70:73], v[10:13], v[34:37], 0
	v_mfma_f32_16x16x32_bf16 v[74:77], v[2:5], v[42:45], 0
	v_mfma_f32_16x16x32_bf16 v[78:81], v[10:13], v[42:45], 0
	v_mfma_f32_16x16x32_bf16 v[82:85], v[2:5], v[50:53], 0
	v_mfma_f32_16x16x32_bf16 v[94:97], v[6:9], v[62:65], v[86:89]
	v_mfma_f32_16x16x32_bf16 v[86:89], v[10:13], v[58:61], 0
	v_mfma_f32_16x16x32_bf16 v[66:69], v[6:9], v[38:41], v[66:69]
	v_mfma_f32_16x16x32_bf16 v[70:73], v[14:17], v[38:41], v[70:73]
	v_mfma_f32_16x16x32_bf16 v[74:77], v[6:9], v[46:49], v[74:77]
	v_mfma_f32_16x16x32_bf16 v[78:81], v[14:17], v[46:49], v[78:81]
	v_mfma_f32_16x16x32_bf16 v[82:85], v[6:9], v[54:57], v[82:85]
	v_mfma_f32_16x16x32_bf16 v[106:109], v[14:17], v[62:65], v[86:89]
	s_setprio 0
	s_setprio 1
	v_mfma_f32_16x16x32_bf16 v[86:89], v[18:21], v[34:37], 0
	v_mfma_f32_16x16x32_bf16 v[34:37], v[26:29], v[34:37], 0
	v_mfma_f32_16x16x32_bf16 v[110:113], v[22:25], v[38:41], v[86:89]
	v_mfma_f32_16x16x32_bf16 v[34:37], v[30:33], v[38:41], v[34:37]
	v_mfma_f32_16x16x32_bf16 v[38:41], v[18:21], v[42:45], 0
	v_mfma_f32_16x16x32_bf16 v[42:45], v[26:29], v[42:45], 0
	v_mfma_f32_16x16x32_bf16 v[38:41], v[22:25], v[46:49], v[38:41]
	v_mfma_f32_16x16x32_bf16 v[42:45], v[30:33], v[46:49], v[42:45]
	v_mfma_f32_16x16x32_bf16 v[46:49], v[18:21], v[50:53], 0
	v_mfma_f32_16x16x32_bf16 v[50:53], v[26:29], v[50:53], 0
	v_mfma_f32_16x16x32_bf16 v[136:139], v[30:33], v[54:57], v[50:53]
	v_mfma_f32_16x16x32_bf16 v[50:53], v[18:21], v[58:61], 0
	v_mfma_f32_16x16x32_bf16 v[140:143], v[22:25], v[62:65], v[50:53]
	v_mfma_f32_16x16x32_bf16 v[50:53], v[26:29], v[58:61], 0
	v_mfma_f32_16x16x32_bf16 v[46:49], v[22:25], v[54:57], v[46:49]
	v_mfma_f32_16x16x32_bf16 v[58:61], v[30:33], v[62:65], v[50:53]
	s_barrier
	s_setprio 0
	s_add_i32 s74, s74, s15
	s_add_i32 s75, s74, 0x2000
	s_mov_b32 m0, s74
	s_add_u32 s58, s34, s36
	ds_read_b128 v[50:53], v219 offset:16384
	ds_read_b128 v[54:57], v219 offset:17408
	ds_read_b128 v[62:65], v219 offset:18432
	ds_read_b128 v[86:89], v219 offset:19456
	ds_read_b128 v[98:101], v219 offset:20480
	ds_read_b128 v[102:105], v219 offset:21504
	ds_read_b128 v[114:117], v219 offset:22528
	ds_read_b128 v[118:121], v219 offset:23552
	s_addc_u32 s59, s35, s37
	global_load_lds_dwordx4 v0, s[34:35]
	s_mov_b32 m0, s75
	s_add_i32 s76, s76, s15
	s_add_i32 s77, s76, 0x2000
	global_load_lds_dwordx4 v130, s[34:35]
	s_mov_b32 m0, s76
	s_nop 0
	global_load_lds_dwordx4 v0, s[58:59]
	s_mov_b32 m0, s77
	s_nop 0
	global_load_lds_dwordx4 v130, s[58:59]
	s_mov_b32 m0, s18
	s_nop 0
	global_load_lds_dwordx4 v217, s[56:57]
	s_mov_b32 m0, s20
	s_nop 0
	global_load_lds_dwordx4 v216, s[56:57]
	s_waitcnt vmcnt(8)
	s_waitcnt lgkmcnt(0)
	s_setprio 1
	s_barrier
	s_waitcnt lgkmcnt(0)
	v_mfma_f32_16x16x32_bf16 v[122:125], v[2:5], v[50:53], 0
	v_mfma_f32_16x16x32_bf16 v[144:147], v[6:9], v[54:57], v[122:125]
	v_mfma_f32_16x16x32_bf16 v[122:125], v[10:13], v[50:53], 0
	v_mfma_f32_16x16x32_bf16 v[148:151], v[14:17], v[54:57], v[122:125]
	v_mfma_f32_16x16x32_bf16 v[122:125], v[2:5], v[62:65], 0
	v_mfma_f32_16x16x32_bf16 v[152:155], v[6:9], v[86:89], v[122:125]
	v_mfma_f32_16x16x32_bf16 v[122:125], v[10:13], v[62:65], 0
	v_mfma_f32_16x16x32_bf16 v[156:159], v[14:17], v[86:89], v[122:125]
	v_mfma_f32_16x16x32_bf16 v[122:125], v[2:5], v[98:101], 0
	v_mfma_f32_16x16x32_bf16 v[2:5], v[2:5], v[114:117], 0
	v_mfma_f32_16x16x32_bf16 v[160:163], v[6:9], v[102:105], v[122:125]
	v_mfma_f32_16x16x32_bf16 v[2:5], v[6:9], v[118:121], v[2:5]
	v_mfma_f32_16x16x32_bf16 v[6:9], v[10:13], v[114:117], 0
	v_mfma_f32_16x16x32_bf16 v[122:125], v[10:13], v[98:101], 0
	v_mfma_f32_16x16x32_bf16 v[10:13], v[14:17], v[118:121], v[6:9]
	v_mfma_f32_16x16x32_bf16 v[164:167], v[14:17], v[102:105], v[122:125]
	s_setprio 0
	s_setprio 1
	v_mfma_f32_16x16x32_bf16 v[6:9], v[18:21], v[50:53], 0
	v_mfma_f32_16x16x32_bf16 v[14:17], v[22:25], v[54:57], v[6:9]
	v_mfma_f32_16x16x32_bf16 v[6:9], v[26:29], v[50:53], 0
	v_mfma_f32_16x16x32_bf16 v[168:171], v[30:33], v[54:57], v[6:9]
	v_mfma_f32_16x16x32_bf16 v[6:9], v[18:21], v[62:65], 0
	v_mfma_f32_16x16x32_bf16 v[172:175], v[22:25], v[86:89], v[6:9]
	v_mfma_f32_16x16x32_bf16 v[6:9], v[26:29], v[62:65], 0
	v_mfma_f32_16x16x32_bf16 v[176:179], v[30:33], v[86:89], v[6:9]
	v_mfma_f32_16x16x32_bf16 v[6:9], v[18:21], v[98:101], 0
	v_mfma_f32_16x16x32_bf16 v[180:183], v[22:25], v[102:105], v[6:9]
	v_mfma_f32_16x16x32_bf16 v[6:9], v[26:29], v[98:101], 0
	v_mfma_f32_16x16x32_bf16 v[184:187], v[30:33], v[102:105], v[6:9]
	v_mfma_f32_16x16x32_bf16 v[6:9], v[18:21], v[114:117], 0
	v_mfma_f32_16x16x32_bf16 v[188:191], v[22:25], v[118:121], v[6:9]
	v_mfma_f32_16x16x32_bf16 v[6:9], v[26:29], v[114:117], 0
	v_mfma_f32_16x16x32_bf16 v[194:197], v[30:33], v[118:121], v[6:9]
	s_barrier
	s_setprio 0
	s_add_i32 s78, 0, 0x18000
	s_add_i32 s80, 0, 0x1c000
	v_add_u32_e32 v134, s78, v218
	v_add_u32_e32 v135, s80, v218
	s_nop 0
	ds_read_b128 v[6:9], v134
	ds_read_b128 v[26:29], v134 offset:1024
	ds_read_b128 v[30:33], v134 offset:2048
	ds_read_b128 v[198:201], v134 offset:3072
	ds_read_b128 v[202:205], v135
	ds_read_b128 v[206:209], v135 offset:1024
	ds_read_b128 v[210:213], v135 offset:2048
	ds_read_b128 v[220:223], v135 offset:3072
	s_add_u32 s56, s56, 0x4000
	s_addc_u32 s57, s57, 0
	s_mov_b32 m0, s25
	ds_read_b128 v[18:21], v219 offset:32768
	ds_read_b128 v[22:25], v219 offset:33792
	ds_read_b128 v[62:65], v219 offset:34816
	ds_read_b128 v[224:227], v219 offset:35840
	ds_read_b128 v[232:235], v219 offset:36864
	ds_read_b128 v[236:239], v219 offset:37888
	ds_read_b128 v[240:243], v219 offset:38912
	ds_read_b128 v[244:247], v219 offset:39936
	s_nop 0
	global_load_lds_dwordx4 v217, s[56:57]
	s_mov_b32 m0, s60
	s_nop 0
	global_load_lds_dwordx4 v216, s[56:57]
	s_waitcnt vmcnt(8)
	s_waitcnt lgkmcnt(0)
	s_setprio 1
	s_barrier
	s_waitcnt lgkmcnt(0)
	v_mfma_f32_16x16x32_bf16 v[50:53], v[6:9], v[18:21], v[66:69]
	v_mfma_f32_16x16x32_bf16 v[126:129], v[26:29], v[22:25], v[50:53]
	v_mfma_f32_16x16x32_bf16 v[50:53], v[30:33], v[18:21], v[70:73]
	v_mfma_f32_16x16x32_bf16 v[122:125], v[198:201], v[22:25], v[50:53]
	v_mfma_f32_16x16x32_bf16 v[50:53], v[6:9], v[62:65], v[74:77]
	v_mfma_f32_16x16x32_bf16 v[102:105], v[26:29], v[224:227], v[50:53]
	v_mfma_f32_16x16x32_bf16 v[50:53], v[30:33], v[62:65], v[78:81]
	v_mfma_f32_16x16x32_bf16 v[98:101], v[198:201], v[224:227], v[50:53]
	v_mfma_f32_16x16x32_bf16 v[50:53], v[6:9], v[232:235], v[82:85]
	v_mfma_f32_16x16x32_bf16 v[86:89], v[26:29], v[236:239], v[50:53]
	v_mfma_f32_16x16x32_bf16 v[50:53], v[30:33], v[232:235], v[90:93]
	v_mfma_f32_16x16x32_bf16 v[82:85], v[198:201], v[236:239], v[50:53]
	v_mfma_f32_16x16x32_bf16 v[50:53], v[6:9], v[240:243], v[94:97]
	v_mfma_f32_16x16x32_bf16 v[54:57], v[26:29], v[244:247], v[50:53]
	v_mfma_f32_16x16x32_bf16 v[50:53], v[30:33], v[240:243], v[106:109]
	v_mfma_f32_16x16x32_bf16 v[50:53], v[198:201], v[244:247], v[50:53]
	s_setprio 0
	s_setprio 1
	v_mfma_f32_16x16x32_bf16 v[66:69], v[202:205], v[18:21], v[110:113]
	v_mfma_f32_16x16x32_bf16 v[18:21], v[210:213], v[18:21], v[34:37]
	v_mfma_f32_16x16x32_bf16 v[114:117], v[220:223], v[22:25], v[18:21]
	v_mfma_f32_16x16x32_bf16 v[18:21], v[202:205], v[62:65], v[38:41]
	v_mfma_f32_16x16x32_bf16 v[110:113], v[206:209], v[224:227], v[18:21]
	v_mfma_f32_16x16x32_bf16 v[18:21], v[210:213], v[62:65], v[42:45]
	v_mfma_f32_16x16x32_bf16 v[106:109], v[220:223], v[224:227], v[18:21]
	v_mfma_f32_16x16x32_bf16 v[18:21], v[202:205], v[232:235], v[46:49]
	v_mfma_f32_16x16x32_bf16 v[94:97], v[206:209], v[236:239], v[18:21]
	v_mfma_f32_16x16x32_bf16 v[18:21], v[210:213], v[232:235], v[136:139]
	v_mfma_f32_16x16x32_bf16 v[90:93], v[220:223], v[236:239], v[18:21]
	v_mfma_f32_16x16x32_bf16 v[18:21], v[202:205], v[240:243], v[140:143]
	v_mfma_f32_16x16x32_bf16 v[62:65], v[206:209], v[244:247], v[18:21]
	v_mfma_f32_16x16x32_bf16 v[18:21], v[210:213], v[240:243], v[58:61]
	v_mfma_f32_16x16x32_bf16 v[118:121], v[206:209], v[22:25], v[66:69]
	v_mfma_f32_16x16x32_bf16 v[58:61], v[220:223], v[244:247], v[18:21]
	s_barrier
	s_setprio 0
	ds_read_b128 v[42:45], v219 offset:49152
	ds_read_b128 v[46:49], v219 offset:50176
	ds_read_b128 v[136:139], v219 offset:51200
	ds_read_b128 v[140:143], v219 offset:52224
	ds_read_b128 v[224:227], v219 offset:53248
	ds_read_b128 v[232:235], v219 offset:54272
	ds_read_b128 v[236:239], v219 offset:55296
	ds_read_b128 v[240:243], v219 offset:56320
	s_add_i32 s78, s78, s15
	v_lshl_add_u64 v[18:19], s[34:35], 0, v[0:1]
	v_lshl_add_u64 v[18:19], v[18:19], 0, s[16:17]
	s_mov_b32 m0, s78
	v_mov_b32_e32 v131, v1
	global_load_lds_dwordx4 v[18:19], off
	s_add_i32 s79, s78, 0x2000
	v_lshl_add_u64 v[18:19], s[34:35], 0, v[130:131]
	v_lshl_add_u64 v[18:19], v[18:19], 0, s[16:17]
	s_mov_b32 m0, s79
	s_add_i32 s80, s80, s15
	global_load_lds_dwordx4 v[18:19], off
	s_mov_b32 m0, s80
	v_lshl_add_u64 v[18:19], s[58:59], 0, v[0:1]
	v_lshl_add_u64 v[18:19], v[18:19], 0, s[16:17]
	global_load_lds_dwordx4 v[18:19], off
	s_nop 0
	v_lshl_add_u64 v[18:19], s[58:59], 0, v[130:131]
	s_add_i32 s58, s80, 0x2000
	v_lshl_add_u64 v[18:19], v[18:19], 0, s[16:17]
	s_mov_b32 m0, s58
	s_nop 0
	global_load_lds_dwordx4 v[18:19], off
	s_mov_b32 m0, s65
	s_nop 0
	global_load_lds_dwordx4 v217, s[30:31]
	s_mov_b32 m0, s66
	s_nop 0
	global_load_lds_dwordx4 v216, s[30:31]
	s_waitcnt vmcnt(8)
	s_waitcnt lgkmcnt(0)
	s_setprio 1
	s_barrier
	s_waitcnt lgkmcnt(0)
	v_mfma_f32_16x16x32_bf16 v[18:21], v[6:9], v[42:45], v[144:147]
	v_mfma_f32_16x16x32_bf16 v[70:73], v[26:29], v[46:49], v[18:21]
	v_mfma_f32_16x16x32_bf16 v[18:21], v[30:33], v[42:45], v[148:151]
	v_mfma_f32_16x16x32_bf16 v[66:69], v[198:201], v[46:49], v[18:21]
	v_mfma_f32_16x16x32_bf16 v[18:21], v[6:9], v[136:139], v[152:155]
	v_mfma_f32_16x16x32_bf16 v[38:41], v[26:29], v[140:143], v[18:21]
	v_mfma_f32_16x16x32_bf16 v[18:21], v[30:33], v[136:139], v[156:159]
	v_mfma_f32_16x16x32_bf16 v[34:37], v[198:201], v[140:143], v[18:21]
	v_mfma_f32_16x16x32_bf16 v[18:21], v[6:9], v[224:227], v[160:163]
	v_mfma_f32_16x16x32_bf16 v[2:5], v[6:9], v[236:239], v[2:5]
	v_mfma_f32_16x16x32_bf16 v[22:25], v[26:29], v[232:235], v[18:21]
	v_mfma_f32_16x16x32_bf16 v[18:21], v[30:33], v[224:227], v[164:167]
	v_mfma_f32_16x16x32_bf16 v[6:9], v[26:29], v[240:243], v[2:5]
	v_mfma_f32_16x16x32_bf16 v[2:5], v[30:33], v[236:239], v[10:13]
	v_mfma_f32_16x16x32_bf16 v[18:21], v[198:201], v[232:235], v[18:21]
	v_mfma_f32_16x16x32_bf16 v[2:5], v[198:201], v[240:243], v[2:5]
	s_setprio 0
	s_setprio 1
	v_mfma_f32_16x16x32_bf16 v[10:13], v[202:205], v[42:45], v[14:17]
	v_mfma_f32_16x16x32_bf16 v[78:81], v[206:209], v[46:49], v[10:13]
	v_mfma_f32_16x16x32_bf16 v[10:13], v[210:213], v[42:45], v[168:171]
	v_mfma_f32_16x16x32_bf16 v[74:77], v[220:223], v[46:49], v[10:13]
	v_mfma_f32_16x16x32_bf16 v[10:13], v[202:205], v[136:139], v[172:175]
	v_mfma_f32_16x16x32_bf16 v[46:49], v[206:209], v[140:143], v[10:13]
	v_mfma_f32_16x16x32_bf16 v[10:13], v[210:213], v[136:139], v[176:179]
	v_mfma_f32_16x16x32_bf16 v[42:45], v[220:223], v[140:143], v[10:13]
	v_mfma_f32_16x16x32_bf16 v[10:13], v[202:205], v[224:227], v[180:183]
	v_mfma_f32_16x16x32_bf16 v[30:33], v[206:209], v[232:235], v[10:13]
	v_mfma_f32_16x16x32_bf16 v[10:13], v[210:213], v[224:227], v[184:187]
	v_mfma_f32_16x16x32_bf16 v[26:29], v[220:223], v[232:235], v[10:13]
	v_mfma_f32_16x16x32_bf16 v[10:13], v[202:205], v[236:239], v[188:191]
	v_mfma_f32_16x16x32_bf16 v[14:17], v[206:209], v[240:243], v[10:13]
	v_mfma_f32_16x16x32_bf16 v[10:13], v[210:213], v[236:239], v[194:197]
	v_mfma_f32_16x16x32_bf16 v[10:13], v[220:223], v[240:243], v[10:13]
	s_barrier
	s_setprio 0
	s_andn2_b64 vcc, exec, s[50:51]
	s_cbranch_vccnz .LBB0_968
	s_add_u32 s59, s26, 0x200
	s_addc_u32 s81, s27, 0
	s_add_u32 s26, s28, 0x1c000
	s_addc_u32 s27, s29, 0
	s_mov_b32 s82, 4
.LBB0_967:
	ds_read_b128 v[136:139], v132
	ds_read_b128 v[140:143], v132 offset:1024
	ds_read_b128 v[144:147], v132 offset:2048
	ds_read_b128 v[148:151], v132 offset:3072
	ds_read_b128 v[152:155], v133
	ds_read_b128 v[156:159], v133 offset:1024
	ds_read_b128 v[160:163], v133 offset:2048
	ds_read_b128 v[164:167], v133 offset:3072
	s_add_u32 s28, s26, 0x4000
	s_addc_u32 s29, s27, 0
	s_cmp_eq_u32 s63, s82
	s_cselect_b32 s34, s42, s28
	s_cselect_b32 s35, s43, s29
	s_cselect_b32 s30, s54, s59
	s_cselect_b32 s31, s55, s81
	s_add_u32 s28, s34, 0x8000
	s_addc_u32 s29, s35, 0
	s_mov_b32 m0, s72
	ds_read_b128 v[168:171], v219
	ds_read_b128 v[172:175], v219 offset:1024
	ds_read_b128 v[176:179], v219 offset:2048
	ds_read_b128 v[180:183], v219 offset:3072
	ds_read_b128 v[184:187], v219 offset:4096
	ds_read_b128 v[188:191], v219 offset:5120
	ds_read_b128 v[194:197], v219 offset:6144
	ds_read_b128 v[198:201], v219 offset:7168
	s_nop 0
	global_load_lds_dwordx4 v217, s[26:27]
	s_mov_b32 m0, s73
	s_nop 0
	global_load_lds_dwordx4 v216, s[26:27]
	s_waitcnt vmcnt(8)
	s_waitcnt lgkmcnt(0)
	s_setprio 1
	s_barrier
	s_waitcnt lgkmcnt(0)
	v_mfma_f32_16x16x32_bf16 v[126:129], v[136:139], v[168:171], v[126:129]
	v_mfma_f32_16x16x32_bf16 v[122:125], v[144:147], v[168:171], v[122:125]
	v_mfma_f32_16x16x32_bf16 v[102:105], v[136:139], v[176:179], v[102:105]
	v_mfma_f32_16x16x32_bf16 v[98:101], v[144:147], v[176:179], v[98:101]
	v_mfma_f32_16x16x32_bf16 v[86:89], v[136:139], v[184:187], v[86:89]
	v_mfma_f32_16x16x32_bf16 v[82:85], v[144:147], v[184:187], v[82:85]
	v_mfma_f32_16x16x32_bf16 v[54:57], v[136:139], v[194:197], v[54:57]
	v_mfma_f32_16x16x32_bf16 v[50:53], v[144:147], v[194:197], v[50:53]
	v_mfma_f32_16x16x32_bf16 v[126:129], v[140:143], v[172:175], v[126:129]
	v_mfma_f32_16x16x32_bf16 v[122:125], v[148:151], v[172:175], v[122:125]
	v_mfma_f32_16x16x32_bf16 v[102:105], v[140:143], v[180:183], v[102:105]
	v_mfma_f32_16x16x32_bf16 v[98:101], v[148:151], v[180:183], v[98:101]
	v_mfma_f32_16x16x32_bf16 v[86:89], v[140:143], v[188:191], v[86:89]
	v_mfma_f32_16x16x32_bf16 v[82:85], v[148:151], v[188:191], v[82:85]
	v_mfma_f32_16x16x32_bf16 v[54:57], v[140:143], v[198:201], v[54:57]
	v_mfma_f32_16x16x32_bf16 v[50:53], v[148:151], v[198:201], v[50:53]
	s_setprio 0
	s_setprio 1
	v_mfma_f32_16x16x32_bf16 v[118:121], v[152:155], v[168:171], v[118:121]
	v_mfma_f32_16x16x32_bf16 v[114:117], v[160:163], v[168:171], v[114:117]
	v_mfma_f32_16x16x32_bf16 v[110:113], v[152:155], v[176:179], v[110:113]
	v_mfma_f32_16x16x32_bf16 v[106:109], v[160:163], v[176:179], v[106:109]
	v_mfma_f32_16x16x32_bf16 v[94:97], v[152:155], v[184:187], v[94:97]
	v_mfma_f32_16x16x32_bf16 v[90:93], v[160:163], v[184:187], v[90:93]
	v_mfma_f32_16x16x32_bf16 v[62:65], v[152:155], v[194:197], v[62:65]
	v_mfma_f32_16x16x32_bf16 v[58:61], v[160:163], v[194:197], v[58:61]
	v_mfma_f32_16x16x32_bf16 v[118:121], v[156:159], v[172:175], v[118:121]
	v_mfma_f32_16x16x32_bf16 v[114:117], v[164:167], v[172:175], v[114:117]
	v_mfma_f32_16x16x32_bf16 v[110:113], v[156:159], v[180:183], v[110:113]
	v_mfma_f32_16x16x32_bf16 v[106:109], v[164:167], v[180:183], v[106:109]
	v_mfma_f32_16x16x32_bf16 v[94:97], v[156:159], v[188:191], v[94:97]
	v_mfma_f32_16x16x32_bf16 v[90:93], v[164:167], v[188:191], v[90:93]
	v_mfma_f32_16x16x32_bf16 v[62:65], v[156:159], v[198:201], v[62:65]
	v_mfma_f32_16x16x32_bf16 v[58:61], v[164:167], v[198:201], v[58:61]
	s_barrier
	s_setprio 0
	s_mov_b32 m0, s74
	ds_read_b128 v[168:171], v219 offset:16384
	ds_read_b128 v[172:175], v219 offset:17408
	ds_read_b128 v[176:179], v219 offset:18432
	ds_read_b128 v[180:183], v219 offset:19456
	ds_read_b128 v[184:187], v219 offset:20480
	ds_read_b128 v[188:191], v219 offset:21504
	ds_read_b128 v[194:197], v219 offset:22528
	ds_read_b128 v[198:201], v219 offset:23552
	s_add_u32 s56, s30, s36
	global_load_lds_dwordx4 v0, s[30:31]
	s_mov_b32 m0, s75
	s_addc_u32 s57, s31, s37
	global_load_lds_dwordx4 v130, s[30:31]
	s_mov_b32 m0, s76
	s_nop 0
	global_load_lds_dwordx4 v0, s[56:57]
	s_mov_b32 m0, s77
	s_nop 0
	global_load_lds_dwordx4 v130, s[56:57]
	s_mov_b32 m0, s18
	s_nop 0
	global_load_lds_dwordx4 v217, s[34:35]
	s_mov_b32 m0, s20
	s_nop 0
	global_load_lds_dwordx4 v216, s[34:35]
	s_waitcnt vmcnt(8)
	s_waitcnt lgkmcnt(0)
	s_setprio 1
	s_barrier
	s_waitcnt lgkmcnt(0)
	v_mfma_f32_16x16x32_bf16 v[70:73], v[136:139], v[168:171], v[70:73]
	v_mfma_f32_16x16x32_bf16 v[66:69], v[144:147], v[168:171], v[66:69]
	v_mfma_f32_16x16x32_bf16 v[38:41], v[136:139], v[176:179], v[38:41]
	v_mfma_f32_16x16x32_bf16 v[34:37], v[144:147], v[176:179], v[34:37]
	v_mfma_f32_16x16x32_bf16 v[22:25], v[136:139], v[184:187], v[22:25]
	v_mfma_f32_16x16x32_bf16 v[18:21], v[144:147], v[184:187], v[18:21]
	v_mfma_f32_16x16x32_bf16 v[6:9], v[136:139], v[194:197], v[6:9]
	v_mfma_f32_16x16x32_bf16 v[2:5], v[144:147], v[194:197], v[2:5]
	v_mfma_f32_16x16x32_bf16 v[70:73], v[140:143], v[172:175], v[70:73]
	v_mfma_f32_16x16x32_bf16 v[66:69], v[148:151], v[172:175], v[66:69]
	v_mfma_f32_16x16x32_bf16 v[38:41], v[140:143], v[180:183], v[38:41]
	v_mfma_f32_16x16x32_bf16 v[34:37], v[148:151], v[180:183], v[34:37]
	v_mfma_f32_16x16x32_bf16 v[22:25], v[140:143], v[188:191], v[22:25]
	v_mfma_f32_16x16x32_bf16 v[18:21], v[148:151], v[188:191], v[18:21]
	v_mfma_f32_16x16x32_bf16 v[6:9], v[140:143], v[198:201], v[6:9]
	v_mfma_f32_16x16x32_bf16 v[2:5], v[148:151], v[198:201], v[2:5]
	s_setprio 0
	s_setprio 1
	v_mfma_f32_16x16x32_bf16 v[78:81], v[152:155], v[168:171], v[78:81]
	v_mfma_f32_16x16x32_bf16 v[74:77], v[160:163], v[168:171], v[74:77]
	v_mfma_f32_16x16x32_bf16 v[46:49], v[152:155], v[176:179], v[46:49]
	v_mfma_f32_16x16x32_bf16 v[42:45], v[160:163], v[176:179], v[42:45]
	v_mfma_f32_16x16x32_bf16 v[30:33], v[152:155], v[184:187], v[30:33]
	v_mfma_f32_16x16x32_bf16 v[26:29], v[160:163], v[184:187], v[26:29]
	v_mfma_f32_16x16x32_bf16 v[14:17], v[152:155], v[194:197], v[14:17]
	v_mfma_f32_16x16x32_bf16 v[10:13], v[160:163], v[194:197], v[10:13]
	v_mfma_f32_16x16x32_bf16 v[78:81], v[156:159], v[172:175], v[78:81]
	v_mfma_f32_16x16x32_bf16 v[74:77], v[164:167], v[172:175], v[74:77]
	v_mfma_f32_16x16x32_bf16 v[46:49], v[156:159], v[180:183], v[46:49]
	v_mfma_f32_16x16x32_bf16 v[42:45], v[164:167], v[180:183], v[42:45]
	v_mfma_f32_16x16x32_bf16 v[30:33], v[156:159], v[188:191], v[30:33]
	v_mfma_f32_16x16x32_bf16 v[26:29], v[164:167], v[188:191], v[26:29]
	v_mfma_f32_16x16x32_bf16 v[14:17], v[156:159], v[198:201], v[14:17]
	v_mfma_f32_16x16x32_bf16 v[10:13], v[164:167], v[198:201], v[10:13]
	s_barrier
	s_setprio 0
	ds_read_b128 v[136:139], v134
	ds_read_b128 v[140:143], v134 offset:1024
	ds_read_b128 v[144:147], v134 offset:2048
	ds_read_b128 v[148:151], v134 offset:3072
	ds_read_b128 v[152:155], v135
	ds_read_b128 v[156:159], v135 offset:1024
	ds_read_b128 v[160:163], v135 offset:2048
	ds_read_b128 v[164:167], v135 offset:3072
	s_add_u32 s34, s34, 0x4000
	s_addc_u32 s35, s35, 0
	s_mov_b32 m0, s25
	ds_read_b128 v[168:171], v219 offset:32768
	ds_read_b128 v[172:175], v219 offset:33792
	ds_read_b128 v[176:179], v219 offset:34816
	ds_read_b128 v[180:183], v219 offset:35840
	ds_read_b128 v[184:187], v219 offset:36864
	ds_read_b128 v[188:191], v219 offset:37888
	ds_read_b128 v[194:197], v219 offset:38912
	ds_read_b128 v[198:201], v219 offset:39936
	s_nop 0
	global_load_lds_dwordx4 v217, s[34:35]
	s_mov_b32 m0, s60
	s_nop 0
	global_load_lds_dwordx4 v216, s[34:35]
	s_waitcnt vmcnt(8)
	s_waitcnt lgkmcnt(0)
	s_setprio 1
	s_barrier
	s_waitcnt lgkmcnt(0)
	v_mfma_f32_16x16x32_bf16 v[126:129], v[136:139], v[168:171], v[126:129]
	v_mfma_f32_16x16x32_bf16 v[122:125], v[144:147], v[168:171], v[122:125]
	v_mfma_f32_16x16x32_bf16 v[102:105], v[136:139], v[176:179], v[102:105]
	v_mfma_f32_16x16x32_bf16 v[98:101], v[144:147], v[176:179], v[98:101]
	v_mfma_f32_16x16x32_bf16 v[86:89], v[136:139], v[184:187], v[86:89]
	v_mfma_f32_16x16x32_bf16 v[82:85], v[144:147], v[184:187], v[82:85]
	v_mfma_f32_16x16x32_bf16 v[54:57], v[136:139], v[194:197], v[54:57]
	v_mfma_f32_16x16x32_bf16 v[50:53], v[144:147], v[194:197], v[50:53]
	v_mfma_f32_16x16x32_bf16 v[126:129], v[140:143], v[172:175], v[126:129]
	v_mfma_f32_16x16x32_bf16 v[122:125], v[148:151], v[172:175], v[122:125]
	v_mfma_f32_16x16x32_bf16 v[102:105], v[140:143], v[180:183], v[102:105]
	v_mfma_f32_16x16x32_bf16 v[98:101], v[148:151], v[180:183], v[98:101]
	v_mfma_f32_16x16x32_bf16 v[86:89], v[140:143], v[188:191], v[86:89]
	v_mfma_f32_16x16x32_bf16 v[82:85], v[148:151], v[188:191], v[82:85]
	v_mfma_f32_16x16x32_bf16 v[54:57], v[140:143], v[198:201], v[54:57]
	v_mfma_f32_16x16x32_bf16 v[50:53], v[148:151], v[198:201], v[50:53]
	s_setprio 0
	s_setprio 1
	v_mfma_f32_16x16x32_bf16 v[118:121], v[152:155], v[168:171], v[118:121]
	v_mfma_f32_16x16x32_bf16 v[114:117], v[160:163], v[168:171], v[114:117]
	v_mfma_f32_16x16x32_bf16 v[110:113], v[152:155], v[176:179], v[110:113]
	v_mfma_f32_16x16x32_bf16 v[106:109], v[160:163], v[176:179], v[106:109]
	v_mfma_f32_16x16x32_bf16 v[94:97], v[152:155], v[184:187], v[94:97]
	v_mfma_f32_16x16x32_bf16 v[90:93], v[160:163], v[184:187], v[90:93]
	v_mfma_f32_16x16x32_bf16 v[62:65], v[152:155], v[194:197], v[62:65]
	v_mfma_f32_16x16x32_bf16 v[58:61], v[160:163], v[194:197], v[58:61]
	v_mfma_f32_16x16x32_bf16 v[118:121], v[156:159], v[172:175], v[118:121]
	v_mfma_f32_16x16x32_bf16 v[114:117], v[164:167], v[172:175], v[114:117]
	v_mfma_f32_16x16x32_bf16 v[110:113], v[156:159], v[180:183], v[110:113]
	v_mfma_f32_16x16x32_bf16 v[106:109], v[164:167], v[180:183], v[106:109]
	v_mfma_f32_16x16x32_bf16 v[94:97], v[156:159], v[188:191], v[94:97]
	v_mfma_f32_16x16x32_bf16 v[90:93], v[164:167], v[188:191], v[90:93]
	v_mfma_f32_16x16x32_bf16 v[62:65], v[156:159], v[198:201], v[62:65]
	v_mfma_f32_16x16x32_bf16 v[58:61], v[164:167], v[198:201], v[58:61]
	s_barrier
	s_setprio 0
	ds_read_b128 v[168:171], v219 offset:49152
	ds_read_b128 v[172:175], v219 offset:50176
	ds_read_b128 v[176:179], v219 offset:51200
	ds_read_b128 v[180:183], v219 offset:52224
	ds_read_b128 v[184:187], v219 offset:53248
	ds_read_b128 v[188:191], v219 offset:54272
	ds_read_b128 v[194:197], v219 offset:55296
	ds_read_b128 v[198:201], v219 offset:56320
	s_mov_b32 m0, s78
	v_lshl_add_u64 v[202:203], s[30:31], 0, v[0:1]
	v_lshl_add_u64 v[202:203], v[202:203], 0, s[16:17]
	v_mov_b32_e32 v131, v1
	global_load_lds_dwordx4 v[202:203], off
	s_mov_b32 m0, s79
	v_lshl_add_u64 v[202:203], s[30:31], 0, v[130:131]
	v_lshl_add_u64 v[202:203], v[202:203], 0, s[16:17]
	global_load_lds_dwordx4 v[202:203], off
	s_mov_b32 m0, s80
	v_lshl_add_u64 v[202:203], s[56:57], 0, v[0:1]
	v_lshl_add_u64 v[202:203], v[202:203], 0, s[16:17]
	global_load_lds_dwordx4 v[202:203], off
	s_mov_b32 m0, s58
	v_lshl_add_u64 v[202:203], s[56:57], 0, v[130:131]
	v_lshl_add_u64 v[202:203], v[202:203], 0, s[16:17]
	global_load_lds_dwordx4 v[202:203], off
	s_mov_b32 m0, s65
	s_nop 0
	global_load_lds_dwordx4 v217, s[28:29]
	s_mov_b32 m0, s66
	s_nop 0
	global_load_lds_dwordx4 v216, s[28:29]
	s_waitcnt vmcnt(8)
	s_waitcnt lgkmcnt(0)
	s_setprio 1
	s_barrier
	s_waitcnt lgkmcnt(0)
	v_mfma_f32_16x16x32_bf16 v[70:73], v[136:139], v[168:171], v[70:73]
	v_mfma_f32_16x16x32_bf16 v[66:69], v[144:147], v[168:171], v[66:69]
	v_mfma_f32_16x16x32_bf16 v[38:41], v[136:139], v[176:179], v[38:41]
	v_mfma_f32_16x16x32_bf16 v[34:37], v[144:147], v[176:179], v[34:37]
	v_mfma_f32_16x16x32_bf16 v[22:25], v[136:139], v[184:187], v[22:25]
	v_mfma_f32_16x16x32_bf16 v[18:21], v[144:147], v[184:187], v[18:21]
	v_mfma_f32_16x16x32_bf16 v[6:9], v[136:139], v[194:197], v[6:9]
	v_mfma_f32_16x16x32_bf16 v[2:5], v[144:147], v[194:197], v[2:5]
	v_mfma_f32_16x16x32_bf16 v[70:73], v[140:143], v[172:175], v[70:73]
	v_mfma_f32_16x16x32_bf16 v[66:69], v[148:151], v[172:175], v[66:69]
	v_mfma_f32_16x16x32_bf16 v[38:41], v[140:143], v[180:183], v[38:41]
	v_mfma_f32_16x16x32_bf16 v[34:37], v[148:151], v[180:183], v[34:37]
	v_mfma_f32_16x16x32_bf16 v[22:25], v[140:143], v[188:191], v[22:25]
	v_mfma_f32_16x16x32_bf16 v[18:21], v[148:151], v[188:191], v[18:21]
	v_mfma_f32_16x16x32_bf16 v[6:9], v[140:143], v[198:201], v[6:9]
	v_mfma_f32_16x16x32_bf16 v[2:5], v[148:151], v[198:201], v[2:5]
	s_setprio 0
	s_setprio 1
	v_mfma_f32_16x16x32_bf16 v[78:81], v[152:155], v[168:171], v[78:81]
	v_mfma_f32_16x16x32_bf16 v[74:77], v[160:163], v[168:171], v[74:77]
	v_mfma_f32_16x16x32_bf16 v[46:49], v[152:155], v[176:179], v[46:49]
	v_mfma_f32_16x16x32_bf16 v[42:45], v[160:163], v[176:179], v[42:45]
	v_mfma_f32_16x16x32_bf16 v[30:33], v[152:155], v[184:187], v[30:33]
	v_mfma_f32_16x16x32_bf16 v[26:29], v[160:163], v[184:187], v[26:29]
	v_mfma_f32_16x16x32_bf16 v[14:17], v[152:155], v[194:197], v[14:17]
	v_mfma_f32_16x16x32_bf16 v[10:13], v[160:163], v[194:197], v[10:13]
	v_mfma_f32_16x16x32_bf16 v[78:81], v[156:159], v[172:175], v[78:81]
	v_mfma_f32_16x16x32_bf16 v[74:77], v[164:167], v[172:175], v[74:77]
	v_mfma_f32_16x16x32_bf16 v[46:49], v[156:159], v[180:183], v[46:49]
	v_mfma_f32_16x16x32_bf16 v[42:45], v[164:167], v[180:183], v[42:45]
	v_mfma_f32_16x16x32_bf16 v[30:33], v[156:159], v[188:191], v[30:33]
	v_mfma_f32_16x16x32_bf16 v[26:29], v[164:167], v[188:191], v[26:29]
	v_mfma_f32_16x16x32_bf16 v[14:17], v[156:159], v[198:201], v[14:17]
	v_mfma_f32_16x16x32_bf16 v[10:13], v[164:167], v[198:201], v[10:13]
	s_barrier
	s_setprio 0
	s_add_i32 s28, s82, 2
	s_add_u32 s59, s59, 0x100
	s_addc_u32 s81, s81, 0
	s_add_u32 s26, s26, 0x10000
	s_addc_u32 s27, s27, 0
	s_cmp_lt_i32 s82, s63
	s_mov_b32 s82, s28
	s_cbranch_scc1 .LBB0_967

.LBB0_1072:
	s_add_u32 s21, s26, 0x10000
	s_addc_u32 s34, s27, 0
	s_and_b64 s[30:31], s[48:49], exec
	s_cselect_b32 s55, s43, s34
	s_cselect_b32 s54, s42, s21
	s_add_u32 s21, s28, 0x100
	s_addc_u32 s56, s29, 0
	s_add_u32 s30, s54, 0x8000
	s_addc_u32 s31, s55, 0
	s_add_i32 s71, 0, 0x10000
	s_and_b64 s[34:35], s[48:49], exec
	s_cselect_b32 s35, s45, s56
	s_cselect_b32 s34, s44, s21
	s_add_i32 s73, 0, 0x14000
	v_add_u32_e32 v114, s71, v237
	v_add_u32_e32 v115, s73, v237
	ds_read_b128 v[2:5], v114
	s_waitcnt lgkmcnt(0)
	ds_read_b128 v[6:9], v114 offset:1024
	ds_read_b128 v[10:13], v114 offset:2048
	ds_read_b128 v[14:17], v114 offset:3072
	ds_read_b128 v[18:21], v115
	ds_read_b128 v[22:25], v115 offset:1024
	ds_read_b128 v[26:29], v115 offset:2048
	ds_read_b128 v[30:33], v115 offset:3072
	s_add_u32 s56, s26, 0xc000
	s_addc_u32 s57, s27, 0
	s_add_i32 s21, s20, 0xc000
	s_mov_b32 m0, s21
	s_add_i32 s70, s20, 0xe000
	ds_read_b128 v[34:37], v238
	ds_read_b128 v[38:41], v238 offset:1024
	ds_read_b128 v[42:45], v238 offset:2048
	ds_read_b128 v[46:49], v238 offset:3072
	ds_read_b128 v[50:53], v238 offset:4096
	ds_read_b128 v[54:57], v238 offset:5120
	ds_read_b128 v[58:61], v238 offset:6144
	ds_read_b128 v[62:65], v238 offset:7168
	s_nop 0
	global_load_lds_dwordx4 v236, s[56:57]
	s_mov_b32 m0, s70
	s_nop 0
	global_load_lds_dwordx4 v235, s[56:57]
	s_waitcnt vmcnt(8)
	s_waitcnt lgkmcnt(0)
	s_setprio 1
	s_barrier
	s_waitcnt lgkmcnt(0)
	v_mfma_f32_16x16x32_bf16 v[90:93], v[2:5], v[58:61], 0
	v_mfma_f32_16x16x32_bf16 v[66:69], v[2:5], v[34:37], 0
	v_mfma_f32_16x16x32_bf16 v[70:73], v[10:13], v[34:37], 0
	v_mfma_f32_16x16x32_bf16 v[74:77], v[2:5], v[42:45], 0
	v_mfma_f32_16x16x32_bf16 v[78:81], v[10:13], v[42:45], 0
	v_mfma_f32_16x16x32_bf16 v[82:85], v[2:5], v[50:53], 0
	v_mfma_f32_16x16x32_bf16 v[86:89], v[10:13], v[50:53], 0
	v_mfma_f32_16x16x32_bf16 v[98:101], v[6:9], v[62:65], v[90:93]
	v_mfma_f32_16x16x32_bf16 v[90:93], v[10:13], v[58:61], 0
	v_mfma_f32_16x16x32_bf16 v[66:69], v[6:9], v[38:41], v[66:69]
	v_mfma_f32_16x16x32_bf16 v[70:73], v[14:17], v[38:41], v[70:73]
	v_mfma_f32_16x16x32_bf16 v[74:77], v[6:9], v[46:49], v[74:77]
	v_mfma_f32_16x16x32_bf16 v[78:81], v[14:17], v[46:49], v[78:81]
	v_mfma_f32_16x16x32_bf16 v[82:85], v[6:9], v[54:57], v[82:85]
	v_mfma_f32_16x16x32_bf16 v[86:89], v[14:17], v[54:57], v[86:89]
	v_mfma_f32_16x16x32_bf16 v[102:105], v[14:17], v[62:65], v[90:93]
	s_setprio 0
	s_setprio 1
	v_mfma_f32_16x16x32_bf16 v[90:93], v[18:21], v[34:37], 0
	v_mfma_f32_16x16x32_bf16 v[34:37], v[26:29], v[34:37], 0
	v_mfma_f32_16x16x32_bf16 v[118:121], v[22:25], v[38:41], v[90:93]
	v_mfma_f32_16x16x32_bf16 v[34:37], v[30:33], v[38:41], v[34:37]
	v_mfma_f32_16x16x32_bf16 v[38:41], v[18:21], v[42:45], 0
	v_mfma_f32_16x16x32_bf16 v[42:45], v[26:29], v[42:45], 0
	v_mfma_f32_16x16x32_bf16 v[38:41], v[22:25], v[46:49], v[38:41]
	v_mfma_f32_16x16x32_bf16 v[42:45], v[30:33], v[46:49], v[42:45]
	v_mfma_f32_16x16x32_bf16 v[46:49], v[18:21], v[50:53], 0
	v_mfma_f32_16x16x32_bf16 v[50:53], v[26:29], v[50:53], 0
	v_mfma_f32_16x16x32_bf16 v[46:49], v[22:25], v[54:57], v[46:49]
	v_mfma_f32_16x16x32_bf16 v[50:53], v[30:33], v[54:57], v[50:53]
	v_mfma_f32_16x16x32_bf16 v[54:57], v[18:21], v[58:61], 0
	v_mfma_f32_16x16x32_bf16 v[58:61], v[26:29], v[58:61], 0
	v_mfma_f32_16x16x32_bf16 v[54:57], v[22:25], v[62:65], v[54:57]
	v_mfma_f32_16x16x32_bf16 v[58:61], v[30:33], v[62:65], v[58:61]
	s_barrier
	s_setprio 0
	s_add_i32 s71, s71, s18
	s_add_i32 s72, s71, 0x2000
	s_mov_b32 m0, s71
	s_add_u32 s56, s34, s36
	ds_read_b128 v[62:65], v238 offset:16384
	ds_read_b128 v[90:93], v238 offset:17408
	ds_read_b128 v[94:97], v238 offset:18432
	ds_read_b128 v[106:109], v238 offset:19456
	ds_read_b128 v[110:113], v238 offset:20480
	ds_read_b128 v[122:125], v238 offset:21504
	ds_read_b128 v[126:129], v238 offset:22528
	ds_read_b128 v[130:133], v238 offset:23552
	s_addc_u32 s57, s35, s37
	global_load_lds_dwordx4 v0, s[34:35]
	s_mov_b32 m0, s72
	s_add_i32 s73, s73, s18
	s_add_i32 s74, s73, 0x2000
	global_load_lds_dwordx4 v210, s[34:35]
	s_mov_b32 m0, s73
	s_nop 0
	global_load_lds_dwordx4 v0, s[56:57]
	s_mov_b32 m0, s74
	s_nop 0
	global_load_lds_dwordx4 v210, s[56:57]
	s_mov_b32 m0, s20
	s_nop 0
	global_load_lds_dwordx4 v236, s[54:55]
	s_mov_b32 m0, s25
	s_nop 0
	global_load_lds_dwordx4 v235, s[54:55]
	s_waitcnt vmcnt(8)
	s_waitcnt lgkmcnt(0)
	s_setprio 1
	s_barrier
	s_waitcnt lgkmcnt(0)
	v_mfma_f32_16x16x32_bf16 v[134:137], v[2:5], v[62:65], 0
	v_mfma_f32_16x16x32_bf16 v[142:145], v[2:5], v[94:97], 0
	v_mfma_f32_16x16x32_bf16 v[150:153], v[2:5], v[110:113], 0
	v_mfma_f32_16x16x32_bf16 v[2:5], v[2:5], v[126:129], 0
	v_mfma_f32_16x16x32_bf16 v[134:137], v[6:9], v[90:93], v[134:137]
	v_mfma_f32_16x16x32_bf16 v[142:145], v[6:9], v[106:109], v[142:145]
	v_mfma_f32_16x16x32_bf16 v[150:153], v[6:9], v[122:125], v[150:153]
	v_mfma_f32_16x16x32_bf16 v[2:5], v[6:9], v[130:133], v[2:5]
	v_mfma_f32_16x16x32_bf16 v[6:9], v[10:13], v[126:129], 0
	v_mfma_f32_16x16x32_bf16 v[138:141], v[10:13], v[62:65], 0
	v_mfma_f32_16x16x32_bf16 v[146:149], v[10:13], v[94:97], 0
	v_mfma_f32_16x16x32_bf16 v[154:157], v[10:13], v[110:113], 0
	v_mfma_f32_16x16x32_bf16 v[6:9], v[14:17], v[130:133], v[6:9]
	v_mfma_f32_16x16x32_bf16 v[138:141], v[14:17], v[90:93], v[138:141]
	v_mfma_f32_16x16x32_bf16 v[146:149], v[14:17], v[106:109], v[146:149]
	v_mfma_f32_16x16x32_bf16 v[154:157], v[14:17], v[122:125], v[154:157]
	s_setprio 0
	s_setprio 1
	v_mfma_f32_16x16x32_bf16 v[10:13], v[18:21], v[62:65], 0
	v_mfma_f32_16x16x32_bf16 v[158:161], v[22:25], v[90:93], v[10:13]
	v_mfma_f32_16x16x32_bf16 v[10:13], v[26:29], v[62:65], 0
	v_mfma_f32_16x16x32_bf16 v[170:173], v[30:33], v[90:93], v[10:13]
	v_mfma_f32_16x16x32_bf16 v[10:13], v[18:21], v[94:97], 0
	v_mfma_f32_16x16x32_bf16 v[174:177], v[22:25], v[106:109], v[10:13]
	v_mfma_f32_16x16x32_bf16 v[10:13], v[26:29], v[94:97], 0
	v_mfma_f32_16x16x32_bf16 v[178:181], v[30:33], v[106:109], v[10:13]
	v_mfma_f32_16x16x32_bf16 v[10:13], v[18:21], v[110:113], 0
	v_mfma_f32_16x16x32_bf16 v[182:185], v[22:25], v[122:125], v[10:13]
	v_mfma_f32_16x16x32_bf16 v[10:13], v[26:29], v[110:113], 0
	v_mfma_f32_16x16x32_bf16 v[186:189], v[30:33], v[122:125], v[10:13]
	v_mfma_f32_16x16x32_bf16 v[10:13], v[18:21], v[126:129], 0
	v_mfma_f32_16x16x32_bf16 v[194:197], v[22:25], v[130:133], v[10:13]
	v_mfma_f32_16x16x32_bf16 v[10:13], v[26:29], v[126:129], 0
	v_mfma_f32_16x16x32_bf16 v[126:129], v[30:33], v[130:133], v[10:13]
	s_barrier
	s_setprio 0
	s_add_i32 s75, 0, 0x18000
	s_add_i32 s77, 0, 0x1c000
	v_add_u32_e32 v116, s75, v237
	v_add_u32_e32 v117, s77, v237
	s_nop 0
	ds_read_b128 v[10:13], v116
	ds_read_b128 v[14:17], v116 offset:1024
	ds_read_b128 v[18:21], v116 offset:2048
	ds_read_b128 v[22:25], v116 offset:3072
	ds_read_b128 v[130:133], v117
	ds_read_b128 v[198:201], v117 offset:1024
	ds_read_b128 v[202:205], v117 offset:2048
	ds_read_b128 v[206:209], v117 offset:3072
	s_add_u32 s54, s54, 0x4000
	s_addc_u32 s55, s55, 0
	s_mov_b32 m0, s58
	ds_read_b128 v[26:29], v238 offset:32768
	ds_read_b128 v[30:33], v238 offset:33792
	ds_read_b128 v[62:65], v238 offset:34816
	ds_read_b128 v[212:215], v238 offset:35840
	ds_read_b128 v[216:219], v238 offset:36864
	ds_read_b128 v[220:223], v238 offset:37888
	ds_read_b128 v[224:227], v238 offset:38912
	ds_read_b128 v[240:243], v238 offset:39936
	s_nop 0
	global_load_lds_dwordx4 v236, s[54:55]
	s_mov_b32 m0, s59
	s_nop 0
	global_load_lds_dwordx4 v235, s[54:55]
	s_waitcnt vmcnt(8)
	s_waitcnt lgkmcnt(0)
	s_setprio 1
	s_barrier
	s_waitcnt lgkmcnt(0)
	v_mfma_f32_16x16x32_bf16 v[66:69], v[10:13], v[26:29], v[66:69]
	v_mfma_f32_16x16x32_bf16 v[162:165], v[14:17], v[30:33], v[66:69]
	v_mfma_f32_16x16x32_bf16 v[66:69], v[18:21], v[26:29], v[70:73]
	v_mfma_f32_16x16x32_bf16 v[166:169], v[22:25], v[30:33], v[66:69]
	v_mfma_f32_16x16x32_bf16 v[66:69], v[10:13], v[62:65], v[74:77]
	v_mfma_f32_16x16x32_bf16 v[110:113], v[14:17], v[212:215], v[66:69]
	v_mfma_f32_16x16x32_bf16 v[66:69], v[18:21], v[62:65], v[78:81]
	v_mfma_f32_16x16x32_bf16 v[106:109], v[22:25], v[212:215], v[66:69]
	v_mfma_f32_16x16x32_bf16 v[66:69], v[10:13], v[216:219], v[82:85]
	v_mfma_f32_16x16x32_bf16 v[94:97], v[14:17], v[220:223], v[66:69]
	v_mfma_f32_16x16x32_bf16 v[66:69], v[18:21], v[216:219], v[86:89]
	v_mfma_f32_16x16x32_bf16 v[90:93], v[22:25], v[220:223], v[66:69]
	v_mfma_f32_16x16x32_bf16 v[66:69], v[10:13], v[224:227], v[98:101]
	v_mfma_f32_16x16x32_bf16 v[70:73], v[14:17], v[240:243], v[66:69]
	v_mfma_f32_16x16x32_bf16 v[66:69], v[18:21], v[224:227], v[102:105]
	v_mfma_f32_16x16x32_bf16 v[66:69], v[22:25], v[240:243], v[66:69]
	s_setprio 0
	s_setprio 1
	v_mfma_f32_16x16x32_bf16 v[74:77], v[130:133], v[26:29], v[118:121]
	v_mfma_f32_16x16x32_bf16 v[26:29], v[202:205], v[26:29], v[34:37]
	v_mfma_f32_16x16x32_bf16 v[118:121], v[206:209], v[30:33], v[26:29]
	v_mfma_f32_16x16x32_bf16 v[26:29], v[130:133], v[62:65], v[38:41]
	v_mfma_f32_16x16x32_bf16 v[102:105], v[198:201], v[212:215], v[26:29]
	v_mfma_f32_16x16x32_bf16 v[26:29], v[202:205], v[62:65], v[42:45]
	v_mfma_f32_16x16x32_bf16 v[98:101], v[206:209], v[212:215], v[26:29]
	v_mfma_f32_16x16x32_bf16 v[26:29], v[130:133], v[216:219], v[46:49]
	v_mfma_f32_16x16x32_bf16 v[86:89], v[198:201], v[220:223], v[26:29]
	v_mfma_f32_16x16x32_bf16 v[26:29], v[202:205], v[216:219], v[50:53]
	v_mfma_f32_16x16x32_bf16 v[82:85], v[206:209], v[220:223], v[26:29]
	v_mfma_f32_16x16x32_bf16 v[26:29], v[130:133], v[224:227], v[54:57]
	v_mfma_f32_16x16x32_bf16 v[54:57], v[198:201], v[240:243], v[26:29]
	v_mfma_f32_16x16x32_bf16 v[26:29], v[202:205], v[224:227], v[58:61]
	v_mfma_f32_16x16x32_bf16 v[122:125], v[198:201], v[30:33], v[74:77]
	v_mfma_f32_16x16x32_bf16 v[50:53], v[206:209], v[240:243], v[26:29]
	s_barrier
	s_setprio 0
	ds_read_b128 v[34:37], v238 offset:49152
	ds_read_b128 v[38:41], v238 offset:50176
	ds_read_b128 v[212:215], v238 offset:51200
	ds_read_b128 v[216:219], v238 offset:52224
	ds_read_b128 v[220:223], v238 offset:53248
	ds_read_b128 v[224:227], v238 offset:54272
	ds_read_b128 v[240:243], v238 offset:55296
	ds_read_b128 v[244:247], v238 offset:56320
	s_add_i32 s75, s75, s18
	v_lshl_add_u64 v[26:27], s[34:35], 0, v[0:1]
	v_lshl_add_u64 v[26:27], v[26:27], 0, s[16:17]
	s_mov_b32 m0, s75
	v_mov_b32_e32 v211, v1
	global_load_lds_dwordx4 v[26:27], off
	s_add_i32 s76, s75, 0x2000
	v_lshl_add_u64 v[26:27], s[34:35], 0, v[210:211]
	v_lshl_add_u64 v[26:27], v[26:27], 0, s[16:17]
	s_mov_b32 m0, s76
	s_add_i32 s77, s77, s18
	global_load_lds_dwordx4 v[26:27], off
	s_mov_b32 m0, s77
	v_lshl_add_u64 v[26:27], s[56:57], 0, v[0:1]
	v_lshl_add_u64 v[26:27], v[26:27], 0, s[16:17]
	global_load_lds_dwordx4 v[26:27], off
	s_nop 0
	v_lshl_add_u64 v[26:27], s[56:57], 0, v[210:211]
	s_add_i32 s56, s77, 0x2000
	v_lshl_add_u64 v[26:27], v[26:27], 0, s[16:17]
	s_mov_b32 m0, s56
	s_nop 0
	global_load_lds_dwordx4 v[26:27], off
	s_mov_b32 m0, s62
	s_nop 0
	global_load_lds_dwordx4 v236, s[30:31]
	s_mov_b32 m0, s63
	s_nop 0
	global_load_lds_dwordx4 v235, s[30:31]
	s_waitcnt vmcnt(8)
	s_waitcnt lgkmcnt(0)
	s_setprio 1
	s_barrier
	s_waitcnt lgkmcnt(0)
	v_mfma_f32_16x16x32_bf16 v[26:29], v[10:13], v[34:37], v[134:137]
	v_mfma_f32_16x16x32_bf16 v[78:81], v[14:17], v[38:41], v[26:29]
	v_mfma_f32_16x16x32_bf16 v[26:29], v[18:21], v[34:37], v[138:141]
	v_mfma_f32_16x16x32_bf16 v[74:77], v[22:25], v[38:41], v[26:29]
	v_mfma_f32_16x16x32_bf16 v[26:29], v[10:13], v[212:215], v[142:145]
	v_mfma_f32_16x16x32_bf16 v[46:49], v[14:17], v[216:219], v[26:29]
	v_mfma_f32_16x16x32_bf16 v[26:29], v[18:21], v[212:215], v[146:149]
	v_mfma_f32_16x16x32_bf16 v[42:45], v[22:25], v[216:219], v[26:29]
	v_mfma_f32_16x16x32_bf16 v[26:29], v[10:13], v[220:223], v[150:153]
	v_mfma_f32_16x16x32_bf16 v[2:5], v[10:13], v[240:243], v[2:5]
	v_mfma_f32_16x16x32_bf16 v[30:33], v[14:17], v[224:227], v[26:29]
	v_mfma_f32_16x16x32_bf16 v[26:29], v[18:21], v[220:223], v[154:157]
	v_mfma_f32_16x16x32_bf16 v[14:17], v[14:17], v[244:247], v[2:5]
	v_mfma_f32_16x16x32_bf16 v[2:5], v[18:21], v[240:243], v[6:9]
	v_mfma_f32_16x16x32_bf16 v[26:29], v[22:25], v[224:227], v[26:29]
	v_mfma_f32_16x16x32_bf16 v[10:13], v[22:25], v[244:247], v[2:5]
	s_setprio 0
	s_setprio 1
	v_mfma_f32_16x16x32_bf16 v[2:5], v[130:133], v[34:37], v[158:161]
	v_mfma_f32_16x16x32_bf16 v[62:65], v[198:201], v[38:41], v[2:5]
	v_mfma_f32_16x16x32_bf16 v[2:5], v[202:205], v[34:37], v[170:173]
	v_mfma_f32_16x16x32_bf16 v[58:61], v[206:209], v[38:41], v[2:5]
	v_mfma_f32_16x16x32_bf16 v[2:5], v[130:133], v[212:215], v[174:177]
	v_mfma_f32_16x16x32_bf16 v[38:41], v[198:201], v[216:219], v[2:5]
	v_mfma_f32_16x16x32_bf16 v[2:5], v[202:205], v[212:215], v[178:181]
	v_mfma_f32_16x16x32_bf16 v[34:37], v[206:209], v[216:219], v[2:5]
	v_mfma_f32_16x16x32_bf16 v[2:5], v[130:133], v[220:223], v[182:185]
	v_mfma_f32_16x16x32_bf16 v[22:25], v[198:201], v[224:227], v[2:5]
	v_mfma_f32_16x16x32_bf16 v[2:5], v[202:205], v[220:223], v[186:189]
	v_mfma_f32_16x16x32_bf16 v[18:21], v[206:209], v[224:227], v[2:5]
	v_mfma_f32_16x16x32_bf16 v[2:5], v[130:133], v[240:243], v[194:197]
	v_mfma_f32_16x16x32_bf16 v[6:9], v[198:201], v[244:247], v[2:5]
	v_mfma_f32_16x16x32_bf16 v[2:5], v[202:205], v[240:243], v[126:129]
	v_mfma_f32_16x16x32_bf16 v[2:5], v[206:209], v[244:247], v[2:5]
	s_barrier
	s_setprio 0
	s_andn2_b64 vcc, exec, s[50:51]
	s_cbranch_vccnz .LBB0_1075
	s_add_u32 s57, s28, 0x200
	s_addc_u32 s78, s29, 0
	s_add_u32 s26, s26, 0x1c000
	s_addc_u32 s27, s27, 0
	s_mov_b32 s79, 4
.LBB0_1074:
	ds_read_b128 v[126:129], v114
	ds_read_b128 v[130:133], v114 offset:1024
	ds_read_b128 v[134:137], v114 offset:2048
	ds_read_b128 v[138:141], v114 offset:3072
	ds_read_b128 v[142:145], v115
	ds_read_b128 v[146:149], v115 offset:1024
	ds_read_b128 v[150:153], v115 offset:2048
	ds_read_b128 v[154:157], v115 offset:3072
	s_add_u32 s28, s26, 0x4000
	s_addc_u32 s29, s27, 0
	s_cmp_eq_u32 s60, s79
	s_cselect_b32 s34, s42, s28
	s_cselect_b32 s35, s43, s29
	s_cselect_b32 s30, s44, s57
	s_cselect_b32 s31, s45, s78
	s_add_u32 s28, s34, 0x8000
	s_addc_u32 s29, s35, 0
	s_mov_b32 m0, s21
	ds_read_b128 v[158:161], v238
	ds_read_b128 v[170:173], v238 offset:1024
	ds_read_b128 v[174:177], v238 offset:2048
	ds_read_b128 v[178:181], v238 offset:3072
	ds_read_b128 v[182:185], v238 offset:4096
	ds_read_b128 v[186:189], v238 offset:5120
	ds_read_b128 v[194:197], v238 offset:6144
	ds_read_b128 v[198:201], v238 offset:7168
	s_nop 0
	global_load_lds_dwordx4 v236, s[26:27]
	s_mov_b32 m0, s70
	s_nop 0
	global_load_lds_dwordx4 v235, s[26:27]
	s_waitcnt vmcnt(8)
	s_waitcnt lgkmcnt(0)
	s_setprio 1
	s_barrier
	s_waitcnt lgkmcnt(0)
	v_mfma_f32_16x16x32_bf16 v[162:165], v[126:129], v[158:161], v[162:165]
	v_mfma_f32_16x16x32_bf16 v[166:169], v[134:137], v[158:161], v[166:169]
	v_mfma_f32_16x16x32_bf16 v[110:113], v[126:129], v[174:177], v[110:113]
	v_mfma_f32_16x16x32_bf16 v[106:109], v[134:137], v[174:177], v[106:109]
	v_mfma_f32_16x16x32_bf16 v[94:97], v[126:129], v[182:185], v[94:97]
	v_mfma_f32_16x16x32_bf16 v[90:93], v[134:137], v[182:185], v[90:93]
	v_mfma_f32_16x16x32_bf16 v[70:73], v[126:129], v[194:197], v[70:73]
	v_mfma_f32_16x16x32_bf16 v[66:69], v[134:137], v[194:197], v[66:69]
	v_mfma_f32_16x16x32_bf16 v[162:165], v[130:133], v[170:173], v[162:165]
	v_mfma_f32_16x16x32_bf16 v[166:169], v[138:141], v[170:173], v[166:169]
	v_mfma_f32_16x16x32_bf16 v[110:113], v[130:133], v[178:181], v[110:113]
	v_mfma_f32_16x16x32_bf16 v[106:109], v[138:141], v[178:181], v[106:109]
	v_mfma_f32_16x16x32_bf16 v[94:97], v[130:133], v[186:189], v[94:97]
	v_mfma_f32_16x16x32_bf16 v[90:93], v[138:141], v[186:189], v[90:93]
	v_mfma_f32_16x16x32_bf16 v[70:73], v[130:133], v[198:201], v[70:73]
	v_mfma_f32_16x16x32_bf16 v[66:69], v[138:141], v[198:201], v[66:69]
	s_setprio 0
	s_setprio 1
	v_mfma_f32_16x16x32_bf16 v[122:125], v[142:145], v[158:161], v[122:125]
	v_mfma_f32_16x16x32_bf16 v[118:121], v[150:153], v[158:161], v[118:121]
	v_mfma_f32_16x16x32_bf16 v[102:105], v[142:145], v[174:177], v[102:105]
	v_mfma_f32_16x16x32_bf16 v[98:101], v[150:153], v[174:177], v[98:101]
	v_mfma_f32_16x16x32_bf16 v[86:89], v[142:145], v[182:185], v[86:89]
	v_mfma_f32_16x16x32_bf16 v[82:85], v[150:153], v[182:185], v[82:85]
	v_mfma_f32_16x16x32_bf16 v[54:57], v[142:145], v[194:197], v[54:57]
	v_mfma_f32_16x16x32_bf16 v[50:53], v[150:153], v[194:197], v[50:53]
	v_mfma_f32_16x16x32_bf16 v[122:125], v[146:149], v[170:173], v[122:125]
	v_mfma_f32_16x16x32_bf16 v[118:121], v[154:157], v[170:173], v[118:121]
	v_mfma_f32_16x16x32_bf16 v[102:105], v[146:149], v[178:181], v[102:105]
	v_mfma_f32_16x16x32_bf16 v[98:101], v[154:157], v[178:181], v[98:101]
	v_mfma_f32_16x16x32_bf16 v[86:89], v[146:149], v[186:189], v[86:89]
	v_mfma_f32_16x16x32_bf16 v[82:85], v[154:157], v[186:189], v[82:85]
	v_mfma_f32_16x16x32_bf16 v[54:57], v[146:149], v[198:201], v[54:57]
	v_mfma_f32_16x16x32_bf16 v[50:53], v[154:157], v[198:201], v[50:53]
	s_barrier
	s_setprio 0
	s_mov_b32 m0, s71
	ds_read_b128 v[158:161], v238 offset:16384
	ds_read_b128 v[170:173], v238 offset:17408
	ds_read_b128 v[174:177], v238 offset:18432
	ds_read_b128 v[178:181], v238 offset:19456
	ds_read_b128 v[182:185], v238 offset:20480
	ds_read_b128 v[186:189], v238 offset:21504
	ds_read_b128 v[194:197], v238 offset:22528
	ds_read_b128 v[198:201], v238 offset:23552
	s_add_u32 s54, s30, s36
	global_load_lds_dwordx4 v0, s[30:31]
	s_mov_b32 m0, s72
	s_addc_u32 s55, s31, s37
	global_load_lds_dwordx4 v210, s[30:31]
	s_mov_b32 m0, s73
	s_nop 0
	global_load_lds_dwordx4 v0, s[54:55]
	s_mov_b32 m0, s74
	s_nop 0
	global_load_lds_dwordx4 v210, s[54:55]
	s_mov_b32 m0, s20
	s_nop 0
	global_load_lds_dwordx4 v236, s[34:35]
	s_mov_b32 m0, s25
	s_nop 0
	global_load_lds_dwordx4 v235, s[34:35]
	s_waitcnt vmcnt(8)
	s_waitcnt lgkmcnt(0)
	s_setprio 1
	s_barrier
	s_waitcnt lgkmcnt(0)
	v_mfma_f32_16x16x32_bf16 v[78:81], v[126:129], v[158:161], v[78:81]
	v_mfma_f32_16x16x32_bf16 v[74:77], v[134:137], v[158:161], v[74:77]
	v_mfma_f32_16x16x32_bf16 v[46:49], v[126:129], v[174:177], v[46:49]
	v_mfma_f32_16x16x32_bf16 v[42:45], v[134:137], v[174:177], v[42:45]
	v_mfma_f32_16x16x32_bf16 v[30:33], v[126:129], v[182:185], v[30:33]
	v_mfma_f32_16x16x32_bf16 v[26:29], v[134:137], v[182:185], v[26:29]
	v_mfma_f32_16x16x32_bf16 v[14:17], v[126:129], v[194:197], v[14:17]
	v_mfma_f32_16x16x32_bf16 v[10:13], v[134:137], v[194:197], v[10:13]
	v_mfma_f32_16x16x32_bf16 v[78:81], v[130:133], v[170:173], v[78:81]
	v_mfma_f32_16x16x32_bf16 v[74:77], v[138:141], v[170:173], v[74:77]
	v_mfma_f32_16x16x32_bf16 v[46:49], v[130:133], v[178:181], v[46:49]
	v_mfma_f32_16x16x32_bf16 v[42:45], v[138:141], v[178:181], v[42:45]
	v_mfma_f32_16x16x32_bf16 v[30:33], v[130:133], v[186:189], v[30:33]
	v_mfma_f32_16x16x32_bf16 v[26:29], v[138:141], v[186:189], v[26:29]
	v_mfma_f32_16x16x32_bf16 v[14:17], v[130:133], v[198:201], v[14:17]
	v_mfma_f32_16x16x32_bf16 v[10:13], v[138:141], v[198:201], v[10:13]
	s_setprio 0
	s_setprio 1
	v_mfma_f32_16x16x32_bf16 v[62:65], v[142:145], v[158:161], v[62:65]
	v_mfma_f32_16x16x32_bf16 v[58:61], v[150:153], v[158:161], v[58:61]
	v_mfma_f32_16x16x32_bf16 v[38:41], v[142:145], v[174:177], v[38:41]
	v_mfma_f32_16x16x32_bf16 v[34:37], v[150:153], v[174:177], v[34:37]
	v_mfma_f32_16x16x32_bf16 v[22:25], v[142:145], v[182:185], v[22:25]
	v_mfma_f32_16x16x32_bf16 v[18:21], v[150:153], v[182:185], v[18:21]
	v_mfma_f32_16x16x32_bf16 v[6:9], v[142:145], v[194:197], v[6:9]
	v_mfma_f32_16x16x32_bf16 v[2:5], v[150:153], v[194:197], v[2:5]
	v_mfma_f32_16x16x32_bf16 v[62:65], v[146:149], v[170:173], v[62:65]
	v_mfma_f32_16x16x32_bf16 v[58:61], v[154:157], v[170:173], v[58:61]
	v_mfma_f32_16x16x32_bf16 v[38:41], v[146:149], v[178:181], v[38:41]
	v_mfma_f32_16x16x32_bf16 v[34:37], v[154:157], v[178:181], v[34:37]
	v_mfma_f32_16x16x32_bf16 v[22:25], v[146:149], v[186:189], v[22:25]
	v_mfma_f32_16x16x32_bf16 v[18:21], v[154:157], v[186:189], v[18:21]
	v_mfma_f32_16x16x32_bf16 v[6:9], v[146:149], v[198:201], v[6:9]
	v_mfma_f32_16x16x32_bf16 v[2:5], v[154:157], v[198:201], v[2:5]
	s_barrier
	s_setprio 0
	ds_read_b128 v[126:129], v116
	ds_read_b128 v[130:133], v116 offset:1024
	ds_read_b128 v[134:137], v116 offset:2048
	ds_read_b128 v[138:141], v116 offset:3072
	ds_read_b128 v[142:145], v117
	ds_read_b128 v[146:149], v117 offset:1024
	ds_read_b128 v[150:153], v117 offset:2048
	ds_read_b128 v[154:157], v117 offset:3072
	s_add_u32 s34, s34, 0x4000
	s_addc_u32 s35, s35, 0
	s_mov_b32 m0, s58
	ds_read_b128 v[158:161], v238 offset:32768
	ds_read_b128 v[170:173], v238 offset:33792
	ds_read_b128 v[174:177], v238 offset:34816
	ds_read_b128 v[178:181], v238 offset:35840
	ds_read_b128 v[182:185], v238 offset:36864
	ds_read_b128 v[186:189], v238 offset:37888
	ds_read_b128 v[194:197], v238 offset:38912
	ds_read_b128 v[198:201], v238 offset:39936
	s_nop 0
	global_load_lds_dwordx4 v236, s[34:35]
	s_mov_b32 m0, s59
	s_nop 0
	global_load_lds_dwordx4 v235, s[34:35]
	s_waitcnt vmcnt(8)
	s_waitcnt lgkmcnt(0)
	s_setprio 1
	s_barrier
	s_waitcnt lgkmcnt(0)
	v_mfma_f32_16x16x32_bf16 v[162:165], v[126:129], v[158:161], v[162:165]
	v_mfma_f32_16x16x32_bf16 v[166:169], v[134:137], v[158:161], v[166:169]
	v_mfma_f32_16x16x32_bf16 v[110:113], v[126:129], v[174:177], v[110:113]
	v_mfma_f32_16x16x32_bf16 v[106:109], v[134:137], v[174:177], v[106:109]
	v_mfma_f32_16x16x32_bf16 v[94:97], v[126:129], v[182:185], v[94:97]
	v_mfma_f32_16x16x32_bf16 v[90:93], v[134:137], v[182:185], v[90:93]
	v_mfma_f32_16x16x32_bf16 v[70:73], v[126:129], v[194:197], v[70:73]
	v_mfma_f32_16x16x32_bf16 v[66:69], v[134:137], v[194:197], v[66:69]
	v_mfma_f32_16x16x32_bf16 v[162:165], v[130:133], v[170:173], v[162:165]
	v_mfma_f32_16x16x32_bf16 v[166:169], v[138:141], v[170:173], v[166:169]
	v_mfma_f32_16x16x32_bf16 v[110:113], v[130:133], v[178:181], v[110:113]
	v_mfma_f32_16x16x32_bf16 v[106:109], v[138:141], v[178:181], v[106:109]
	v_mfma_f32_16x16x32_bf16 v[94:97], v[130:133], v[186:189], v[94:97]
	v_mfma_f32_16x16x32_bf16 v[90:93], v[138:141], v[186:189], v[90:93]
	v_mfma_f32_16x16x32_bf16 v[70:73], v[130:133], v[198:201], v[70:73]
	v_mfma_f32_16x16x32_bf16 v[66:69], v[138:141], v[198:201], v[66:69]
	s_setprio 0
	s_setprio 1
	v_mfma_f32_16x16x32_bf16 v[122:125], v[142:145], v[158:161], v[122:125]
	v_mfma_f32_16x16x32_bf16 v[118:121], v[150:153], v[158:161], v[118:121]
	v_mfma_f32_16x16x32_bf16 v[102:105], v[142:145], v[174:177], v[102:105]
	v_mfma_f32_16x16x32_bf16 v[98:101], v[150:153], v[174:177], v[98:101]
	v_mfma_f32_16x16x32_bf16 v[86:89], v[142:145], v[182:185], v[86:89]
	v_mfma_f32_16x16x32_bf16 v[82:85], v[150:153], v[182:185], v[82:85]
	v_mfma_f32_16x16x32_bf16 v[54:57], v[142:145], v[194:197], v[54:57]
	v_mfma_f32_16x16x32_bf16 v[50:53], v[150:153], v[194:197], v[50:53]
	v_mfma_f32_16x16x32_bf16 v[122:125], v[146:149], v[170:173], v[122:125]
	v_mfma_f32_16x16x32_bf16 v[118:121], v[154:157], v[170:173], v[118:121]
	v_mfma_f32_16x16x32_bf16 v[102:105], v[146:149], v[178:181], v[102:105]
	v_mfma_f32_16x16x32_bf16 v[98:101], v[154:157], v[178:181], v[98:101]
	v_mfma_f32_16x16x32_bf16 v[86:89], v[146:149], v[186:189], v[86:89]
	v_mfma_f32_16x16x32_bf16 v[82:85], v[154:157], v[186:189], v[82:85]
	v_mfma_f32_16x16x32_bf16 v[54:57], v[146:149], v[198:201], v[54:57]
	v_mfma_f32_16x16x32_bf16 v[50:53], v[154:157], v[198:201], v[50:53]
	s_barrier
	s_setprio 0
	ds_read_b128 v[158:161], v238 offset:49152
	ds_read_b128 v[170:173], v238 offset:50176
	ds_read_b128 v[174:177], v238 offset:51200
	ds_read_b128 v[178:181], v238 offset:52224
	ds_read_b128 v[182:185], v238 offset:53248
	ds_read_b128 v[186:189], v238 offset:54272
	ds_read_b128 v[194:197], v238 offset:55296
	ds_read_b128 v[198:201], v238 offset:56320
	s_mov_b32 m0, s75
	v_lshl_add_u64 v[190:191], s[30:31], 0, v[0:1]
	v_lshl_add_u64 v[190:191], v[190:191], 0, s[16:17]
	v_mov_b32_e32 v211, v1
	global_load_lds_dwordx4 v[190:191], off
	s_mov_b32 m0, s76
	v_lshl_add_u64 v[190:191], s[30:31], 0, v[210:211]
	v_lshl_add_u64 v[190:191], v[190:191], 0, s[16:17]
	global_load_lds_dwordx4 v[190:191], off
	s_mov_b32 m0, s77
	v_lshl_add_u64 v[190:191], s[54:55], 0, v[0:1]
	v_lshl_add_u64 v[190:191], v[190:191], 0, s[16:17]
	global_load_lds_dwordx4 v[190:191], off
	s_mov_b32 m0, s56
	v_lshl_add_u64 v[190:191], s[54:55], 0, v[210:211]
	v_lshl_add_u64 v[190:191], v[190:191], 0, s[16:17]
	global_load_lds_dwordx4 v[190:191], off
	s_mov_b32 m0, s62
	s_nop 0
	global_load_lds_dwordx4 v236, s[28:29]
	s_mov_b32 m0, s63
	s_nop 0
	global_load_lds_dwordx4 v235, s[28:29]
	s_waitcnt vmcnt(8)
	s_waitcnt lgkmcnt(0)
	s_setprio 1
	s_barrier
	s_waitcnt lgkmcnt(0)
	v_mfma_f32_16x16x32_bf16 v[78:81], v[126:129], v[158:161], v[78:81]
	v_mfma_f32_16x16x32_bf16 v[74:77], v[134:137], v[158:161], v[74:77]
	v_mfma_f32_16x16x32_bf16 v[46:49], v[126:129], v[174:177], v[46:49]
	v_mfma_f32_16x16x32_bf16 v[42:45], v[134:137], v[174:177], v[42:45]
	v_mfma_f32_16x16x32_bf16 v[30:33], v[126:129], v[182:185], v[30:33]
	v_mfma_f32_16x16x32_bf16 v[26:29], v[134:137], v[182:185], v[26:29]
	v_mfma_f32_16x16x32_bf16 v[14:17], v[126:129], v[194:197], v[14:17]
	v_mfma_f32_16x16x32_bf16 v[10:13], v[134:137], v[194:197], v[10:13]
	v_mfma_f32_16x16x32_bf16 v[78:81], v[130:133], v[170:173], v[78:81]
	v_mfma_f32_16x16x32_bf16 v[74:77], v[138:141], v[170:173], v[74:77]
	v_mfma_f32_16x16x32_bf16 v[46:49], v[130:133], v[178:181], v[46:49]
	v_mfma_f32_16x16x32_bf16 v[42:45], v[138:141], v[178:181], v[42:45]
	v_mfma_f32_16x16x32_bf16 v[30:33], v[130:133], v[186:189], v[30:33]
	v_mfma_f32_16x16x32_bf16 v[26:29], v[138:141], v[186:189], v[26:29]
	v_mfma_f32_16x16x32_bf16 v[14:17], v[130:133], v[198:201], v[14:17]
	v_mfma_f32_16x16x32_bf16 v[10:13], v[138:141], v[198:201], v[10:13]
	s_setprio 0
	s_setprio 1
	v_mfma_f32_16x16x32_bf16 v[62:65], v[142:145], v[158:161], v[62:65]
	v_mfma_f32_16x16x32_bf16 v[58:61], v[150:153], v[158:161], v[58:61]
	v_mfma_f32_16x16x32_bf16 v[38:41], v[142:145], v[174:177], v[38:41]
	v_mfma_f32_16x16x32_bf16 v[34:37], v[150:153], v[174:177], v[34:37]
	v_mfma_f32_16x16x32_bf16 v[22:25], v[142:145], v[182:185], v[22:25]
	v_mfma_f32_16x16x32_bf16 v[18:21], v[150:153], v[182:185], v[18:21]
	v_mfma_f32_16x16x32_bf16 v[6:9], v[142:145], v[194:197], v[6:9]
	v_mfma_f32_16x16x32_bf16 v[2:5], v[150:153], v[194:197], v[2:5]
	v_mfma_f32_16x16x32_bf16 v[62:65], v[146:149], v[170:173], v[62:65]
	v_mfma_f32_16x16x32_bf16 v[58:61], v[154:157], v[170:173], v[58:61]
	v_mfma_f32_16x16x32_bf16 v[38:41], v[146:149], v[178:181], v[38:41]
	v_mfma_f32_16x16x32_bf16 v[34:37], v[154:157], v[178:181], v[34:37]
	v_mfma_f32_16x16x32_bf16 v[22:25], v[146:149], v[186:189], v[22:25]
	v_mfma_f32_16x16x32_bf16 v[18:21], v[154:157], v[186:189], v[18:21]
	v_mfma_f32_16x16x32_bf16 v[6:9], v[146:149], v[198:201], v[6:9]
	v_mfma_f32_16x16x32_bf16 v[2:5], v[154:157], v[198:201], v[2:5]
	s_barrier
	s_setprio 0
	s_add_i32 s28, s79, 2
	s_add_u32 s57, s57, 0x100
	s_addc_u32 s78, s78, 0
	s_add_u32 s26, s26, 0x10000
	s_addc_u32 s27, s27, 0
	s_cmp_lt_i32 s79, s60
	s_mov_b32 s79, s28
	s_cbranch_scc1 .LBB0_1074

.LBB0_1147:
	s_or_b64 exec, exec, s[58:59]
	s_add_u32 s60, s54, 0x10000
	s_addc_u32 s61, s55, 0
	s_and_b64 s[58:59], s[34:35], exec
	s_cselect_b32 s65, s49, s61
	s_cselect_b32 s64, s48, s60
	s_add_u32 s60, s56, 0x10000
	s_addc_u32 s61, s57, 0
	s_and_b64 s[58:59], s[34:35], exec
	s_cselect_b32 s61, s51, s61
	s_cselect_b32 s60, s50, s60
	s_add_u32 s58, s64, 0x8000
	s_addc_u32 s59, s65, 0
	s_add_u32 s62, s60, 0x8000
	s_addc_u32 s63, s61, 0
	s_add_i32 s82, 0, 0x10000
	s_add_i32 s83, 0, 0x14000
	v_add_u32_e32 v132, s82, v140
	v_add_u32_e32 v133, s83, v140
	ds_read_b128 v[2:5], v132
	ds_read_b128 v[6:9], v132 offset:1024
	ds_read_b128 v[10:13], v132 offset:2048
	ds_read_b128 v[14:17], v132 offset:3072
	ds_read_b128 v[18:21], v133
	ds_read_b128 v[22:25], v133 offset:1024
	ds_read_b128 v[26:29], v133 offset:2048
	ds_read_b128 v[30:33], v133 offset:3072
	s_add_u32 s80, s54, 0xc000
	s_addc_u32 s81, s55, 0
	s_add_i32 s78, s15, 0xc000
	s_mov_b32 m0, s78
	s_add_i32 s79, s15, 0xe000
	ds_read_b128 v[34:37], v142
	ds_read_b128 v[38:41], v142 offset:1024
	ds_read_b128 v[42:45], v142 offset:2048
	ds_read_b128 v[46:49], v142 offset:3072
	ds_read_b128 v[50:53], v142 offset:4096
	ds_read_b128 v[54:57], v142 offset:5120
	ds_read_b128 v[58:61], v142 offset:6144
	ds_read_b128 v[62:65], v142 offset:7168
	s_nop 0
	global_load_lds_dwordx4 v136, s[80:81]
	s_mov_b32 m0, s79
	s_nop 0
	global_load_lds_dwordx4 v138, s[80:81]
	s_waitcnt vmcnt(8)
	s_waitcnt lgkmcnt(0)
	s_setprio 1
	s_barrier
	s_waitcnt lgkmcnt(0)
	v_mfma_f32_16x16x32_bf16 v[86:89], v[10:13], v[50:53], 0
	v_mfma_f32_16x16x32_bf16 v[90:93], v[14:17], v[54:57], v[86:89]
	v_mfma_f32_16x16x32_bf16 v[86:89], v[2:5], v[58:61], 0
	v_mfma_f32_16x16x32_bf16 v[66:69], v[2:5], v[34:37], 0
	v_mfma_f32_16x16x32_bf16 v[70:73], v[10:13], v[34:37], 0
	v_mfma_f32_16x16x32_bf16 v[74:77], v[2:5], v[42:45], 0
	v_mfma_f32_16x16x32_bf16 v[78:81], v[10:13], v[42:45], 0
	v_mfma_f32_16x16x32_bf16 v[82:85], v[2:5], v[50:53], 0
	v_mfma_f32_16x16x32_bf16 v[94:97], v[6:9], v[62:65], v[86:89]
	v_mfma_f32_16x16x32_bf16 v[86:89], v[10:13], v[58:61], 0
	v_mfma_f32_16x16x32_bf16 v[66:69], v[6:9], v[38:41], v[66:69]
	v_mfma_f32_16x16x32_bf16 v[70:73], v[14:17], v[38:41], v[70:73]
	v_mfma_f32_16x16x32_bf16 v[74:77], v[6:9], v[46:49], v[74:77]
	v_mfma_f32_16x16x32_bf16 v[78:81], v[14:17], v[46:49], v[78:81]
	v_mfma_f32_16x16x32_bf16 v[82:85], v[6:9], v[54:57], v[82:85]
	v_mfma_f32_16x16x32_bf16 v[106:109], v[14:17], v[62:65], v[86:89]
	s_setprio 0
	s_setprio 1
	v_mfma_f32_16x16x32_bf16 v[86:89], v[18:21], v[34:37], 0
	v_mfma_f32_16x16x32_bf16 v[34:37], v[26:29], v[34:37], 0
	v_mfma_f32_16x16x32_bf16 v[110:113], v[22:25], v[38:41], v[86:89]
	v_mfma_f32_16x16x32_bf16 v[34:37], v[30:33], v[38:41], v[34:37]
	v_mfma_f32_16x16x32_bf16 v[38:41], v[18:21], v[42:45], 0
	v_mfma_f32_16x16x32_bf16 v[42:45], v[26:29], v[42:45], 0
	v_mfma_f32_16x16x32_bf16 v[38:41], v[22:25], v[46:49], v[38:41]
	v_mfma_f32_16x16x32_bf16 v[42:45], v[30:33], v[46:49], v[42:45]
	v_mfma_f32_16x16x32_bf16 v[46:49], v[18:21], v[50:53], 0
	v_mfma_f32_16x16x32_bf16 v[50:53], v[26:29], v[50:53], 0
	v_mfma_f32_16x16x32_bf16 v[46:49], v[22:25], v[54:57], v[46:49]
	v_mfma_f32_16x16x32_bf16 v[50:53], v[30:33], v[54:57], v[50:53]
	v_mfma_f32_16x16x32_bf16 v[54:57], v[18:21], v[58:61], 0
	v_mfma_f32_16x16x32_bf16 v[144:147], v[22:25], v[62:65], v[54:57]
	v_mfma_f32_16x16x32_bf16 v[54:57], v[26:29], v[58:61], 0
	v_mfma_f32_16x16x32_bf16 v[58:61], v[30:33], v[62:65], v[54:57]
	s_barrier
	s_setprio 0
	s_add_i32 s80, s82, s14
	s_add_i32 s81, s80, 0x2000
	s_mov_b32 m0, s80
	s_add_u32 s84, s60, 0x4000
	s_nop 0
	ds_read_b128 v[54:57], v142 offset:16384
	ds_read_b128 v[62:65], v142 offset:17408
	ds_read_b128 v[86:89], v142 offset:18432
	ds_read_b128 v[98:101], v142 offset:19456
	ds_read_b128 v[102:105], v142 offset:20480
	ds_read_b128 v[114:117], v142 offset:21504
	ds_read_b128 v[118:121], v142 offset:22528
	ds_read_b128 v[122:125], v142 offset:23552
	s_addc_u32 s85, s61, 0
	global_load_lds_dwordx4 v137, s[60:61]
	s_mov_b32 m0, s81
	s_add_i32 s82, s83, s14
	s_add_i32 s83, s82, 0x2000
	global_load_lds_dwordx4 v139, s[60:61]
	s_mov_b32 m0, s82
	s_nop 0
	global_load_lds_dwordx4 v137, s[84:85]
	s_mov_b32 m0, s83
	s_nop 0
	global_load_lds_dwordx4 v139, s[84:85]
	s_mov_b32 m0, s15
	s_nop 0
	global_load_lds_dwordx4 v136, s[64:65]
	s_mov_b32 m0, s18
	s_nop 0
	global_load_lds_dwordx4 v138, s[64:65]
	s_waitcnt vmcnt(8)
	s_waitcnt lgkmcnt(0)
	s_setprio 1
	s_barrier
	s_waitcnt lgkmcnt(0)
	v_mfma_f32_16x16x32_bf16 v[126:129], v[2:5], v[54:57], 0
	v_mfma_f32_16x16x32_bf16 v[148:151], v[6:9], v[62:65], v[126:129]
	v_mfma_f32_16x16x32_bf16 v[126:129], v[10:13], v[54:57], 0
	v_mfma_f32_16x16x32_bf16 v[152:155], v[14:17], v[62:65], v[126:129]
	v_mfma_f32_16x16x32_bf16 v[126:129], v[2:5], v[86:89], 0
	v_mfma_f32_16x16x32_bf16 v[156:159], v[6:9], v[98:101], v[126:129]
	v_mfma_f32_16x16x32_bf16 v[126:129], v[10:13], v[86:89], 0
	v_mfma_f32_16x16x32_bf16 v[160:163], v[14:17], v[98:101], v[126:129]
	v_mfma_f32_16x16x32_bf16 v[126:129], v[2:5], v[102:105], 0
	v_mfma_f32_16x16x32_bf16 v[2:5], v[2:5], v[118:121], 0
	v_mfma_f32_16x16x32_bf16 v[164:167], v[6:9], v[114:117], v[126:129]
	v_mfma_f32_16x16x32_bf16 v[2:5], v[6:9], v[122:125], v[2:5]
	v_mfma_f32_16x16x32_bf16 v[6:9], v[10:13], v[118:121], 0
	v_mfma_f32_16x16x32_bf16 v[126:129], v[10:13], v[102:105], 0
	v_mfma_f32_16x16x32_bf16 v[10:13], v[14:17], v[122:125], v[6:9]
	v_mfma_f32_16x16x32_bf16 v[168:171], v[14:17], v[114:117], v[126:129]
	s_setprio 0
	s_setprio 1
	v_mfma_f32_16x16x32_bf16 v[6:9], v[18:21], v[54:57], 0
	v_mfma_f32_16x16x32_bf16 v[14:17], v[22:25], v[62:65], v[6:9]
	v_mfma_f32_16x16x32_bf16 v[6:9], v[26:29], v[54:57], 0
	v_mfma_f32_16x16x32_bf16 v[172:175], v[30:33], v[62:65], v[6:9]
	v_mfma_f32_16x16x32_bf16 v[6:9], v[18:21], v[86:89], 0
	v_mfma_f32_16x16x32_bf16 v[176:179], v[22:25], v[98:101], v[6:9]
	v_mfma_f32_16x16x32_bf16 v[6:9], v[26:29], v[86:89], 0
	v_mfma_f32_16x16x32_bf16 v[180:183], v[30:33], v[98:101], v[6:9]
	v_mfma_f32_16x16x32_bf16 v[6:9], v[18:21], v[102:105], 0
	v_mfma_f32_16x16x32_bf16 v[184:187], v[22:25], v[114:117], v[6:9]
	v_mfma_f32_16x16x32_bf16 v[6:9], v[26:29], v[102:105], 0
	v_mfma_f32_16x16x32_bf16 v[188:191], v[30:33], v[114:117], v[6:9]
	v_mfma_f32_16x16x32_bf16 v[6:9], v[18:21], v[118:121], 0
	v_mfma_f32_16x16x32_bf16 v[194:197], v[22:25], v[122:125], v[6:9]
	v_mfma_f32_16x16x32_bf16 v[6:9], v[26:29], v[118:121], 0
	v_mfma_f32_16x16x32_bf16 v[198:201], v[30:33], v[122:125], v[6:9]
	s_barrier
	s_setprio 0
	s_add_i32 s84, 0, 0x18000
	s_add_i32 s85, 0, 0x1c000
	v_add_u32_e32 v134, s84, v140
	v_add_u32_e32 v135, s85, v140
	s_nop 0
	ds_read_b128 v[6:9], v134
	ds_read_b128 v[26:29], v134 offset:1024
	ds_read_b128 v[30:33], v134 offset:2048
	ds_read_b128 v[202:205], v134 offset:3072
	ds_read_b128 v[206:209], v135
	ds_read_b128 v[210:213], v135 offset:1024
	ds_read_b128 v[214:217], v135 offset:2048
	ds_read_b128 v[218:221], v135 offset:3072
	s_add_u32 s64, s64, 0x4000
	s_addc_u32 s65, s65, 0
	s_mov_b32 m0, s20
	ds_read_b128 v[18:21], v142 offset:32768
	ds_read_b128 v[22:25], v142 offset:33792
	ds_read_b128 v[222:225], v142 offset:34816
	ds_read_b128 v[226:229], v142 offset:35840
	ds_read_b128 v[232:235], v142 offset:36864
	ds_read_b128 v[236:239], v142 offset:37888
	ds_read_b128 v[240:243], v142 offset:38912
	ds_read_b128 v[244:247], v142 offset:39936
	s_nop 0
	global_load_lds_dwordx4 v136, s[64:65]
	s_mov_b32 m0, s21
	s_nop 0
	global_load_lds_dwordx4 v138, s[64:65]
	s_waitcnt vmcnt(8)
	s_waitcnt lgkmcnt(0)
	s_setprio 1
	s_barrier
	s_waitcnt lgkmcnt(0)
	v_mfma_f32_16x16x32_bf16 v[54:57], v[6:9], v[18:21], v[66:69]
	v_mfma_f32_16x16x32_bf16 v[118:121], v[26:29], v[22:25], v[54:57]
	v_mfma_f32_16x16x32_bf16 v[54:57], v[30:33], v[18:21], v[70:73]
	v_mfma_f32_16x16x32_bf16 v[114:117], v[202:205], v[22:25], v[54:57]
	v_mfma_f32_16x16x32_bf16 v[54:57], v[6:9], v[222:225], v[74:77]
	v_mfma_f32_16x16x32_bf16 v[102:105], v[26:29], v[226:229], v[54:57]
	v_mfma_f32_16x16x32_bf16 v[54:57], v[30:33], v[222:225], v[78:81]
	v_mfma_f32_16x16x32_bf16 v[98:101], v[202:205], v[226:229], v[54:57]
	v_mfma_f32_16x16x32_bf16 v[54:57], v[6:9], v[232:235], v[82:85]
	v_mfma_f32_16x16x32_bf16 v[86:89], v[26:29], v[236:239], v[54:57]
	v_mfma_f32_16x16x32_bf16 v[54:57], v[30:33], v[232:235], v[90:93]
	v_mfma_f32_16x16x32_bf16 v[82:85], v[202:205], v[236:239], v[54:57]
	v_mfma_f32_16x16x32_bf16 v[54:57], v[6:9], v[240:243], v[94:97]
	v_mfma_f32_16x16x32_bf16 v[62:65], v[26:29], v[244:247], v[54:57]
	v_mfma_f32_16x16x32_bf16 v[54:57], v[30:33], v[240:243], v[106:109]
	v_mfma_f32_16x16x32_bf16 v[54:57], v[202:205], v[244:247], v[54:57]
	s_setprio 0
	s_setprio 1
	v_mfma_f32_16x16x32_bf16 v[66:69], v[206:209], v[18:21], v[110:113]
	v_mfma_f32_16x16x32_bf16 v[18:21], v[214:217], v[18:21], v[34:37]
	v_mfma_f32_16x16x32_bf16 v[122:125], v[218:221], v[22:25], v[18:21]
	v_mfma_f32_16x16x32_bf16 v[18:21], v[206:209], v[222:225], v[38:41]
	v_mfma_f32_16x16x32_bf16 v[110:113], v[210:213], v[226:229], v[18:21]
	v_mfma_f32_16x16x32_bf16 v[18:21], v[214:217], v[222:225], v[42:45]
	v_mfma_f32_16x16x32_bf16 v[106:109], v[218:221], v[226:229], v[18:21]
	v_mfma_f32_16x16x32_bf16 v[18:21], v[206:209], v[232:235], v[46:49]
	v_mfma_f32_16x16x32_bf16 v[94:97], v[210:213], v[236:239], v[18:21]
	v_mfma_f32_16x16x32_bf16 v[18:21], v[214:217], v[232:235], v[50:53]
	v_mfma_f32_16x16x32_bf16 v[90:93], v[218:221], v[236:239], v[18:21]
	v_mfma_f32_16x16x32_bf16 v[18:21], v[206:209], v[240:243], v[144:147]
	v_mfma_f32_16x16x32_bf16 v[78:81], v[210:213], v[244:247], v[18:21]
	v_mfma_f32_16x16x32_bf16 v[18:21], v[214:217], v[240:243], v[58:61]
	v_mfma_f32_16x16x32_bf16 v[126:129], v[210:213], v[22:25], v[66:69]
	v_mfma_f32_16x16x32_bf16 v[70:73], v[218:221], v[244:247], v[18:21]
	s_barrier
	s_setprio 0
	s_add_i32 s64, s84, s14
	s_add_i32 s65, s64, 0x2000
	s_mov_b32 m0, s64
	s_add_u32 s60, s60, 0xc000
	ds_read_b128 v[42:45], v142 offset:49152
	ds_read_b128 v[46:49], v142 offset:50176
	ds_read_b128 v[144:147], v142 offset:51200
	ds_read_b128 v[222:225], v142 offset:52224
	ds_read_b128 v[226:229], v142 offset:53248
	ds_read_b128 v[232:235], v142 offset:54272
	ds_read_b128 v[236:239], v142 offset:55296
	ds_read_b128 v[240:243], v142 offset:56320
	s_addc_u32 s61, s61, 0
	global_load_lds_dwordx4 v137, s[62:63]
	s_mov_b32 m0, s65
	s_add_i32 s84, s85, s14
	s_add_i32 s85, s84, 0x2000
	global_load_lds_dwordx4 v139, s[62:63]
	s_mov_b32 m0, s84
	s_nop 0
	global_load_lds_dwordx4 v137, s[60:61]
	s_mov_b32 m0, s85
	s_nop 0
	global_load_lds_dwordx4 v139, s[60:61]
	s_mov_b32 m0, s67
	s_nop 0
	global_load_lds_dwordx4 v136, s[58:59]
	s_mov_b32 m0, s68
	s_nop 0
	global_load_lds_dwordx4 v138, s[58:59]
	s_waitcnt vmcnt(8)
	s_waitcnt lgkmcnt(0)
	s_setprio 1
	s_barrier
	s_waitcnt lgkmcnt(0)
	v_mfma_f32_16x16x32_bf16 v[18:21], v[6:9], v[42:45], v[148:151]
	v_mfma_f32_16x16x32_bf16 v[58:61], v[26:29], v[46:49], v[18:21]
	v_mfma_f32_16x16x32_bf16 v[18:21], v[30:33], v[42:45], v[152:155]
	v_mfma_f32_16x16x32_bf16 v[50:53], v[202:205], v[46:49], v[18:21]
	v_mfma_f32_16x16x32_bf16 v[18:21], v[6:9], v[144:147], v[156:159]
	v_mfma_f32_16x16x32_bf16 v[38:41], v[26:29], v[222:225], v[18:21]
	v_mfma_f32_16x16x32_bf16 v[18:21], v[30:33], v[144:147], v[160:163]
	v_mfma_f32_16x16x32_bf16 v[34:37], v[202:205], v[222:225], v[18:21]
	v_mfma_f32_16x16x32_bf16 v[18:21], v[6:9], v[226:229], v[164:167]
	v_mfma_f32_16x16x32_bf16 v[2:5], v[6:9], v[236:239], v[2:5]
	v_mfma_f32_16x16x32_bf16 v[22:25], v[26:29], v[232:235], v[18:21]
	v_mfma_f32_16x16x32_bf16 v[18:21], v[30:33], v[226:229], v[168:171]
	v_mfma_f32_16x16x32_bf16 v[6:9], v[26:29], v[240:243], v[2:5]
	v_mfma_f32_16x16x32_bf16 v[2:5], v[30:33], v[236:239], v[10:13]
	v_mfma_f32_16x16x32_bf16 v[18:21], v[202:205], v[232:235], v[18:21]
	v_mfma_f32_16x16x32_bf16 v[2:5], v[202:205], v[240:243], v[2:5]
	s_setprio 0
	s_setprio 1
	v_mfma_f32_16x16x32_bf16 v[10:13], v[206:209], v[42:45], v[14:17]
	v_mfma_f32_16x16x32_bf16 v[74:77], v[210:213], v[46:49], v[10:13]
	v_mfma_f32_16x16x32_bf16 v[10:13], v[214:217], v[42:45], v[172:175]
	v_mfma_f32_16x16x32_bf16 v[66:69], v[218:221], v[46:49], v[10:13]
	v_mfma_f32_16x16x32_bf16 v[10:13], v[206:209], v[144:147], v[176:179]
	v_mfma_f32_16x16x32_bf16 v[46:49], v[210:213], v[222:225], v[10:13]
	v_mfma_f32_16x16x32_bf16 v[10:13], v[214:217], v[144:147], v[180:183]
	v_mfma_f32_16x16x32_bf16 v[42:45], v[218:221], v[222:225], v[10:13]
	v_mfma_f32_16x16x32_bf16 v[10:13], v[206:209], v[226:229], v[184:187]
	v_mfma_f32_16x16x32_bf16 v[30:33], v[210:213], v[232:235], v[10:13]
	v_mfma_f32_16x16x32_bf16 v[10:13], v[214:217], v[226:229], v[188:191]
	v_mfma_f32_16x16x32_bf16 v[26:29], v[218:221], v[232:235], v[10:13]
	v_mfma_f32_16x16x32_bf16 v[10:13], v[206:209], v[236:239], v[194:197]
	v_mfma_f32_16x16x32_bf16 v[14:17], v[210:213], v[240:243], v[10:13]
	v_mfma_f32_16x16x32_bf16 v[10:13], v[214:217], v[236:239], v[198:201]
	v_mfma_f32_16x16x32_bf16 v[10:13], v[218:221], v[240:243], v[10:13]
	s_barrier
	s_setprio 0
	s_andn2_b64 vcc, exec, s[38:39]
	s_cbranch_vccnz .LBB0_1153
	s_lshl_b32 s58, s72, 10
	s_xor_b32 s86, s58, 0x400
	s_add_u32 s87, s56, 0x20000
	s_addc_u32 s88, s57, 0
	v_ashrrev_i32_e32 v131, 31, v130
	s_add_u32 s54, s54, 0x1c000
	v_lshl_add_u64 v[130:131], v[130:131], 3, s[26:27]
	s_addc_u32 s55, s55, 0
	s_mov_b32 s89, 4

.LBB0_1151:
	s_or_b64 exec, exec, s[58:59]
	ds_read_b128 v[144:147], v132
	ds_read_b128 v[148:151], v132 offset:1024
	ds_read_b128 v[152:155], v132 offset:2048
	ds_read_b128 v[156:159], v132 offset:3072
	ds_read_b128 v[160:163], v133
	ds_read_b128 v[164:167], v133 offset:1024
	ds_read_b128 v[168:171], v133 offset:2048
	ds_read_b128 v[172:175], v133 offset:3072
	s_add_u32 s58, s54, 0x4000
	s_addc_u32 s59, s55, 0
	s_and_b64 s[56:57], s[56:57], exec
	s_cselect_b32 s62, s48, s58
	s_cselect_b32 s63, s49, s59
	s_cselect_b32 s59, s51, s88
	s_cselect_b32 s58, s50, s87
	s_add_u32 s56, s62, 0x8000
	s_addc_u32 s57, s63, 0
	s_add_u32 s60, s58, 0x8000
	s_addc_u32 s61, s59, 0
	s_mov_b32 m0, s78
	ds_read_b128 v[176:179], v142
	ds_read_b128 v[180:183], v142 offset:1024
	ds_read_b128 v[184:187], v142 offset:2048
	ds_read_b128 v[188:191], v142 offset:3072
	ds_read_b128 v[194:197], v142 offset:4096
	ds_read_b128 v[198:201], v142 offset:5120
	ds_read_b128 v[202:205], v142 offset:6144
	ds_read_b128 v[206:209], v142 offset:7168
	s_nop 0
	global_load_lds_dwordx4 v136, s[54:55]
	s_mov_b32 m0, s79
	s_nop 0
	global_load_lds_dwordx4 v138, s[54:55]
	s_waitcnt vmcnt(8)
	s_waitcnt lgkmcnt(0)
	s_setprio 1
	s_barrier
	s_waitcnt lgkmcnt(0)
	v_mfma_f32_16x16x32_bf16 v[118:121], v[144:147], v[176:179], v[118:121]
	v_mfma_f32_16x16x32_bf16 v[114:117], v[152:155], v[176:179], v[114:117]
	v_mfma_f32_16x16x32_bf16 v[102:105], v[144:147], v[184:187], v[102:105]
	v_mfma_f32_16x16x32_bf16 v[98:101], v[152:155], v[184:187], v[98:101]
	v_mfma_f32_16x16x32_bf16 v[86:89], v[144:147], v[194:197], v[86:89]
	v_mfma_f32_16x16x32_bf16 v[82:85], v[152:155], v[194:197], v[82:85]
	v_mfma_f32_16x16x32_bf16 v[62:65], v[144:147], v[202:205], v[62:65]
	v_mfma_f32_16x16x32_bf16 v[54:57], v[152:155], v[202:205], v[54:57]
	v_mfma_f32_16x16x32_bf16 v[118:121], v[148:151], v[180:183], v[118:121]
	v_mfma_f32_16x16x32_bf16 v[114:117], v[156:159], v[180:183], v[114:117]
	v_mfma_f32_16x16x32_bf16 v[102:105], v[148:151], v[188:191], v[102:105]
	v_mfma_f32_16x16x32_bf16 v[98:101], v[156:159], v[188:191], v[98:101]
	v_mfma_f32_16x16x32_bf16 v[86:89], v[148:151], v[198:201], v[86:89]
	v_mfma_f32_16x16x32_bf16 v[82:85], v[156:159], v[198:201], v[82:85]
	v_mfma_f32_16x16x32_bf16 v[62:65], v[148:151], v[206:209], v[62:65]
	v_mfma_f32_16x16x32_bf16 v[54:57], v[156:159], v[206:209], v[54:57]
	s_setprio 0
	s_setprio 1
	v_mfma_f32_16x16x32_bf16 v[126:129], v[160:163], v[176:179], v[126:129]
	v_mfma_f32_16x16x32_bf16 v[122:125], v[168:171], v[176:179], v[122:125]
	v_mfma_f32_16x16x32_bf16 v[110:113], v[160:163], v[184:187], v[110:113]
	v_mfma_f32_16x16x32_bf16 v[106:109], v[168:171], v[184:187], v[106:109]
	v_mfma_f32_16x16x32_bf16 v[94:97], v[160:163], v[194:197], v[94:97]
	v_mfma_f32_16x16x32_bf16 v[90:93], v[168:171], v[194:197], v[90:93]
	v_mfma_f32_16x16x32_bf16 v[78:81], v[160:163], v[202:205], v[78:81]
	v_mfma_f32_16x16x32_bf16 v[70:73], v[168:171], v[202:205], v[70:73]
	v_mfma_f32_16x16x32_bf16 v[126:129], v[164:167], v[180:183], v[126:129]
	v_mfma_f32_16x16x32_bf16 v[122:125], v[172:175], v[180:183], v[122:125]
	v_mfma_f32_16x16x32_bf16 v[110:113], v[164:167], v[188:191], v[110:113]
	v_mfma_f32_16x16x32_bf16 v[106:109], v[172:175], v[188:191], v[106:109]
	v_mfma_f32_16x16x32_bf16 v[94:97], v[164:167], v[198:201], v[94:97]
	v_mfma_f32_16x16x32_bf16 v[90:93], v[172:175], v[198:201], v[90:93]
	v_mfma_f32_16x16x32_bf16 v[78:81], v[164:167], v[206:209], v[78:81]
	v_mfma_f32_16x16x32_bf16 v[70:73], v[172:175], v[206:209], v[70:73]
	s_barrier
	s_setprio 0
	s_mov_b32 m0, s80
	ds_read_b128 v[176:179], v142 offset:16384
	ds_read_b128 v[180:183], v142 offset:17408
	ds_read_b128 v[184:187], v142 offset:18432
	ds_read_b128 v[188:191], v142 offset:19456
	ds_read_b128 v[194:197], v142 offset:20480
	ds_read_b128 v[198:201], v142 offset:21504
	ds_read_b128 v[202:205], v142 offset:22528
	ds_read_b128 v[206:209], v142 offset:23552
	s_add_u32 s90, s58, 0x4000
	global_load_lds_dwordx4 v137, s[58:59]
	s_mov_b32 m0, s81
	s_addc_u32 s91, s59, 0
	global_load_lds_dwordx4 v139, s[58:59]
	s_mov_b32 m0, s82
	s_nop 0
	global_load_lds_dwordx4 v137, s[90:91]
	s_mov_b32 m0, s83
	s_nop 0
	global_load_lds_dwordx4 v139, s[90:91]
	s_mov_b32 m0, s15
	s_nop 0
	global_load_lds_dwordx4 v136, s[62:63]
	s_mov_b32 m0, s18
	s_nop 0
	global_load_lds_dwordx4 v138, s[62:63]
	s_waitcnt vmcnt(8)
	s_waitcnt lgkmcnt(0)
	s_setprio 1
	s_barrier
	s_waitcnt lgkmcnt(0)
	v_mfma_f32_16x16x32_bf16 v[58:61], v[144:147], v[176:179], v[58:61]
	v_mfma_f32_16x16x32_bf16 v[50:53], v[152:155], v[176:179], v[50:53]
	v_mfma_f32_16x16x32_bf16 v[38:41], v[144:147], v[184:187], v[38:41]
	v_mfma_f32_16x16x32_bf16 v[34:37], v[152:155], v[184:187], v[34:37]
	v_mfma_f32_16x16x32_bf16 v[22:25], v[144:147], v[194:197], v[22:25]
	v_mfma_f32_16x16x32_bf16 v[18:21], v[152:155], v[194:197], v[18:21]
	v_mfma_f32_16x16x32_bf16 v[6:9], v[144:147], v[202:205], v[6:9]
	v_mfma_f32_16x16x32_bf16 v[2:5], v[152:155], v[202:205], v[2:5]
	v_mfma_f32_16x16x32_bf16 v[58:61], v[148:151], v[180:183], v[58:61]
	v_mfma_f32_16x16x32_bf16 v[50:53], v[156:159], v[180:183], v[50:53]
	v_mfma_f32_16x16x32_bf16 v[38:41], v[148:151], v[188:191], v[38:41]
	v_mfma_f32_16x16x32_bf16 v[34:37], v[156:159], v[188:191], v[34:37]
	v_mfma_f32_16x16x32_bf16 v[22:25], v[148:151], v[198:201], v[22:25]
	v_mfma_f32_16x16x32_bf16 v[18:21], v[156:159], v[198:201], v[18:21]
	v_mfma_f32_16x16x32_bf16 v[6:9], v[148:151], v[206:209], v[6:9]
	v_mfma_f32_16x16x32_bf16 v[2:5], v[156:159], v[206:209], v[2:5]
	s_setprio 0
	s_setprio 1
	v_mfma_f32_16x16x32_bf16 v[74:77], v[160:163], v[176:179], v[74:77]
	v_mfma_f32_16x16x32_bf16 v[66:69], v[168:171], v[176:179], v[66:69]
	v_mfma_f32_16x16x32_bf16 v[46:49], v[160:163], v[184:187], v[46:49]
	v_mfma_f32_16x16x32_bf16 v[42:45], v[168:171], v[184:187], v[42:45]
	v_mfma_f32_16x16x32_bf16 v[30:33], v[160:163], v[194:197], v[30:33]
	v_mfma_f32_16x16x32_bf16 v[26:29], v[168:171], v[194:197], v[26:29]
	v_mfma_f32_16x16x32_bf16 v[14:17], v[160:163], v[202:205], v[14:17]
	v_mfma_f32_16x16x32_bf16 v[10:13], v[168:171], v[202:205], v[10:13]
	v_mfma_f32_16x16x32_bf16 v[74:77], v[164:167], v[180:183], v[74:77]
	v_mfma_f32_16x16x32_bf16 v[66:69], v[172:175], v[180:183], v[66:69]
	v_mfma_f32_16x16x32_bf16 v[46:49], v[164:167], v[188:191], v[46:49]
	v_mfma_f32_16x16x32_bf16 v[42:45], v[172:175], v[188:191], v[42:45]
	v_mfma_f32_16x16x32_bf16 v[30:33], v[164:167], v[198:201], v[30:33]
	v_mfma_f32_16x16x32_bf16 v[26:29], v[172:175], v[198:201], v[26:29]
	v_mfma_f32_16x16x32_bf16 v[14:17], v[164:167], v[206:209], v[14:17]
	v_mfma_f32_16x16x32_bf16 v[10:13], v[172:175], v[206:209], v[10:13]
	s_barrier
	s_setprio 0
	ds_read_b128 v[144:147], v134
	ds_read_b128 v[148:151], v134 offset:1024
	ds_read_b128 v[152:155], v134 offset:2048
	ds_read_b128 v[156:159], v134 offset:3072
	ds_read_b128 v[160:163], v135
	ds_read_b128 v[164:167], v135 offset:1024
	ds_read_b128 v[168:171], v135 offset:2048
	ds_read_b128 v[172:175], v135 offset:3072
	s_add_u32 s62, s62, 0x4000
	s_addc_u32 s63, s63, 0
	s_mov_b32 m0, s20
	ds_read_b128 v[176:179], v142 offset:32768
	ds_read_b128 v[180:183], v142 offset:33792
	ds_read_b128 v[184:187], v142 offset:34816
	ds_read_b128 v[188:191], v142 offset:35840
	ds_read_b128 v[194:197], v142 offset:36864
	ds_read_b128 v[198:201], v142 offset:37888
	ds_read_b128 v[202:205], v142 offset:38912
	ds_read_b128 v[206:209], v142 offset:39936
	s_nop 0
	global_load_lds_dwordx4 v136, s[62:63]
	s_mov_b32 m0, s21
	s_nop 0
	global_load_lds_dwordx4 v138, s[62:63]
	s_waitcnt vmcnt(8)
	s_waitcnt lgkmcnt(0)
	s_setprio 1
	s_barrier
	s_waitcnt lgkmcnt(0)
	v_mfma_f32_16x16x32_bf16 v[118:121], v[144:147], v[176:179], v[118:121]
	v_mfma_f32_16x16x32_bf16 v[114:117], v[152:155], v[176:179], v[114:117]
	v_mfma_f32_16x16x32_bf16 v[102:105], v[144:147], v[184:187], v[102:105]
	v_mfma_f32_16x16x32_bf16 v[98:101], v[152:155], v[184:187], v[98:101]
	v_mfma_f32_16x16x32_bf16 v[86:89], v[144:147], v[194:197], v[86:89]
	v_mfma_f32_16x16x32_bf16 v[82:85], v[152:155], v[194:197], v[82:85]
	v_mfma_f32_16x16x32_bf16 v[62:65], v[144:147], v[202:205], v[62:65]
	v_mfma_f32_16x16x32_bf16 v[54:57], v[152:155], v[202:205], v[54:57]
	v_mfma_f32_16x16x32_bf16 v[118:121], v[148:151], v[180:183], v[118:121]
	v_mfma_f32_16x16x32_bf16 v[114:117], v[156:159], v[180:183], v[114:117]
	v_mfma_f32_16x16x32_bf16 v[102:105], v[148:151], v[188:191], v[102:105]
	v_mfma_f32_16x16x32_bf16 v[98:101], v[156:159], v[188:191], v[98:101]
	v_mfma_f32_16x16x32_bf16 v[86:89], v[148:151], v[198:201], v[86:89]
	v_mfma_f32_16x16x32_bf16 v[82:85], v[156:159], v[198:201], v[82:85]
	v_mfma_f32_16x16x32_bf16 v[62:65], v[148:151], v[206:209], v[62:65]
	v_mfma_f32_16x16x32_bf16 v[54:57], v[156:159], v[206:209], v[54:57]
	s_setprio 0
	s_setprio 1
	v_mfma_f32_16x16x32_bf16 v[126:129], v[160:163], v[176:179], v[126:129]
	v_mfma_f32_16x16x32_bf16 v[122:125], v[168:171], v[176:179], v[122:125]
	v_mfma_f32_16x16x32_bf16 v[110:113], v[160:163], v[184:187], v[110:113]
	v_mfma_f32_16x16x32_bf16 v[106:109], v[168:171], v[184:187], v[106:109]
	v_mfma_f32_16x16x32_bf16 v[94:97], v[160:163], v[194:197], v[94:97]
	v_mfma_f32_16x16x32_bf16 v[90:93], v[168:171], v[194:197], v[90:93]
	v_mfma_f32_16x16x32_bf16 v[78:81], v[160:163], v[202:205], v[78:81]
	v_mfma_f32_16x16x32_bf16 v[70:73], v[168:171], v[202:205], v[70:73]
	v_mfma_f32_16x16x32_bf16 v[126:129], v[164:167], v[180:183], v[126:129]
	v_mfma_f32_16x16x32_bf16 v[122:125], v[172:175], v[180:183], v[122:125]
	v_mfma_f32_16x16x32_bf16 v[110:113], v[164:167], v[188:191], v[110:113]
	v_mfma_f32_16x16x32_bf16 v[106:109], v[172:175], v[188:191], v[106:109]
	v_mfma_f32_16x16x32_bf16 v[94:97], v[164:167], v[198:201], v[94:97]
	v_mfma_f32_16x16x32_bf16 v[90:93], v[172:175], v[198:201], v[90:93]
	v_mfma_f32_16x16x32_bf16 v[78:81], v[164:167], v[206:209], v[78:81]
	v_mfma_f32_16x16x32_bf16 v[70:73], v[172:175], v[206:209], v[70:73]
	s_barrier
	s_setprio 0
	s_mov_b32 m0, s64
	ds_read_b128 v[176:179], v142 offset:49152
	ds_read_b128 v[180:183], v142 offset:50176
	ds_read_b128 v[184:187], v142 offset:51200
	ds_read_b128 v[188:191], v142 offset:52224
	ds_read_b128 v[194:197], v142 offset:53248
	ds_read_b128 v[198:201], v142 offset:54272
	ds_read_b128 v[202:205], v142 offset:55296
	ds_read_b128 v[206:209], v142 offset:56320
	s_add_u32 s58, s58, 0xc000
	global_load_lds_dwordx4 v137, s[60:61]
	s_mov_b32 m0, s65
	s_addc_u32 s59, s59, 0
	global_load_lds_dwordx4 v139, s[60:61]
	s_mov_b32 m0, s84
	s_nop 0
	global_load_lds_dwordx4 v137, s[58:59]
	s_mov_b32 m0, s85
	s_nop 0
	global_load_lds_dwordx4 v139, s[58:59]
	s_mov_b32 m0, s67
	s_nop 0
	global_load_lds_dwordx4 v136, s[56:57]
	s_mov_b32 m0, s68
	s_nop 0
	global_load_lds_dwordx4 v138, s[56:57]
	s_waitcnt vmcnt(8)
	s_waitcnt lgkmcnt(0)
	s_setprio 1
	s_barrier
	s_waitcnt lgkmcnt(0)
	v_mfma_f32_16x16x32_bf16 v[58:61], v[144:147], v[176:179], v[58:61]
	v_mfma_f32_16x16x32_bf16 v[50:53], v[152:155], v[176:179], v[50:53]
	v_mfma_f32_16x16x32_bf16 v[38:41], v[144:147], v[184:187], v[38:41]
	v_mfma_f32_16x16x32_bf16 v[34:37], v[152:155], v[184:187], v[34:37]
	v_mfma_f32_16x16x32_bf16 v[22:25], v[144:147], v[194:197], v[22:25]
	v_mfma_f32_16x16x32_bf16 v[18:21], v[152:155], v[194:197], v[18:21]
	v_mfma_f32_16x16x32_bf16 v[6:9], v[144:147], v[202:205], v[6:9]
	v_mfma_f32_16x16x32_bf16 v[2:5], v[152:155], v[202:205], v[2:5]
	v_mfma_f32_16x16x32_bf16 v[58:61], v[148:151], v[180:183], v[58:61]
	v_mfma_f32_16x16x32_bf16 v[50:53], v[156:159], v[180:183], v[50:53]
	v_mfma_f32_16x16x32_bf16 v[38:41], v[148:151], v[188:191], v[38:41]
	v_mfma_f32_16x16x32_bf16 v[34:37], v[156:159], v[188:191], v[34:37]
	v_mfma_f32_16x16x32_bf16 v[22:25], v[148:151], v[198:201], v[22:25]
	v_mfma_f32_16x16x32_bf16 v[18:21], v[156:159], v[198:201], v[18:21]
	v_mfma_f32_16x16x32_bf16 v[6:9], v[148:151], v[206:209], v[6:9]
	v_mfma_f32_16x16x32_bf16 v[2:5], v[156:159], v[206:209], v[2:5]
	s_setprio 0
	s_setprio 1
	v_mfma_f32_16x16x32_bf16 v[74:77], v[160:163], v[176:179], v[74:77]
	v_mfma_f32_16x16x32_bf16 v[66:69], v[168:171], v[176:179], v[66:69]
	v_mfma_f32_16x16x32_bf16 v[46:49], v[160:163], v[184:187], v[46:49]
	v_mfma_f32_16x16x32_bf16 v[42:45], v[168:171], v[184:187], v[42:45]
	v_mfma_f32_16x16x32_bf16 v[30:33], v[160:163], v[194:197], v[30:33]
	v_mfma_f32_16x16x32_bf16 v[26:29], v[168:171], v[194:197], v[26:29]
	v_mfma_f32_16x16x32_bf16 v[14:17], v[160:163], v[202:205], v[14:17]
	v_mfma_f32_16x16x32_bf16 v[10:13], v[168:171], v[202:205], v[10:13]
	v_mfma_f32_16x16x32_bf16 v[74:77], v[164:167], v[180:183], v[74:77]
	v_mfma_f32_16x16x32_bf16 v[66:69], v[172:175], v[180:183], v[66:69]
	v_mfma_f32_16x16x32_bf16 v[46:49], v[164:167], v[188:191], v[46:49]
	v_mfma_f32_16x16x32_bf16 v[42:45], v[172:175], v[188:191], v[42:45]
	v_mfma_f32_16x16x32_bf16 v[30:33], v[164:167], v[198:201], v[30:33]
	v_mfma_f32_16x16x32_bf16 v[26:29], v[172:175], v[198:201], v[26:29]
	v_mfma_f32_16x16x32_bf16 v[14:17], v[164:167], v[206:209], v[14:17]
	v_mfma_f32_16x16x32_bf16 v[10:13], v[172:175], v[206:209], v[10:13]
	s_barrier
	s_setprio 0
	s_add_i32 s56, s89, 2
	s_add_u32 s87, s87, 0x10000
	s_addc_u32 s88, s88, 0
	s_add_u32 s54, s54, 0x10000
	s_addc_u32 s55, s55, 0
	s_cmp_lt_i32 s89, s25
	s_cbranch_scc0 .LBB0_1153
	s_mov_b32 s89, s56
	s_branch .LBB0_1149

.LBB0_1225:
	s_add_u32 s34, s26, 0x10000
	s_addc_u32 s35, s27, 0
	s_and_b64 s[30:31], s[46:47], exec
	s_cselect_b32 s53, s39, s35
	s_cselect_b32 s52, s38, s34
	s_add_u32 s65, s28, 0x10000
	s_addc_u32 s66, s29, 0
	s_add_u32 s30, s52, 0x8000
	s_addc_u32 s31, s53, 0
	s_add_i32 s67, 0, 0x10000
	s_and_b64 s[34:35], s[46:47], exec
	s_cselect_b32 s35, s41, s66
	s_cselect_b32 s34, s40, s65
	s_add_i32 s70, 0, 0x14000
	v_add_u32_e32 v114, s67, v236
	v_add_u32_e32 v115, s70, v236
	ds_read_b128 v[2:5], v114
	s_waitcnt lgkmcnt(0)
	ds_read_b128 v[6:9], v114 offset:1024
	ds_read_b128 v[10:13], v114 offset:2048
	ds_read_b128 v[14:17], v114 offset:3072
	ds_read_b128 v[18:21], v115
	ds_read_b128 v[22:25], v115 offset:1024
	ds_read_b128 v[26:29], v115 offset:2048
	ds_read_b128 v[30:33], v115 offset:3072
	s_add_u32 s68, s26, 0xc000
	s_addc_u32 s69, s27, 0
	s_add_i32 s65, s20, 0xc000
	s_mov_b32 m0, s65
	s_add_i32 s66, s20, 0xe000
	ds_read_b128 v[34:37], v237
	ds_read_b128 v[38:41], v237 offset:1024
	ds_read_b128 v[42:45], v237 offset:2048
	ds_read_b128 v[46:49], v237 offset:3072
	ds_read_b128 v[50:53], v237 offset:4096
	ds_read_b128 v[54:57], v237 offset:5120
	ds_read_b128 v[58:61], v237 offset:6144
	ds_read_b128 v[62:65], v237 offset:7168
	s_nop 0
	global_load_lds_dwordx4 v235, s[68:69]
	s_mov_b32 m0, s66
	s_nop 0
	global_load_lds_dwordx4 v226, s[68:69]
	s_waitcnt vmcnt(8)
	s_waitcnt lgkmcnt(0)
	s_setprio 1
	s_barrier
	s_waitcnt lgkmcnt(0)
	v_mfma_f32_16x16x32_bf16 v[90:93], v[2:5], v[58:61], 0
	v_mfma_f32_16x16x32_bf16 v[66:69], v[2:5], v[34:37], 0
	v_mfma_f32_16x16x32_bf16 v[70:73], v[10:13], v[34:37], 0
	v_mfma_f32_16x16x32_bf16 v[74:77], v[2:5], v[42:45], 0
	v_mfma_f32_16x16x32_bf16 v[78:81], v[10:13], v[42:45], 0
	v_mfma_f32_16x16x32_bf16 v[82:85], v[2:5], v[50:53], 0
	v_mfma_f32_16x16x32_bf16 v[86:89], v[10:13], v[50:53], 0
	v_mfma_f32_16x16x32_bf16 v[98:101], v[6:9], v[62:65], v[90:93]
	v_mfma_f32_16x16x32_bf16 v[90:93], v[10:13], v[58:61], 0
	v_mfma_f32_16x16x32_bf16 v[66:69], v[6:9], v[38:41], v[66:69]
	v_mfma_f32_16x16x32_bf16 v[70:73], v[14:17], v[38:41], v[70:73]
	v_mfma_f32_16x16x32_bf16 v[74:77], v[6:9], v[46:49], v[74:77]
	v_mfma_f32_16x16x32_bf16 v[78:81], v[14:17], v[46:49], v[78:81]
	v_mfma_f32_16x16x32_bf16 v[82:85], v[6:9], v[54:57], v[82:85]
	v_mfma_f32_16x16x32_bf16 v[86:89], v[14:17], v[54:57], v[86:89]
	v_mfma_f32_16x16x32_bf16 v[102:105], v[14:17], v[62:65], v[90:93]
	s_setprio 0
	s_setprio 1
	v_mfma_f32_16x16x32_bf16 v[90:93], v[18:21], v[34:37], 0
	v_mfma_f32_16x16x32_bf16 v[34:37], v[26:29], v[34:37], 0
	v_mfma_f32_16x16x32_bf16 v[118:121], v[22:25], v[38:41], v[90:93]
	v_mfma_f32_16x16x32_bf16 v[34:37], v[30:33], v[38:41], v[34:37]
	v_mfma_f32_16x16x32_bf16 v[38:41], v[18:21], v[42:45], 0
	v_mfma_f32_16x16x32_bf16 v[42:45], v[26:29], v[42:45], 0
	v_mfma_f32_16x16x32_bf16 v[38:41], v[22:25], v[46:49], v[38:41]
	v_mfma_f32_16x16x32_bf16 v[42:45], v[30:33], v[46:49], v[42:45]
	v_mfma_f32_16x16x32_bf16 v[46:49], v[18:21], v[50:53], 0
	v_mfma_f32_16x16x32_bf16 v[50:53], v[26:29], v[50:53], 0
	v_mfma_f32_16x16x32_bf16 v[46:49], v[22:25], v[54:57], v[46:49]
	v_mfma_f32_16x16x32_bf16 v[50:53], v[30:33], v[54:57], v[50:53]
	v_mfma_f32_16x16x32_bf16 v[54:57], v[18:21], v[58:61], 0
	v_mfma_f32_16x16x32_bf16 v[58:61], v[26:29], v[58:61], 0
	v_mfma_f32_16x16x32_bf16 v[54:57], v[22:25], v[62:65], v[54:57]
	v_mfma_f32_16x16x32_bf16 v[58:61], v[30:33], v[62:65], v[58:61]
	s_barrier
	s_setprio 0
	s_add_i32 s67, s67, s18
	s_add_i32 s68, s67, 0x2000
	s_mov_b32 m0, s67
	s_add_u32 s72, s34, 0x4000
	ds_read_b128 v[62:65], v237 offset:16384
	ds_read_b128 v[90:93], v237 offset:17408
	ds_read_b128 v[94:97], v237 offset:18432
	ds_read_b128 v[106:109], v237 offset:19456
	ds_read_b128 v[110:113], v237 offset:20480
	ds_read_b128 v[122:125], v237 offset:21504
	ds_read_b128 v[126:129], v237 offset:22528
	ds_read_b128 v[130:133], v237 offset:23552
	s_addc_u32 s73, s35, 0
	global_load_lds_dwordx4 v227, s[34:35]
	s_mov_b32 m0, s68
	s_add_i32 s69, s70, s18
	s_add_i32 s70, s69, 0x2000
	global_load_lds_dwordx4 v0, s[34:35]
	s_mov_b32 m0, s69
	s_nop 0
	global_load_lds_dwordx4 v227, s[72:73]
	s_mov_b32 m0, s70
	s_nop 0
	global_load_lds_dwordx4 v0, s[72:73]
	s_mov_b32 m0, s20
	s_nop 0
	global_load_lds_dwordx4 v235, s[52:53]
	s_mov_b32 m0, s25
	s_nop 0
	global_load_lds_dwordx4 v226, s[52:53]
	s_waitcnt vmcnt(8)
	s_waitcnt lgkmcnt(0)
	s_setprio 1
	s_barrier
	s_waitcnt lgkmcnt(0)
	v_mfma_f32_16x16x32_bf16 v[134:137], v[2:5], v[62:65], 0
	v_mfma_f32_16x16x32_bf16 v[142:145], v[2:5], v[94:97], 0
	v_mfma_f32_16x16x32_bf16 v[150:153], v[2:5], v[110:113], 0
	v_mfma_f32_16x16x32_bf16 v[2:5], v[2:5], v[126:129], 0
	v_mfma_f32_16x16x32_bf16 v[134:137], v[6:9], v[90:93], v[134:137]
	v_mfma_f32_16x16x32_bf16 v[142:145], v[6:9], v[106:109], v[142:145]
	v_mfma_f32_16x16x32_bf16 v[150:153], v[6:9], v[122:125], v[150:153]
	v_mfma_f32_16x16x32_bf16 v[2:5], v[6:9], v[130:133], v[2:5]
	v_mfma_f32_16x16x32_bf16 v[6:9], v[10:13], v[126:129], 0
	v_mfma_f32_16x16x32_bf16 v[138:141], v[10:13], v[62:65], 0
	v_mfma_f32_16x16x32_bf16 v[146:149], v[10:13], v[94:97], 0
	v_mfma_f32_16x16x32_bf16 v[154:157], v[10:13], v[110:113], 0
	v_mfma_f32_16x16x32_bf16 v[6:9], v[14:17], v[130:133], v[6:9]
	v_mfma_f32_16x16x32_bf16 v[138:141], v[14:17], v[90:93], v[138:141]
	v_mfma_f32_16x16x32_bf16 v[146:149], v[14:17], v[106:109], v[146:149]
	v_mfma_f32_16x16x32_bf16 v[154:157], v[14:17], v[122:125], v[154:157]
	s_setprio 0
	s_setprio 1
	v_mfma_f32_16x16x32_bf16 v[10:13], v[18:21], v[62:65], 0
	v_mfma_f32_16x16x32_bf16 v[158:161], v[22:25], v[90:93], v[10:13]
	v_mfma_f32_16x16x32_bf16 v[10:13], v[26:29], v[62:65], 0
	v_mfma_f32_16x16x32_bf16 v[162:165], v[30:33], v[90:93], v[10:13]
	v_mfma_f32_16x16x32_bf16 v[10:13], v[18:21], v[94:97], 0
	v_mfma_f32_16x16x32_bf16 v[174:177], v[22:25], v[106:109], v[10:13]
	v_mfma_f32_16x16x32_bf16 v[10:13], v[26:29], v[94:97], 0
	v_mfma_f32_16x16x32_bf16 v[178:181], v[30:33], v[106:109], v[10:13]
	v_mfma_f32_16x16x32_bf16 v[10:13], v[18:21], v[110:113], 0
	v_mfma_f32_16x16x32_bf16 v[182:185], v[22:25], v[122:125], v[10:13]
	v_mfma_f32_16x16x32_bf16 v[10:13], v[26:29], v[110:113], 0
	v_mfma_f32_16x16x32_bf16 v[122:125], v[30:33], v[122:125], v[10:13]
	v_mfma_f32_16x16x32_bf16 v[10:13], v[18:21], v[126:129], 0
	v_mfma_f32_16x16x32_bf16 v[186:189], v[22:25], v[130:133], v[10:13]
	v_mfma_f32_16x16x32_bf16 v[10:13], v[26:29], v[126:129], 0
	v_mfma_f32_16x16x32_bf16 v[130:133], v[30:33], v[130:133], v[10:13]
	s_barrier
	s_setprio 0
	s_add_i32 s71, 0, 0x18000
	s_add_i32 s74, 0, 0x1c000
	v_add_u32_e32 v116, s71, v236
	v_add_u32_e32 v117, s74, v236
	s_nop 0
	ds_read_b128 v[10:13], v116
	ds_read_b128 v[14:17], v116 offset:1024
	ds_read_b128 v[18:21], v116 offset:2048
	ds_read_b128 v[22:25], v116 offset:3072
	ds_read_b128 v[194:197], v117
	ds_read_b128 v[198:201], v117 offset:1024
	ds_read_b128 v[202:205], v117 offset:2048
	ds_read_b128 v[206:209], v117 offset:3072
	s_add_u32 s52, s52, 0x4000
	s_addc_u32 s53, s53, 0
	s_mov_b32 m0, s54
	ds_read_b128 v[26:29], v237 offset:32768
	ds_read_b128 v[30:33], v237 offset:33792
	ds_read_b128 v[62:65], v237 offset:34816
	ds_read_b128 v[210:213], v237 offset:35840
	ds_read_b128 v[214:217], v237 offset:36864
	ds_read_b128 v[218:221], v237 offset:37888
	ds_read_b128 v[222:225], v237 offset:38912
	ds_read_b128 v[238:241], v237 offset:39936
	s_nop 0
	global_load_lds_dwordx4 v235, s[52:53]
	s_mov_b32 m0, s55
	s_nop 0
	global_load_lds_dwordx4 v226, s[52:53]
	s_waitcnt vmcnt(8)
	s_waitcnt lgkmcnt(0)
	s_setprio 1
	s_barrier
	s_waitcnt lgkmcnt(0)
	v_mfma_f32_16x16x32_bf16 v[66:69], v[10:13], v[26:29], v[66:69]
	v_mfma_f32_16x16x32_bf16 v[166:169], v[14:17], v[30:33], v[66:69]
	v_mfma_f32_16x16x32_bf16 v[66:69], v[18:21], v[26:29], v[70:73]
	v_mfma_f32_16x16x32_bf16 v[170:173], v[22:25], v[30:33], v[66:69]
	v_mfma_f32_16x16x32_bf16 v[66:69], v[10:13], v[62:65], v[74:77]
	v_mfma_f32_16x16x32_bf16 v[110:113], v[14:17], v[210:213], v[66:69]
	v_mfma_f32_16x16x32_bf16 v[66:69], v[18:21], v[62:65], v[78:81]
	v_mfma_f32_16x16x32_bf16 v[106:109], v[22:25], v[210:213], v[66:69]
	v_mfma_f32_16x16x32_bf16 v[66:69], v[10:13], v[214:217], v[82:85]
	v_mfma_f32_16x16x32_bf16 v[94:97], v[14:17], v[218:221], v[66:69]
	v_mfma_f32_16x16x32_bf16 v[66:69], v[18:21], v[214:217], v[86:89]
	v_mfma_f32_16x16x32_bf16 v[90:93], v[22:25], v[218:221], v[66:69]
	v_mfma_f32_16x16x32_bf16 v[66:69], v[10:13], v[222:225], v[98:101]
	v_mfma_f32_16x16x32_bf16 v[78:81], v[14:17], v[238:241], v[66:69]
	v_mfma_f32_16x16x32_bf16 v[66:69], v[18:21], v[222:225], v[102:105]
	v_mfma_f32_16x16x32_bf16 v[70:73], v[22:25], v[238:241], v[66:69]
	s_setprio 0
	s_setprio 1
	v_mfma_f32_16x16x32_bf16 v[66:69], v[194:197], v[26:29], v[118:121]
	v_mfma_f32_16x16x32_bf16 v[26:29], v[202:205], v[26:29], v[34:37]
	v_mfma_f32_16x16x32_bf16 v[118:121], v[206:209], v[30:33], v[26:29]
	v_mfma_f32_16x16x32_bf16 v[26:29], v[194:197], v[62:65], v[38:41]
	v_mfma_f32_16x16x32_bf16 v[102:105], v[198:201], v[210:213], v[26:29]
	v_mfma_f32_16x16x32_bf16 v[26:29], v[202:205], v[62:65], v[42:45]
	v_mfma_f32_16x16x32_bf16 v[98:101], v[206:209], v[210:213], v[26:29]
	v_mfma_f32_16x16x32_bf16 v[26:29], v[194:197], v[214:217], v[46:49]
	v_mfma_f32_16x16x32_bf16 v[86:89], v[198:201], v[218:221], v[26:29]
	v_mfma_f32_16x16x32_bf16 v[26:29], v[202:205], v[214:217], v[50:53]
	v_mfma_f32_16x16x32_bf16 v[82:85], v[206:209], v[218:221], v[26:29]
	v_mfma_f32_16x16x32_bf16 v[26:29], v[194:197], v[222:225], v[54:57]
	v_mfma_f32_16x16x32_bf16 v[62:65], v[198:201], v[238:241], v[26:29]
	v_mfma_f32_16x16x32_bf16 v[26:29], v[202:205], v[222:225], v[58:61]
	v_mfma_f32_16x16x32_bf16 v[126:129], v[198:201], v[30:33], v[66:69]
	v_mfma_f32_16x16x32_bf16 v[54:57], v[206:209], v[238:241], v[26:29]
	s_barrier
	s_setprio 0
	s_add_u32 s72, s34, 0x8000
	s_addc_u32 s73, s35, 0
	s_add_i32 s52, s71, s18
	s_add_i32 s53, s52, 0x2000
	s_mov_b32 m0, s52
	s_add_u32 s34, s34, 0xc000
	ds_read_b128 v[34:37], v237 offset:49152
	ds_read_b128 v[38:41], v237 offset:50176
	ds_read_b128 v[210:213], v237 offset:51200
	ds_read_b128 v[214:217], v237 offset:52224
	ds_read_b128 v[218:221], v237 offset:53248
	ds_read_b128 v[222:225], v237 offset:54272
	ds_read_b128 v[238:241], v237 offset:55296
	ds_read_b128 v[242:245], v237 offset:56320
	s_addc_u32 s35, s35, 0
	global_load_lds_dwordx4 v227, s[72:73]
	s_mov_b32 m0, s53
	s_add_i32 s71, s74, s18
	s_nop 0
	global_load_lds_dwordx4 v0, s[72:73]
	s_mov_b32 m0, s71
	s_add_i32 s72, s71, 0x2000
	s_nop 0
	global_load_lds_dwordx4 v227, s[34:35]
	s_mov_b32 m0, s72
	s_nop 0
	global_load_lds_dwordx4 v0, s[34:35]
	s_mov_b32 m0, s58
	s_nop 0
	global_load_lds_dwordx4 v235, s[30:31]
	s_mov_b32 m0, s59
	s_nop 0
	global_load_lds_dwordx4 v226, s[30:31]
	s_waitcnt vmcnt(8)
	s_waitcnt lgkmcnt(0)
	s_setprio 1
	s_barrier
	s_waitcnt lgkmcnt(0)
	v_mfma_f32_16x16x32_bf16 v[26:29], v[10:13], v[34:37], v[134:137]
	v_mfma_f32_16x16x32_bf16 v[74:77], v[14:17], v[38:41], v[26:29]
	v_mfma_f32_16x16x32_bf16 v[26:29], v[18:21], v[34:37], v[138:141]
	v_mfma_f32_16x16x32_bf16 v[66:69], v[22:25], v[38:41], v[26:29]
	v_mfma_f32_16x16x32_bf16 v[26:29], v[10:13], v[210:213], v[142:145]
	v_mfma_f32_16x16x32_bf16 v[46:49], v[14:17], v[214:217], v[26:29]
	v_mfma_f32_16x16x32_bf16 v[26:29], v[18:21], v[210:213], v[146:149]
	v_mfma_f32_16x16x32_bf16 v[42:45], v[22:25], v[214:217], v[26:29]
	v_mfma_f32_16x16x32_bf16 v[26:29], v[10:13], v[218:221], v[150:153]
	v_mfma_f32_16x16x32_bf16 v[2:5], v[10:13], v[238:241], v[2:5]
	v_mfma_f32_16x16x32_bf16 v[30:33], v[14:17], v[222:225], v[26:29]
	v_mfma_f32_16x16x32_bf16 v[26:29], v[18:21], v[218:221], v[154:157]
	v_mfma_f32_16x16x32_bf16 v[14:17], v[14:17], v[242:245], v[2:5]
	v_mfma_f32_16x16x32_bf16 v[2:5], v[18:21], v[238:241], v[6:9]
	v_mfma_f32_16x16x32_bf16 v[26:29], v[22:25], v[222:225], v[26:29]
	v_mfma_f32_16x16x32_bf16 v[10:13], v[22:25], v[242:245], v[2:5]
	s_setprio 0
	s_setprio 1
	v_mfma_f32_16x16x32_bf16 v[2:5], v[194:197], v[34:37], v[158:161]
	v_mfma_f32_16x16x32_bf16 v[58:61], v[198:201], v[38:41], v[2:5]
	v_mfma_f32_16x16x32_bf16 v[2:5], v[202:205], v[34:37], v[162:165]
	v_mfma_f32_16x16x32_bf16 v[50:53], v[206:209], v[38:41], v[2:5]
	v_mfma_f32_16x16x32_bf16 v[2:5], v[194:197], v[210:213], v[174:177]
	v_mfma_f32_16x16x32_bf16 v[38:41], v[198:201], v[214:217], v[2:5]
	v_mfma_f32_16x16x32_bf16 v[2:5], v[202:205], v[210:213], v[178:181]
	v_mfma_f32_16x16x32_bf16 v[34:37], v[206:209], v[214:217], v[2:5]
	v_mfma_f32_16x16x32_bf16 v[2:5], v[194:197], v[218:221], v[182:185]
	v_mfma_f32_16x16x32_bf16 v[22:25], v[198:201], v[222:225], v[2:5]
	v_mfma_f32_16x16x32_bf16 v[2:5], v[202:205], v[218:221], v[122:125]
	v_mfma_f32_16x16x32_bf16 v[18:21], v[206:209], v[222:225], v[2:5]
	v_mfma_f32_16x16x32_bf16 v[2:5], v[194:197], v[238:241], v[186:189]
	v_mfma_f32_16x16x32_bf16 v[6:9], v[198:201], v[242:245], v[2:5]
	v_mfma_f32_16x16x32_bf16 v[2:5], v[202:205], v[238:241], v[130:133]
	v_mfma_f32_16x16x32_bf16 v[2:5], v[206:209], v[242:245], v[2:5]
	s_barrier
	s_setprio 0
	s_andn2_b64 vcc, exec, s[48:49]
	s_cbranch_vccnz .LBB0_1228
	s_add_u32 s73, s28, 0x20000
	s_addc_u32 s74, s29, 0
	s_add_u32 s26, s26, 0x1c000
	s_addc_u32 s27, s27, 0
	s_mov_b32 s75, 4
.LBB0_1227:
	ds_read_b128 v[122:125], v114
	ds_read_b128 v[130:133], v114 offset:1024
	ds_read_b128 v[134:137], v114 offset:2048
	ds_read_b128 v[138:141], v114 offset:3072
	ds_read_b128 v[142:145], v115
	ds_read_b128 v[146:149], v115 offset:1024
	ds_read_b128 v[150:153], v115 offset:2048
	ds_read_b128 v[154:157], v115 offset:3072
	s_add_u32 s28, s26, 0x4000
	s_addc_u32 s29, s27, 0
	s_cmp_eq_u32 s56, s75
	s_cselect_b32 s34, s38, s28
	s_cselect_b32 s35, s39, s29
	s_cselect_b32 s30, s40, s73
	s_cselect_b32 s31, s41, s74
	s_add_u32 s28, s34, 0x8000
	s_addc_u32 s29, s35, 0
	s_mov_b32 m0, s65
	ds_read_b128 v[158:161], v237
	ds_read_b128 v[162:165], v237 offset:1024
	ds_read_b128 v[174:177], v237 offset:2048
	ds_read_b128 v[178:181], v237 offset:3072
	ds_read_b128 v[182:185], v237 offset:4096
	ds_read_b128 v[186:189], v237 offset:5120
	ds_read_b128 v[194:197], v237 offset:6144
	ds_read_b128 v[198:201], v237 offset:7168
	s_nop 0
	global_load_lds_dwordx4 v235, s[26:27]
	s_mov_b32 m0, s66
	s_nop 0
	global_load_lds_dwordx4 v226, s[26:27]
	s_waitcnt vmcnt(8)
	s_waitcnt lgkmcnt(0)
	s_setprio 1
	s_barrier
	s_waitcnt lgkmcnt(0)
	v_mfma_f32_16x16x32_bf16 v[166:169], v[122:125], v[158:161], v[166:169]
	v_mfma_f32_16x16x32_bf16 v[170:173], v[134:137], v[158:161], v[170:173]
	v_mfma_f32_16x16x32_bf16 v[110:113], v[122:125], v[174:177], v[110:113]
	v_mfma_f32_16x16x32_bf16 v[106:109], v[134:137], v[174:177], v[106:109]
	v_mfma_f32_16x16x32_bf16 v[94:97], v[122:125], v[182:185], v[94:97]
	v_mfma_f32_16x16x32_bf16 v[90:93], v[134:137], v[182:185], v[90:93]
	v_mfma_f32_16x16x32_bf16 v[78:81], v[122:125], v[194:197], v[78:81]
	v_mfma_f32_16x16x32_bf16 v[70:73], v[134:137], v[194:197], v[70:73]
	v_mfma_f32_16x16x32_bf16 v[166:169], v[130:133], v[162:165], v[166:169]
	v_mfma_f32_16x16x32_bf16 v[170:173], v[138:141], v[162:165], v[170:173]
	v_mfma_f32_16x16x32_bf16 v[110:113], v[130:133], v[178:181], v[110:113]
	v_mfma_f32_16x16x32_bf16 v[106:109], v[138:141], v[178:181], v[106:109]
	v_mfma_f32_16x16x32_bf16 v[94:97], v[130:133], v[186:189], v[94:97]
	v_mfma_f32_16x16x32_bf16 v[90:93], v[138:141], v[186:189], v[90:93]
	v_mfma_f32_16x16x32_bf16 v[78:81], v[130:133], v[198:201], v[78:81]
	v_mfma_f32_16x16x32_bf16 v[70:73], v[138:141], v[198:201], v[70:73]
	s_setprio 0
	s_setprio 1
	v_mfma_f32_16x16x32_bf16 v[126:129], v[142:145], v[158:161], v[126:129]
	v_mfma_f32_16x16x32_bf16 v[118:121], v[150:153], v[158:161], v[118:121]
	v_mfma_f32_16x16x32_bf16 v[102:105], v[142:145], v[174:177], v[102:105]
	v_mfma_f32_16x16x32_bf16 v[98:101], v[150:153], v[174:177], v[98:101]
	v_mfma_f32_16x16x32_bf16 v[86:89], v[142:145], v[182:185], v[86:89]
	v_mfma_f32_16x16x32_bf16 v[82:85], v[150:153], v[182:185], v[82:85]
	v_mfma_f32_16x16x32_bf16 v[62:65], v[142:145], v[194:197], v[62:65]
	v_mfma_f32_16x16x32_bf16 v[54:57], v[150:153], v[194:197], v[54:57]
	v_mfma_f32_16x16x32_bf16 v[126:129], v[146:149], v[162:165], v[126:129]
	v_mfma_f32_16x16x32_bf16 v[118:121], v[154:157], v[162:165], v[118:121]
	v_mfma_f32_16x16x32_bf16 v[102:105], v[146:149], v[178:181], v[102:105]
	v_mfma_f32_16x16x32_bf16 v[98:101], v[154:157], v[178:181], v[98:101]
	v_mfma_f32_16x16x32_bf16 v[86:89], v[146:149], v[186:189], v[86:89]
	v_mfma_f32_16x16x32_bf16 v[82:85], v[154:157], v[186:189], v[82:85]
	v_mfma_f32_16x16x32_bf16 v[62:65], v[146:149], v[198:201], v[62:65]
	v_mfma_f32_16x16x32_bf16 v[54:57], v[154:157], v[198:201], v[54:57]
	s_barrier
	s_setprio 0
	s_mov_b32 m0, s67
	ds_read_b128 v[158:161], v237 offset:16384
	ds_read_b128 v[162:165], v237 offset:17408
	ds_read_b128 v[174:177], v237 offset:18432
	ds_read_b128 v[178:181], v237 offset:19456
	ds_read_b128 v[182:185], v237 offset:20480
	ds_read_b128 v[186:189], v237 offset:21504
	ds_read_b128 v[194:197], v237 offset:22528
	ds_read_b128 v[198:201], v237 offset:23552
	s_add_u32 s76, s30, 0x4000
	global_load_lds_dwordx4 v227, s[30:31]
	s_mov_b32 m0, s68
	s_addc_u32 s77, s31, 0
	global_load_lds_dwordx4 v0, s[30:31]
	s_mov_b32 m0, s69
	s_nop 0
	global_load_lds_dwordx4 v227, s[76:77]
	s_mov_b32 m0, s70
	s_nop 0
	global_load_lds_dwordx4 v0, s[76:77]
	s_mov_b32 m0, s20
	s_nop 0
	global_load_lds_dwordx4 v235, s[34:35]
	s_mov_b32 m0, s25
	s_nop 0
	global_load_lds_dwordx4 v226, s[34:35]
	s_waitcnt vmcnt(8)
	s_waitcnt lgkmcnt(0)
	s_setprio 1
	s_barrier
	s_waitcnt lgkmcnt(0)
	v_mfma_f32_16x16x32_bf16 v[74:77], v[122:125], v[158:161], v[74:77]
	v_mfma_f32_16x16x32_bf16 v[66:69], v[134:137], v[158:161], v[66:69]
	v_mfma_f32_16x16x32_bf16 v[46:49], v[122:125], v[174:177], v[46:49]
	v_mfma_f32_16x16x32_bf16 v[42:45], v[134:137], v[174:177], v[42:45]
	v_mfma_f32_16x16x32_bf16 v[30:33], v[122:125], v[182:185], v[30:33]
	v_mfma_f32_16x16x32_bf16 v[26:29], v[134:137], v[182:185], v[26:29]
	v_mfma_f32_16x16x32_bf16 v[14:17], v[122:125], v[194:197], v[14:17]
	v_mfma_f32_16x16x32_bf16 v[10:13], v[134:137], v[194:197], v[10:13]
	v_mfma_f32_16x16x32_bf16 v[74:77], v[130:133], v[162:165], v[74:77]
	v_mfma_f32_16x16x32_bf16 v[66:69], v[138:141], v[162:165], v[66:69]
	v_mfma_f32_16x16x32_bf16 v[46:49], v[130:133], v[178:181], v[46:49]
	v_mfma_f32_16x16x32_bf16 v[42:45], v[138:141], v[178:181], v[42:45]
	v_mfma_f32_16x16x32_bf16 v[30:33], v[130:133], v[186:189], v[30:33]
	v_mfma_f32_16x16x32_bf16 v[26:29], v[138:141], v[186:189], v[26:29]
	v_mfma_f32_16x16x32_bf16 v[14:17], v[130:133], v[198:201], v[14:17]
	v_mfma_f32_16x16x32_bf16 v[10:13], v[138:141], v[198:201], v[10:13]
	s_setprio 0
	s_setprio 1
	v_mfma_f32_16x16x32_bf16 v[58:61], v[142:145], v[158:161], v[58:61]
	v_mfma_f32_16x16x32_bf16 v[50:53], v[150:153], v[158:161], v[50:53]
	v_mfma_f32_16x16x32_bf16 v[38:41], v[142:145], v[174:177], v[38:41]
	v_mfma_f32_16x16x32_bf16 v[34:37], v[150:153], v[174:177], v[34:37]
	v_mfma_f32_16x16x32_bf16 v[22:25], v[142:145], v[182:185], v[22:25]
	v_mfma_f32_16x16x32_bf16 v[18:21], v[150:153], v[182:185], v[18:21]
	v_mfma_f32_16x16x32_bf16 v[6:9], v[142:145], v[194:197], v[6:9]
	v_mfma_f32_16x16x32_bf16 v[2:5], v[150:153], v[194:197], v[2:5]
	v_mfma_f32_16x16x32_bf16 v[58:61], v[146:149], v[162:165], v[58:61]
	v_mfma_f32_16x16x32_bf16 v[50:53], v[154:157], v[162:165], v[50:53]
	v_mfma_f32_16x16x32_bf16 v[38:41], v[146:149], v[178:181], v[38:41]
	v_mfma_f32_16x16x32_bf16 v[34:37], v[154:157], v[178:181], v[34:37]
	v_mfma_f32_16x16x32_bf16 v[22:25], v[146:149], v[186:189], v[22:25]
	v_mfma_f32_16x16x32_bf16 v[18:21], v[154:157], v[186:189], v[18:21]
	v_mfma_f32_16x16x32_bf16 v[6:9], v[146:149], v[198:201], v[6:9]
	v_mfma_f32_16x16x32_bf16 v[2:5], v[154:157], v[198:201], v[2:5]
	s_barrier
	s_setprio 0
	ds_read_b128 v[122:125], v116
	ds_read_b128 v[130:133], v116 offset:1024
	ds_read_b128 v[134:137], v116 offset:2048
	ds_read_b128 v[138:141], v116 offset:3072
	ds_read_b128 v[142:145], v117
	ds_read_b128 v[146:149], v117 offset:1024
	ds_read_b128 v[150:153], v117 offset:2048
	ds_read_b128 v[154:157], v117 offset:3072
	s_add_u32 s34, s34, 0x4000
	s_addc_u32 s35, s35, 0
	s_mov_b32 m0, s54
	ds_read_b128 v[158:161], v237 offset:32768
	ds_read_b128 v[162:165], v237 offset:33792
	ds_read_b128 v[174:177], v237 offset:34816
	ds_read_b128 v[178:181], v237 offset:35840
	ds_read_b128 v[182:185], v237 offset:36864
	ds_read_b128 v[186:189], v237 offset:37888
	ds_read_b128 v[194:197], v237 offset:38912
	ds_read_b128 v[198:201], v237 offset:39936
	s_nop 0
	global_load_lds_dwordx4 v235, s[34:35]
	s_mov_b32 m0, s55
	s_nop 0
	global_load_lds_dwordx4 v226, s[34:35]
	s_waitcnt vmcnt(8)
	s_waitcnt lgkmcnt(0)
	s_setprio 1
	s_barrier
	s_waitcnt lgkmcnt(0)
	v_mfma_f32_16x16x32_bf16 v[166:169], v[122:125], v[158:161], v[166:169]
	v_mfma_f32_16x16x32_bf16 v[170:173], v[134:137], v[158:161], v[170:173]
	v_mfma_f32_16x16x32_bf16 v[110:113], v[122:125], v[174:177], v[110:113]
	v_mfma_f32_16x16x32_bf16 v[106:109], v[134:137], v[174:177], v[106:109]
	v_mfma_f32_16x16x32_bf16 v[94:97], v[122:125], v[182:185], v[94:97]
	v_mfma_f32_16x16x32_bf16 v[90:93], v[134:137], v[182:185], v[90:93]
	v_mfma_f32_16x16x32_bf16 v[78:81], v[122:125], v[194:197], v[78:81]
	v_mfma_f32_16x16x32_bf16 v[70:73], v[134:137], v[194:197], v[70:73]
	v_mfma_f32_16x16x32_bf16 v[166:169], v[130:133], v[162:165], v[166:169]
	v_mfma_f32_16x16x32_bf16 v[170:173], v[138:141], v[162:165], v[170:173]
	v_mfma_f32_16x16x32_bf16 v[110:113], v[130:133], v[178:181], v[110:113]
	v_mfma_f32_16x16x32_bf16 v[106:109], v[138:141], v[178:181], v[106:109]
	v_mfma_f32_16x16x32_bf16 v[94:97], v[130:133], v[186:189], v[94:97]
	v_mfma_f32_16x16x32_bf16 v[90:93], v[138:141], v[186:189], v[90:93]
	v_mfma_f32_16x16x32_bf16 v[78:81], v[130:133], v[198:201], v[78:81]
	v_mfma_f32_16x16x32_bf16 v[70:73], v[138:141], v[198:201], v[70:73]
	s_setprio 0
	s_setprio 1
	v_mfma_f32_16x16x32_bf16 v[126:129], v[142:145], v[158:161], v[126:129]
	v_mfma_f32_16x16x32_bf16 v[118:121], v[150:153], v[158:161], v[118:121]
	v_mfma_f32_16x16x32_bf16 v[102:105], v[142:145], v[174:177], v[102:105]
	v_mfma_f32_16x16x32_bf16 v[98:101], v[150:153], v[174:177], v[98:101]
	v_mfma_f32_16x16x32_bf16 v[86:89], v[142:145], v[182:185], v[86:89]
	v_mfma_f32_16x16x32_bf16 v[82:85], v[150:153], v[182:185], v[82:85]
	v_mfma_f32_16x16x32_bf16 v[62:65], v[142:145], v[194:197], v[62:65]
	v_mfma_f32_16x16x32_bf16 v[54:57], v[150:153], v[194:197], v[54:57]
	v_mfma_f32_16x16x32_bf16 v[126:129], v[146:149], v[162:165], v[126:129]
	v_mfma_f32_16x16x32_bf16 v[118:121], v[154:157], v[162:165], v[118:121]
	v_mfma_f32_16x16x32_bf16 v[102:105], v[146:149], v[178:181], v[102:105]
	v_mfma_f32_16x16x32_bf16 v[98:101], v[154:157], v[178:181], v[98:101]
	v_mfma_f32_16x16x32_bf16 v[86:89], v[146:149], v[186:189], v[86:89]
	v_mfma_f32_16x16x32_bf16 v[82:85], v[154:157], v[186:189], v[82:85]
	v_mfma_f32_16x16x32_bf16 v[62:65], v[146:149], v[198:201], v[62:65]
	v_mfma_f32_16x16x32_bf16 v[54:57], v[154:157], v[198:201], v[54:57]
	s_barrier
	s_setprio 0
	s_add_u32 s34, s30, 0x8000
	s_mov_b32 m0, s52
	s_addc_u32 s35, s31, 0
	ds_read_b128 v[158:161], v237 offset:49152
	ds_read_b128 v[162:165], v237 offset:50176
	ds_read_b128 v[174:177], v237 offset:51200
	ds_read_b128 v[178:181], v237 offset:52224
	ds_read_b128 v[182:185], v237 offset:53248
	ds_read_b128 v[186:189], v237 offset:54272
	ds_read_b128 v[194:197], v237 offset:55296
	ds_read_b128 v[198:201], v237 offset:56320
	s_add_u32 s30, s30, 0xc000
	global_load_lds_dwordx4 v227, s[34:35]
	s_mov_b32 m0, s53
	s_addc_u32 s31, s31, 0
	global_load_lds_dwordx4 v0, s[34:35]
	s_mov_b32 m0, s71
	s_nop 0
	global_load_lds_dwordx4 v227, s[30:31]
	s_mov_b32 m0, s72
	s_nop 0
	global_load_lds_dwordx4 v0, s[30:31]
	s_mov_b32 m0, s58
	s_nop 0
	global_load_lds_dwordx4 v235, s[28:29]
	s_mov_b32 m0, s59
	s_nop 0
	global_load_lds_dwordx4 v226, s[28:29]
	s_waitcnt vmcnt(8)
	s_waitcnt lgkmcnt(0)
	s_setprio 1
	s_barrier
	s_waitcnt lgkmcnt(0)
	v_mfma_f32_16x16x32_bf16 v[74:77], v[122:125], v[158:161], v[74:77]
	v_mfma_f32_16x16x32_bf16 v[66:69], v[134:137], v[158:161], v[66:69]
	v_mfma_f32_16x16x32_bf16 v[46:49], v[122:125], v[174:177], v[46:49]
	v_mfma_f32_16x16x32_bf16 v[42:45], v[134:137], v[174:177], v[42:45]
	v_mfma_f32_16x16x32_bf16 v[30:33], v[122:125], v[182:185], v[30:33]
	v_mfma_f32_16x16x32_bf16 v[26:29], v[134:137], v[182:185], v[26:29]
	v_mfma_f32_16x16x32_bf16 v[14:17], v[122:125], v[194:197], v[14:17]
	v_mfma_f32_16x16x32_bf16 v[10:13], v[134:137], v[194:197], v[10:13]
	v_mfma_f32_16x16x32_bf16 v[74:77], v[130:133], v[162:165], v[74:77]
	v_mfma_f32_16x16x32_bf16 v[66:69], v[138:141], v[162:165], v[66:69]
	v_mfma_f32_16x16x32_bf16 v[46:49], v[130:133], v[178:181], v[46:49]
	v_mfma_f32_16x16x32_bf16 v[42:45], v[138:141], v[178:181], v[42:45]
	v_mfma_f32_16x16x32_bf16 v[30:33], v[130:133], v[186:189], v[30:33]
	v_mfma_f32_16x16x32_bf16 v[26:29], v[138:141], v[186:189], v[26:29]
	v_mfma_f32_16x16x32_bf16 v[14:17], v[130:133], v[198:201], v[14:17]
	v_mfma_f32_16x16x32_bf16 v[10:13], v[138:141], v[198:201], v[10:13]
	s_setprio 0
	s_setprio 1
	v_mfma_f32_16x16x32_bf16 v[58:61], v[142:145], v[158:161], v[58:61]
	v_mfma_f32_16x16x32_bf16 v[50:53], v[150:153], v[158:161], v[50:53]
	v_mfma_f32_16x16x32_bf16 v[38:41], v[142:145], v[174:177], v[38:41]
	v_mfma_f32_16x16x32_bf16 v[34:37], v[150:153], v[174:177], v[34:37]
	v_mfma_f32_16x16x32_bf16 v[22:25], v[142:145], v[182:185], v[22:25]
	v_mfma_f32_16x16x32_bf16 v[18:21], v[150:153], v[182:185], v[18:21]
	v_mfma_f32_16x16x32_bf16 v[6:9], v[142:145], v[194:197], v[6:9]
	v_mfma_f32_16x16x32_bf16 v[2:5], v[150:153], v[194:197], v[2:5]
	v_mfma_f32_16x16x32_bf16 v[58:61], v[146:149], v[162:165], v[58:61]
	v_mfma_f32_16x16x32_bf16 v[50:53], v[154:157], v[162:165], v[50:53]
	v_mfma_f32_16x16x32_bf16 v[38:41], v[146:149], v[178:181], v[38:41]
	v_mfma_f32_16x16x32_bf16 v[34:37], v[154:157], v[178:181], v[34:37]
	v_mfma_f32_16x16x32_bf16 v[22:25], v[146:149], v[186:189], v[22:25]
	v_mfma_f32_16x16x32_bf16 v[18:21], v[154:157], v[186:189], v[18:21]
	v_mfma_f32_16x16x32_bf16 v[6:9], v[146:149], v[198:201], v[6:9]
	v_mfma_f32_16x16x32_bf16 v[2:5], v[154:157], v[198:201], v[2:5]
	s_barrier
	s_setprio 0
	s_add_i32 s28, s75, 2
	s_add_u32 s73, s73, 0x10000
	s_addc_u32 s74, s74, 0
	s_add_u32 s26, s26, 0x10000
	s_addc_u32 s27, s27, 0
	s_cmp_lt_i32 s75, s56
	s_mov_b32 s75, s28
	s_cbranch_scc1 .LBB0_1227
